# norm2+router phase: router-weight LDS reads use one base register + immediates (frees 40+ VGPRs); each row's gain / modulation vector loads issued up front into those registers behind counted waits in
# speedup vs baseline: 1.0241x; 1.0179x over previous
.LBB0_1690:
	s_or_b64 exec, exec, s[4:5]
	s_waitcnt lgkmcnt(0)
	s_barrier
	s_load_dword s28, s[0:1], 0xf8
	s_ashr_i32 s18, s14, 6
	s_add_u32 s20, s0, 0xf8
	s_addc_u32 s21, s1, 0
	s_waitcnt lgkmcnt(0)
	s_abs_i32 s4, s28
	v_cvt_f32_u32_e32 v1, s4
	s_add_i32 s5, s28, 0x41ff
	s_sub_i32 s6, 0xffffbe01, s28
	s_xor_b32 s7, s5, s28
	v_rcp_iflag_f32_e32 v1, v1
	s_max_i32 s5, s5, s6
	s_sub_i32 s6, 0, s4
	s_ashr_i32 s7, s7, 31
	v_mul_f32_e32 v1, 0x4f7ffffe, v1
	v_cvt_u32_f32_e32 v1, v1
	s_nop 0
	v_readfirstlane_b32 s8, v1
	s_mul_i32 s6, s6, s8
	s_mul_hi_u32 s6, s8, s6
	s_add_i32 s8, s8, s6
	s_mul_hi_u32 s6, s5, s8
	s_mul_i32 s8, s6, s4
	s_sub_i32 s5, s5, s8
	s_add_i32 s9, s6, 1
	s_sub_i32 s8, s5, s4
	s_cmp_ge_u32 s5, s4
	s_cselect_b32 s6, s9, s6
	s_cselect_b32 s5, s8, s5
	s_add_i32 s8, s6, 1
	s_cmp_ge_u32 s5, s4
	s_cselect_b32 s4, s8, s6
	s_xor_b32 s4, s4, s7
	s_sub_i32 s30, s4, s7
	s_ashr_i32 s31, s30, 1
	s_cmp_lt_i32 s18, s31
	s_mul_i32 s29, s30, s2
	s_cbranch_scc0 .LBB0_1731
	s_add_u32 s33, s40, 0x100000
	s_addc_u32 s34, s41, 0
	s_add_i32 s4, s29, s18
	s_add_u32 s14, s40, 0x21c00000
	s_addc_u32 s15, s41, 0
	s_ashr_i32 s5, s4, 31
	s_lshl_b64 s[6:7], s[4:5], 12
	s_add_u32 s8, s14, s6
	s_addc_u32 s9, s15, s7
	s_add_u32 s16, s40, 0x36600000
	s_addc_u32 s17, s41, 0
	s_add_u32 s6, s16, s6
	s_addc_u32 s7, s17, s7
	s_add_i32 s4, s4, s31
	v_and_b32_e32 v5, 63, v6
	s_ashr_i32 s5, s4, 31
	v_lshlrev_b32_e32 v2, 3, v5
	s_lshl_b64 s[4:5], s[4:5], 12
	global_load_dwordx2 v[18:19], v2, s[8:9] nt
	global_load_dwordx2 v[20:21], v2, s[8:9] offset:512 nt
	global_load_dwordx2 v[22:23], v2, s[8:9] offset:1024 nt
	global_load_dwordx2 v[24:25], v2, s[8:9] offset:1536 nt
	global_load_dwordx2 v[26:27], v2, s[6:7] nt
	global_load_dwordx2 v[28:29], v2, s[6:7] offset:512 nt
	global_load_dwordx2 v[30:31], v2, s[6:7] offset:1024 nt
	global_load_dwordx2 v[32:33], v2, s[6:7] offset:1536 nt
	global_load_dwordx2 v[34:35], v2, s[8:9] offset:2048 nt
	global_load_dwordx2 v[36:37], v2, s[8:9] offset:2560 nt
	global_load_dwordx2 v[38:39], v2, s[8:9] offset:3072 nt
	global_load_dwordx2 v[40:41], v2, s[8:9] offset:3584 nt
	global_load_dwordx2 v[42:43], v2, s[6:7] offset:2048 nt
	global_load_dwordx2 v[44:45], v2, s[6:7] offset:2560 nt
	global_load_dwordx2 v[46:47], v2, s[6:7] offset:3072 nt
	global_load_dwordx2 v[48:49], v2, s[6:7] offset:3584 nt
	s_add_u32 s6, s14, s4
	s_addc_u32 s7, s15, s5
	s_add_u32 s4, s16, s4
	s_addc_u32 s5, s17, s5
	global_load_dwordx2 v[50:51], v2, s[6:7] nt
	global_load_dwordx2 v[52:53], v2, s[6:7] offset:512 nt
	global_load_dwordx2 v[54:55], v2, s[6:7] offset:1024 nt
	global_load_dwordx2 v[56:57], v2, s[6:7] offset:1536 nt
	global_load_dwordx2 v[58:59], v2, s[4:5] nt
	global_load_dwordx2 v[60:61], v2, s[4:5] offset:512 nt
	global_load_dwordx2 v[62:63], v2, s[4:5] offset:1024 nt
	global_load_dwordx2 v[64:65], v2, s[4:5] offset:1536 nt
	global_load_dwordx2 v[66:67], v2, s[6:7] offset:2048 nt
	global_load_dwordx2 v[68:69], v2, s[6:7] offset:2560 nt
	global_load_dwordx2 v[70:71], v2, s[6:7] offset:3072 nt
	global_load_dwordx2 v[72:73], v2, s[6:7] offset:3584 nt
	global_load_dwordx2 v[74:75], v2, s[4:5] offset:2048 nt
	global_load_dwordx2 v[76:77], v2, s[4:5] offset:2560 nt
	global_load_dwordx2 v[78:79], v2, s[4:5] offset:3072 nt
	global_load_dwordx2 v[80:81], v2, s[4:5] offset:3584 nt
	v_mbcnt_lo_u32_b32 v1, -1, 0
	v_mbcnt_hi_u32_b32 v7, -1, v1
	v_and_b32_e32 v9, 64, v7
	v_add_u32_e32 v11, 64, v9
	v_xor_b32_e32 v1, 1, v7
	v_cmp_lt_i32_e32 vcc, v1, v11
	v_xor_b32_e32 v13, 2, v7
	s_load_dwordx2 s[22:23], s[0:1], 0x38
	v_cndmask_b32_e32 v1, v7, v1, vcc
	v_cmp_lt_i32_e32 vcc, v13, v11
	v_lshlrev_b32_e32 v16, 2, v5
	v_cmp_eq_u32_e64 s[4:5], 0, v5
	v_cndmask_b32_e32 v13, v7, v13, vcc
	v_lshlrev_b32_e32 v15, 2, v13
	v_xor_b32_e32 v13, 4, v7
	v_cmp_lt_i32_e32 vcc, v13, v11
	v_lshlrev_b32_e32 v82, 4, v5
	v_cmp_gt_u32_e64 s[6:7], 32, v5
	v_cndmask_b32_e32 v13, v7, v13, vcc
	v_lshlrev_b32_e32 v180, 2, v13
	v_xor_b32_e32 v13, 8, v7
	v_cmp_lt_i32_e32 vcc, v13, v11
	v_and_b32_e32 v5, 16, v6
	v_cmp_eq_u32_e64 s[8:9], 0, v5
	v_cndmask_b32_e32 v13, v7, v13, vcc
	v_lshlrev_b32_e32 v181, 2, v13
	v_xor_b32_e32 v13, 16, v7
	v_cmp_lt_i32_e32 vcc, v13, v11
	v_and_b32_e32 v5, 8, v6
	v_mov_b32_e32 v17, 0
	v_cndmask_b32_e32 v13, v7, v13, vcc
	v_lshlrev_b32_e32 v182, 2, v13
	v_xor_b32_e32 v13, 32, v7
	v_cmp_lt_i32_e32 vcc, v13, v11
	v_or_b32_e32 v12, 0x400, v16
	v_cmp_eq_u32_e64 s[10:11], 0, v5
	v_cndmask_b32_e32 v7, v7, v13, vcc
	v_and_b32_e32 v5, 4, v6
	v_or_b32_e32 v98, 0x500, v16
	v_lshlrev_b32_e32 v183, 2, v7
	v_cmp_eq_u32_e64 s[12:13], 0, v5
	v_bfe_u32 v104, v6, 2, 4
	v_and_or_b32 v5, v6, 48, v9
	v_lshlrev_b32_e32 v6, 2, v12
	v_mov_b32_e32 v7, v17
	v_or_b32_e32 v100, 0x600, v16
	s_waitcnt lgkmcnt(0)
	v_lshl_add_u64 v[84:85], s[22:23], 0, v[6:7]
	v_lshlrev_b32_e32 v6, 2, v98
	v_or_b32_e32 v102, 0x700, v16
	v_lshl_add_u64 v[86:87], s[22:23], 0, v[6:7]
	v_lshlrev_b32_e32 v6, 2, v100
	s_waitcnt vmcnt(32)
	v_mov_b32_e32 v3, v17
	v_lshl_add_u64 v[88:89], s[22:23], 0, v[6:7]
	v_lshlrev_b32_e32 v6, 2, v102
	v_lshl_add_u64 v[90:91], s[22:23], 0, v[6:7]
	s_add_u32 s35, s40, 0x4dc00000
	v_lshl_add_u64 v[92:93], s[14:15], 0, v[2:3]
	v_lshl_add_u64 v[6:7], s[40:41], 0, v[16:17]
	s_mov_b64 s[14:15], 0x4dd00000
	s_addc_u32 s38, s41, 0
	v_lshl_add_u64 v[94:95], v[6:7], 0, s[14:15]
	s_lshl_b32 s14, s18, 3
	s_add_i32 s14, s14, 0
	s_add_i32 s39, s14, 0x20300
	s_lshl_b32 s14, s18, 2
	s_add_i32 s14, s14, 0
	s_add_i32 s47, s18, 8
	s_add_i32 s18, s18, s31
	s_add_i32 s46, s14, 0x20100
	s_lshl_b32 s14, s18, 3
	s_add_i32 s14, s14, 0
	s_add_i32 s48, s14, 0x20300
	s_lshl_b32 s14, s18, 2
	v_or_b32_e32 v4, 0x100, v16
	v_or_b32_e32 v8, 0x200, v16
	v_or_b32_e32 v10, 0x300, v16
	v_add_u32_e32 v184, 0, v82
	v_lshlrev_b32_e32 v185, 2, v5
	v_lshlrev_b32_e32 v189, 2, v9
	v_mov_b32_e32 v83, v17
	s_add_i32 s14, s14, 0
	v_lshlrev_b32_e32 v1, 2, v1
	v_or_b32_e32 v186, 16, v185
	v_or_b32_e32 v187, 32, v185
	v_or_b32_e32 v188, 48, v185
	v_or_b32_e32 v190, 64, v189
	v_or_b32_e32 v191, 0x80, v189
	v_or_b32_e32 v192, 0xc0, v189
	v_add_u32_e32 v193, 0x10000, v184
	v_lshl_add_u64 v[82:83], s[22:23], 0, v[82:83]
	v_lshl_add_u64 v[96:97], s[16:17], 0, v[2:3]
	s_add_i32 s49, s14, 0x20100
	s_add_i32 s50, s31, s29
	v_lshlrev_b32_e32 v240, 2, v16
	v_lshlrev_b32_e32 v241, 2, v4
	v_lshlrev_b32_e32 v242, 2, v8
	v_lshlrev_b32_e32 v243, 2, v10
	v_lshlrev_b32_e32 v244, 2, v12
	v_lshlrev_b32_e32 v245, 2, v98
	v_lshlrev_b32_e32 v246, 2, v100
	v_lshlrev_b32_e32 v247, 2, v102
	v_mov_b32_e32 v248, 0x358637bd
	s_mov_b32 s51, 0x800000
	v_lshlrev_b32_e32 v249, 2, v104
	s_mov_b32 s52, 0xff61b1e6
	v_mov_b32_e32 v250, 0xff61b1e6
	s_branch .LBB0_1693

.LBB0_1693:
	s_add_i32 s14, s29, s47
	s_add_i32 s16, s14, -8
	s_min_i32 s15, s16, 0x4000
	s_ashr_i32 s15, s15, 13
	s_mul_i32 s18, s15, 0x3000
	s_ashr_i32 s17, s16, 31
	s_ashr_i32 s19, s18, 31
	s_lshl_b64 s[22:23], s[16:17], 11
	s_lshl_b64 s[18:19], s[18:19], 2
	s_add_u32 s15, s33, s18
	s_addc_u32 s26, s34, s19
	s_add_u32 s18, s15, 0x4000
	s_addc_u32 s19, s26, 0
	s_waitcnt lgkmcnt(0)
	s_add_u32 s100, s15, 0x6000
	s_addc_u32 s101, s26, 0
	s_add_u32 s98, s15, 0x8000
	s_addc_u32 s99, s26, 0
	global_load_dwordx4 v[132:135], v240, s[18:19]
	global_load_dwordx4 v[136:139], v241, s[18:19]
	global_load_dwordx4 v[140:143], v242, s[18:19]
	global_load_dwordx4 v[144:147], v243, s[18:19]
	global_load_dwordx4 v[148:151], v244, s[18:19]
	global_load_dwordx4 v[152:155], v245, s[18:19]
	global_load_dwordx4 v[156:159], v246, s[18:19]
	global_load_dwordx4 v[160:163], v247, s[18:19]
	global_load_dwordx4 v[164:167], v[82:83], off
	global_load_dwordx4 v[168:171], v240, s[100:101]
	global_load_dwordx4 v[172:175], v240, s[98:99]
	global_load_dwordx4 v[176:179], v[82:83], off offset:1024
	global_load_dwordx4 v[196:199], v241, s[100:101]
	global_load_dwordx4 v[200:203], v241, s[98:99]
	global_load_dwordx4 v[204:207], v[82:83], off offset:2048
	global_load_dwordx4 v[208:211], v242, s[100:101]
	global_load_dwordx4 v[212:215], v242, s[98:99]
	global_load_dwordx4 v[216:219], v[82:83], off offset:3072
	global_load_dwordx4 v[220:223], v243, s[100:101]
	global_load_dwordx4 v[224:227], v243, s[98:99]
	global_load_dwordx4 v[228:231], v[84:85], off
	global_load_dwordx4 v[232:235], v244, s[100:101]
	global_load_dwordx4 v[236:239], v244, s[98:99]
	global_load_dwordx4 v[252:255], v[86:87], off
	s_waitcnt vmcnt(32)
	v_lshlrev_b32_e32 v2, 16, v18
	v_and_b32_e32 v3, 0xffff0000, v18
	s_waitcnt vmcnt(28)
	v_lshlrev_b32_e32 v8, 16, v26
	v_and_b32_e32 v9, 0xffff0000, v26
	s_lshl_b64 s[24:25], s[16:17], 12
	v_lshl_add_u64 v[118:119], v[92:93], 0, s[24:25]
	s_waitcnt vmcnt(27)
	v_lshlrev_b32_e32 v12, 16, v28
	v_and_b32_e32 v13, 0xffff0000, v28
	s_waitcnt vmcnt(25)
	v_lshlrev_b32_e32 v104, 16, v32
	v_and_b32_e32 v105, 0xffff0000, v32
	s_waitcnt vmcnt(20)
	v_lshlrev_b32_e32 v108, 16, v42
	v_and_b32_e32 v109, 0xffff0000, v42
	v_lshlrev_b32_e32 v128, 16, v40
	v_and_b32_e32 v129, 0xffff0000, v40
	s_waitcnt vmcnt(17)
	v_lshlrev_b32_e32 v130, 16, v48
	v_and_b32_e32 v131, 0xffff0000, v48
	s_add_u32 s24, s15, 0x6000
	s_addc_u32 s25, s26, 0
	s_waitcnt vmcnt(23)
	v_pk_fma_f32 v[4:5], v[132:133], v[8:9], v[2:3]
	v_lshlrev_b32_e32 v2, 16, v19
	v_and_b32_e32 v3, 0xffff0000, v19
	v_lshlrev_b32_e32 v8, 16, v27
	v_and_b32_e32 v9, 0xffff0000, v27
	v_pk_fma_f32 v[10:11], v[134:135], v[8:9], v[2:3]
	v_cvt_pk_bf16_f32 v2, v4, v5
	v_cvt_pk_bf16_f32 v3, v10, v11
	global_store_dwordx2 v[118:119], v[2:3], off nt
	v_lshlrev_b32_e32 v2, 16, v20
	v_and_b32_e32 v3, 0xffff0000, v20
	v_mov_b32_e32 v98, v11
	s_waitcnt vmcnt(23)
	v_pk_fma_f32 v[2:3], v[136:137], v[12:13], v[2:3]
	v_lshlrev_b32_e32 v6, 16, v21
	v_and_b32_e32 v7, 0xffff0000, v21
	v_lshlrev_b32_e32 v12, 16, v29
	v_and_b32_e32 v13, 0xffff0000, v29
	v_pk_fma_f32 v[6:7], v[138:139], v[12:13], v[6:7]
	v_cvt_pk_bf16_f32 v8, v2, v3
	v_cvt_pk_bf16_f32 v9, v6, v7
	v_mov_b32_e32 v12, v5
	v_mov_b32_e32 v13, v3
	global_store_dwordx2 v[118:119], v[8:9], off offset:512 nt
	v_mov_b32_e32 v8, v4
	v_mov_b32_e32 v9, v2
	v_pk_mul_f32 v[12:13], v[12:13], v[12:13]
	v_mov_b32_e32 v99, v7
	v_pk_fma_f32 v[8:9], v[8:9], v[8:9], v[12:13]
	v_mov_b32_e32 v12, v10
	v_mov_b32_e32 v13, v6
	v_pk_mul_f32 v[98:99], v[98:99], v[98:99]
	s_nop 0
	v_pk_fma_f32 v[12:13], v[12:13], v[12:13], v[98:99]
	v_pk_add_f32 v[8:9], v[8:9], v[12:13]
	v_lshlrev_b32_e32 v12, 16, v30
	v_pk_add_f32 v[102:103], v[8:9], v[8:9] op_sel:[0,1] op_sel_hi:[1,0]
	v_lshlrev_b32_e32 v8, 16, v22
	v_and_b32_e32 v9, 0xffff0000, v22
	v_and_b32_e32 v13, 0xffff0000, v30
	s_waitcnt vmcnt(23)
	v_pk_fma_f32 v[12:13], v[140:141], v[12:13], v[8:9]
	v_lshlrev_b32_e32 v8, 16, v23
	v_and_b32_e32 v9, 0xffff0000, v23
	v_lshlrev_b32_e32 v98, 16, v31
	v_and_b32_e32 v99, 0xffff0000, v31
	v_pk_fma_f32 v[110:111], v[142:143], v[98:99], v[8:9]
	v_cvt_pk_bf16_f32 v8, v12, v13
	v_cvt_pk_bf16_f32 v9, v110, v111
	v_mov_b32_e32 v98, v13
	v_mov_b32_e32 v99, v111
	global_store_dwordx2 v[118:119], v[8:9], off offset:1024 nt
	v_mov_b32_e32 v8, v12
	v_mov_b32_e32 v9, v110
	v_pk_mul_f32 v[98:99], v[98:99], v[98:99]
	s_nop 0
	v_pk_fma_f32 v[8:9], v[8:9], v[8:9], v[98:99]
	v_pk_add_f32 v[106:107], v[8:9], v[8:9] op_sel:[0,1] op_sel_hi:[1,0]
	v_lshlrev_b32_e32 v8, 16, v24
	v_and_b32_e32 v9, 0xffff0000, v24
	s_waitcnt vmcnt(23)
	v_pk_fma_f32 v[104:105], v[144:145], v[104:105], v[8:9]
	v_lshlrev_b32_e32 v8, 16, v25
	v_and_b32_e32 v9, 0xffff0000, v25
	v_lshlrev_b32_e32 v98, 16, v33
	v_and_b32_e32 v99, 0xffff0000, v33
	v_pk_fma_f32 v[114:115], v[146:147], v[98:99], v[8:9]
	v_cvt_pk_bf16_f32 v8, v104, v105
	v_cvt_pk_bf16_f32 v9, v114, v115
	global_store_dwordx2 v[118:119], v[8:9], off offset:1536 nt
	v_mul_f32_e32 v8, v105, v105
	v_pk_fma_f32 v[112:113], v[104:105], v[104:105], v[8:9] op_sel_hi:[1,1,0]
	v_mul_f32_e32 v8, v115, v115
	v_pk_fma_f32 v[116:117], v[114:115], v[114:115], v[8:9] op_sel_hi:[1,1,0]
	v_lshlrev_b32_e32 v8, 16, v34
	v_and_b32_e32 v9, 0xffff0000, v34
	s_waitcnt vmcnt(23)
	v_pk_fma_f32 v[8:9], v[148:149], v[108:109], v[8:9]
	v_lshlrev_b32_e32 v98, 16, v35
	v_and_b32_e32 v99, 0xffff0000, v35
	v_lshlrev_b32_e32 v108, 16, v43
	v_and_b32_e32 v109, 0xffff0000, v43
	v_pk_fma_f32 v[108:109], v[150:151], v[108:109], v[98:99]
	v_cvt_pk_bf16_f32 v98, v8, v9
	v_cvt_pk_bf16_f32 v99, v108, v109
	global_store_dwordx2 v[118:119], v[98:99], off offset:2048 nt
	v_pk_mul_f32 v[98:99], v[8:9], v[8:9]
	v_pk_mul_f32 v[100:101], v[108:109], v[108:109]
	v_mov_b32_e32 v103, v98
	v_mov_b32_e32 v107, v99
	v_mov_b32_e32 v113, v100
	v_mov_b32_e32 v117, v101
	v_pk_add_f32 v[98:99], v[102:103], v[106:107]
	v_pk_add_f32 v[100:101], v[112:113], v[116:117]
	v_lshlrev_b32_e32 v102, 16, v36
	v_pk_add_f32 v[98:99], v[98:99], v[100:101]
	v_and_b32_e32 v103, 0xffff0000, v36
	v_pk_add_f32 v[120:121], v[98:99], v[98:99] op_sel:[0,1] op_sel_hi:[1,0]
	v_lshlrev_b32_e32 v106, 16, v44
	v_and_b32_e32 v107, 0xffff0000, v44
	v_lshlrev_b32_e32 v112, 16, v46
	v_and_b32_e32 v113, 0xffff0000, v46
	s_waitcnt vmcnt(23)
	v_pk_fma_f32 v[106:107], v[152:153], v[106:107], v[102:103]
	v_lshlrev_b32_e32 v98, 16, v37
	v_and_b32_e32 v99, 0xffff0000, v37
	v_lshlrev_b32_e32 v102, 16, v45
	v_and_b32_e32 v103, 0xffff0000, v45
	v_pk_fma_f32 v[116:117], v[154:155], v[102:103], v[98:99]
	v_cvt_pk_bf16_f32 v98, v106, v107
	v_cvt_pk_bf16_f32 v99, v116, v117
	v_mov_b32_e32 v100, v107
	v_mov_b32_e32 v101, v117
	global_store_dwordx2 v[118:119], v[98:99], off offset:2560 nt
	v_mov_b32_e32 v98, v106
	v_mov_b32_e32 v99, v116
	v_pk_mul_f32 v[100:101], v[100:101], v[100:101]
	v_lshlrev_b32_e32 v102, 16, v38
	v_pk_fma_f32 v[98:99], v[98:99], v[98:99], v[100:101]
	v_and_b32_e32 v103, 0xffff0000, v38
	v_pk_add_f32 v[122:123], v[98:99], v[98:99] op_sel:[0,1] op_sel_hi:[1,0]
	s_waitcnt vmcnt(23)
	v_pk_fma_f32 v[102:103], v[156:157], v[112:113], v[102:103]
	v_lshlrev_b32_e32 v98, 16, v39
	v_and_b32_e32 v99, 0xffff0000, v39
	v_lshlrev_b32_e32 v112, 16, v47
	v_and_b32_e32 v113, 0xffff0000, v47
	v_pk_fma_f32 v[112:113], v[158:159], v[112:113], v[98:99]
	v_cvt_pk_bf16_f32 v98, v102, v103
	v_cvt_pk_bf16_f32 v99, v112, v113
	global_store_dwordx2 v[118:119], v[98:99], off offset:3072 nt
	v_mul_f32_e32 v16, v103, v103
	v_pk_fma_f32 v[124:125], v[102:103], v[102:103], v[16:17] op_sel_hi:[1,1,0]
	v_mul_f32_e32 v16, v113, v113
	v_pk_fma_f32 v[126:127], v[112:113], v[112:113], v[16:17] op_sel_hi:[1,1,0]
	s_add_u32 s18, s15, 0x8000
	s_addc_u32 s19, s26, 0
	s_waitcnt vmcnt(23)
	v_pk_fma_f32 v[98:99], v[160:161], v[130:131], v[128:129]
	v_lshlrev_b32_e32 v128, 16, v41
	v_and_b32_e32 v129, 0xffff0000, v41
	v_lshlrev_b32_e32 v130, 16, v49
	v_and_b32_e32 v131, 0xffff0000, v49
	v_pk_fma_f32 v[100:101], v[162:163], v[130:131], v[128:129]
	global_load_dwordx4 v[160:163], v245, s[100:101]
	v_cvt_pk_bf16_f32 v128, v98, v99
	v_cvt_pk_bf16_f32 v129, v100, v101
	global_store_dwordx2 v[118:119], v[128:129], off offset:3584 nt
	v_pk_mul_f32 v[118:119], v[98:99], v[98:99]
	v_pk_mul_f32 v[128:129], v[100:101], v[100:101]
	v_mov_b32_e32 v121, v118
	v_mov_b32_e32 v123, v119
	v_mov_b32_e32 v125, v128
	v_mov_b32_e32 v127, v129
	v_pk_add_f32 v[118:119], v[120:121], v[122:123]
	v_pk_add_f32 v[120:121], v[124:125], v[126:127]
	s_nop 0
	v_pk_add_f32 v[118:119], v[118:119], v[120:121]
	s_nop 0
	v_add_f32_e32 v16, v118, v119
	ds_bpermute_b32 v118, v1, v16
	s_waitcnt lgkmcnt(0)
	v_add_f32_e32 v16, v16, v118
	ds_bpermute_b32 v118, v15, v16
	s_waitcnt lgkmcnt(0)
	v_add_f32_e32 v16, v16, v118
	ds_bpermute_b32 v118, v180, v16
	s_waitcnt lgkmcnt(0)
	v_add_f32_e32 v16, v16, v118
	ds_bpermute_b32 v118, v181, v16
	s_waitcnt lgkmcnt(0)
	v_add_f32_e32 v16, v16, v118
	ds_bpermute_b32 v118, v182, v16
	s_waitcnt lgkmcnt(0)
	v_add_f32_e32 v16, v16, v118
	ds_bpermute_b32 v118, v183, v16
	s_waitcnt lgkmcnt(0)
	v_add_f32_e32 v16, v16, v118
	v_fmamk_f32 v16, v16, 0x3a000000, v248
	v_cmp_gt_f32_e32 vcc, s51, v16
	v_mul_f32_e32 v118, 0x4b800000, v16
	s_nop 0
	v_cndmask_b32_e32 v16, v16, v118, vcc
	v_rsq_f32_e32 v16, v16
	s_nop 0
	v_mul_f32_e32 v118, 0x45800000, v16
	v_cndmask_b32_e32 v16, v16, v118, vcc
	v_pk_mul_f32 v[10:11], v[10:11], v[16:17] op_sel_hi:[1,0]
	v_pk_mul_f32 v[4:5], v[4:5], v[16:17] op_sel_hi:[1,0]
	v_pk_mul_f32 v[2:3], v[2:3], v[16:17] op_sel_hi:[1,0]
	v_pk_mul_f32 v[104:105], v[104:105], v[16:17] op_sel_hi:[1,0]
	v_pk_mul_f32 v[8:9], v[8:9], v[16:17] op_sel_hi:[1,0]
	v_pk_mul_f32 v[106:107], v[106:107], v[16:17] op_sel_hi:[1,0]
	v_pk_mul_f32 v[102:103], v[102:103], v[16:17] op_sel_hi:[1,0]
	v_pk_mul_f32 v[100:101], v[100:101], v[16:17] op_sel_hi:[1,0]
	v_pk_mul_f32 v[98:99], v[98:99], v[16:17] op_sel_hi:[1,0]
	s_waitcnt vmcnt(24)
	v_pk_mul_f32 v[4:5], v[164:165], v[4:5]
	v_pk_mul_f32 v[10:11], v[166:167], v[10:11]
	global_load_dwordx4 v[164:167], v245, s[98:99]
	s_waitcnt vmcnt(23)
	v_pk_add_f32 v[118:119], v[174:175], 1.0 op_sel_hi:[1,0]
	v_pk_add_f32 v[120:121], v[172:173], 1.0 op_sel_hi:[1,0]
	global_load_dwordx4 v[172:175], v[88:89], off
	v_pk_fma_f32 v[128:129], v[118:119], v[10:11], v[170:171]
	v_pk_fma_f32 v[130:131], v[120:121], v[4:5], v[168:169]
	global_load_dwordx4 v[168:171], v246, s[100:101]
	v_max_f32_e64 v4, |v128|, |v129|
	v_max3_f32 v136, |v130|, |v131|, v4
	v_pk_mul_f32 v[4:5], v[6:7], v[16:17] op_sel_hi:[1,0]
	s_waitcnt vmcnt(24)
	v_pk_mul_f32 v[2:3], v[176:177], v[2:3]
	v_pk_mul_f32 v[4:5], v[178:179], v[4:5]
	global_load_dwordx4 v[176:179], v246, s[98:99]
	s_waitcnt vmcnt(23)
	v_pk_add_f32 v[6:7], v[202:203], 1.0 op_sel_hi:[1,0]
	v_pk_add_f32 v[10:11], v[200:201], 1.0 op_sel_hi:[1,0]
	global_load_dwordx4 v[200:203], v[90:91], off
	v_pk_fma_f32 v[126:127], v[6:7], v[4:5], v[198:199]
	v_pk_fma_f32 v[132:133], v[10:11], v[2:3], v[196:197]
	global_load_dwordx4 v[196:199], v247, s[100:101]
	v_max_f32_e64 v2, |v126|, |v127|
	v_max3_f32 v2, |v132|, |v133|, v2
	v_max3_f32 v142, v136, 0, v2
	v_pk_mul_f32 v[6:7], v[110:111], v[16:17] op_sel_hi:[1,0]
	v_pk_mul_f32 v[10:11], v[12:13], v[16:17] op_sel_hi:[1,0]
	s_waitcnt vmcnt(24)
	v_pk_mul_f32 v[4:5], v[206:207], v[6:7]
	v_pk_mul_f32 v[2:3], v[204:205], v[10:11]
	global_load_dwordx4 v[204:207], v247, s[98:99]
	s_waitcnt vmcnt(23)
	v_pk_add_f32 v[6:7], v[214:215], 1.0 op_sel_hi:[1,0]
	v_pk_add_f32 v[10:11], v[212:213], 1.0 op_sel_hi:[1,0]
	v_pk_fma_f32 v[138:139], v[6:7], v[4:5], v[210:211]
	v_pk_fma_f32 v[140:141], v[10:11], v[2:3], v[208:209]
	v_max_f32_e64 v2, |v138|, |v139|
	v_max3_f32 v110, |v140|, |v141|, v2
	v_pk_mul_f32 v[6:7], v[114:115], v[16:17] op_sel_hi:[1,0]
	s_waitcnt vmcnt(22)
	v_pk_mul_f32 v[2:3], v[216:217], v[104:105]
	v_pk_mul_f32 v[4:5], v[218:219], v[6:7]
	s_waitcnt vmcnt(20)
	v_pk_add_f32 v[6:7], v[226:227], 1.0 op_sel_hi:[1,0]
	v_pk_add_f32 v[104:105], v[224:225], 1.0 op_sel_hi:[1,0]
	v_pk_fma_f32 v[134:135], v[6:7], v[4:5], v[222:223]
	v_pk_fma_f32 v[136:137], v[104:105], v[2:3], v[220:221]
	v_max_f32_e64 v2, |v134|, |v135|
	v_max3_f32 v2, |v136|, |v137|, v2
	v_max3_f32 v110, v142, v110, v2
	v_pk_mul_f32 v[6:7], v[108:109], v[16:17] op_sel_hi:[1,0]
	v_pk_mul_f32 v[104:105], v[116:117], v[16:17] op_sel_hi:[1,0]
	s_waitcnt vmcnt(19)
	v_pk_mul_f32 v[4:5], v[230:231], v[6:7]
	v_pk_mul_f32 v[2:3], v[228:229], v[8:9]
	s_waitcnt vmcnt(17)
	v_pk_add_f32 v[6:7], v[238:239], 1.0 op_sel_hi:[1,0]
	v_pk_add_f32 v[8:9], v[236:237], 1.0 op_sel_hi:[1,0]
	v_pk_fma_f32 v[144:145], v[4:5], v[6:7], v[234:235]
	v_pk_fma_f32 v[148:149], v[2:3], v[8:9], v[232:233]
	v_max_f32_e64 v2, |v144|, |v145|
	v_max3_f32 v108, |v148|, |v149|, v2
	s_waitcnt vmcnt(16)
	v_pk_mul_f32 v[4:5], v[104:105], v[254:255]
	v_pk_mul_f32 v[2:3], v[106:107], v[252:253]
	s_waitcnt vmcnt(6)
	v_pk_add_f32 v[12:13], v[166:167], 1.0 op_sel_hi:[1,0]
	v_pk_add_f32 v[10:11], v[164:165], 1.0 op_sel_hi:[1,0]
	v_pk_fma_f32 v[142:143], v[4:5], v[12:13], v[162:163]
	v_pk_fma_f32 v[146:147], v[2:3], v[10:11], v[160:161]
	v_max_f32_e64 v2, |v142|, |v143|
	v_max3_f32 v2, |v146|, |v147|, v2
	v_max3_f32 v104, v110, v108, v2
	v_pk_mul_f32 v[106:107], v[112:113], v[16:17] op_sel_hi:[1,0]
	s_waitcnt vmcnt(5)
	v_pk_mul_f32 v[2:3], v[102:103], v[172:173]
	v_pk_mul_f32 v[4:5], v[106:107], v[174:175]
	s_waitcnt vmcnt(3)
	v_pk_add_f32 v[12:13], v[178:179], 1.0 op_sel_hi:[1,0]
	v_pk_add_f32 v[10:11], v[176:177], 1.0 op_sel_hi:[1,0]
	v_pk_fma_f32 v[150:151], v[4:5], v[12:13], v[170:171]
	v_pk_fma_f32 v[152:153], v[2:3], v[10:11], v[168:169]
	v_max_f32_e64 v2, |v150|, |v151|
	v_max3_f32 v102, |v152|, |v153|, v2
	s_waitcnt vmcnt(2)
	v_pk_mul_f32 v[8:9], v[100:101], v[202:203]
	v_pk_mul_f32 v[6:7], v[98:99], v[200:201]
	s_waitcnt vmcnt(0)
	v_pk_add_f32 v[12:13], v[206:207], 1.0 op_sel_hi:[1,0]
	v_pk_add_f32 v[10:11], v[204:205], 1.0 op_sel_hi:[1,0]
	v_pk_fma_f32 v[154:155], v[8:9], v[12:13], v[198:199]
	v_pk_fma_f32 v[156:157], v[6:7], v[10:11], v[196:197]
	v_max_f32_e64 v2, |v154|, |v155|
	v_max3_f32 v2, |v156|, |v157|, v2
	v_max3_f32 v2, v104, v102, v2
	ds_bpermute_b32 v3, v1, v2
	s_waitcnt lgkmcnt(0)
	v_max_f32_e32 v3, v3, v3
	v_max_f32_e32 v2, v2, v3
	ds_bpermute_b32 v3, v15, v2
	s_waitcnt lgkmcnt(0)
	v_max_f32_e32 v3, v3, v3
	v_max_f32_e32 v2, v2, v3
	ds_bpermute_b32 v3, v180, v2
	s_waitcnt lgkmcnt(0)
	v_max_f32_e32 v3, v3, v3
	v_max_f32_e32 v2, v2, v3
	ds_bpermute_b32 v3, v181, v2
	s_waitcnt lgkmcnt(0)
	v_max_f32_e32 v3, v3, v3
	v_max_f32_e32 v2, v2, v3
	ds_bpermute_b32 v3, v182, v2
	s_waitcnt lgkmcnt(0)
	v_max_f32_e32 v3, v3, v3
	v_max_f32_e32 v2, v2, v3
	ds_bpermute_b32 v3, v183, v2
	s_and_saveexec_b64 s[18:19], s[4:5]
	s_cbranch_execz .LBB0_1695
	s_waitcnt lgkmcnt(0)
	v_max_f32_e32 v3, v3, v3
	v_max_f32_e32 v2, v2, v2
	s_lshl_b64 s[16:17], s[16:17], 2
	v_max_f32_e32 v2, v2, v3
	s_add_u32 s16, s35, s16
	v_mul_f32_e32 v2, 0x3c010204, v2
	s_addc_u32 s17, s38, s17
	global_store_dword v17, v2, s[16:17]
.LBB0_1695:
	s_or_b64 exec, exec, s[18:19]
	v_mov_b32_e32 v4, 0
	v_cvt_pk_fp8_f32 v4, v130, v131
	s_waitcnt lgkmcnt(0)
	v_lshl_add_u64 v[2:3], v[94:95], 0, s[22:23]
	s_add_i32 s16, s50, s47
	s_add_i32 s18, s16, -8
	v_cvt_pk_fp8_f32 v4, v128, v129 op_sel:[0,0,1]
	s_min_i32 s15, s18, 0x4000
	s_ashr_i32 s15, s15, 13
	s_mul_i32 s22, s15, 0x3000
	global_store_dword v[2:3], v4, off
	v_mov_b32_e32 v4, 0
	v_cvt_pk_fp8_f32 v4, v132, v133
	s_ashr_i32 s23, s22, 31
	s_ashr_i32 s19, s18, 31
	s_lshl_b64 s[22:23], s[22:23], 2
	v_cvt_pk_fp8_f32 v4, v126, v127 op_sel:[0,0,1]
	s_add_u32 s15, s33, s22
	s_addc_u32 s17, s34, s23
	s_add_u32 s22, s15, 0x4000
	global_store_dword v[2:3], v4, off offset:256
	v_mov_b32_e32 v4, 0
	v_cvt_pk_fp8_f32 v4, v140, v141
	s_addc_u32 s23, s17, 0
	v_lshlrev_b32_e32 v8, 16, v58
	v_and_b32_e32 v9, 0xffff0000, v58
	v_cvt_pk_fp8_f32 v4, v138, v139 op_sel:[0,0,1]
	s_lshl_b64 s[24:25], s[18:19], 12
	v_lshl_add_u64 v[98:99], v[92:93], 0, s[24:25]
	v_lshlrev_b32_e32 v12, 16, v60
	global_store_dword v[2:3], v4, off offset:512
	v_mov_b32_e32 v4, 0
	v_cvt_pk_fp8_f32 v4, v136, v137
	v_and_b32_e32 v13, 0xffff0000, v60
	v_lshlrev_b32_e32 v110, 16, v64
	v_and_b32_e32 v111, 0xffff0000, v64
	v_cvt_pk_fp8_f32 v4, v134, v135 op_sel:[0,0,1]
	v_lshlrev_b32_e32 v114, 16, v74
	v_and_b32_e32 v115, 0xffff0000, v74
	v_lshlrev_b32_e32 v122, 16, v78
	global_store_dword v[2:3], v4, off offset:768
	v_mov_b32_e32 v4, 0
	v_cvt_pk_fp8_f32 v4, v148, v149
	v_and_b32_e32 v123, 0xffff0000, v78
	v_lshlrev_b32_e32 v158, 16, v72
	v_and_b32_e32 v159, 0xffff0000, v72
	v_cvt_pk_fp8_f32 v4, v144, v145 op_sel:[0,0,1]
	v_lshlrev_b32_e32 v160, 16, v80
	v_and_b32_e32 v161, 0xffff0000, v80
	s_add_u32 s24, s15, 0x6000
	global_store_dword v[2:3], v4, off offset:1024
	v_mov_b32_e32 v4, 0
	v_cvt_pk_fp8_f32 v4, v146, v147
	s_addc_u32 s25, s17, 0
	v_cvt_pk_fp8_f32 v4, v142, v143 op_sel:[0,0,1]
	global_store_dword v[2:3], v4, off offset:1280
	v_mov_b32_e32 v4, 0
	v_cvt_pk_fp8_f32 v4, v152, v153
	v_cvt_pk_fp8_f32 v4, v150, v151 op_sel:[0,0,1]
	global_store_dword v[2:3], v4, off offset:1536
	v_mov_b32_e32 v4, 0
	v_cvt_pk_fp8_f32 v4, v156, v157
	v_cvt_pk_fp8_f32 v4, v154, v155 op_sel:[0,0,1]
	global_store_dword v[2:3], v4, off offset:1792
	s_add_u32 s100, s15, 0x6000
	s_addc_u32 s101, s17, 0
	s_add_u32 s98, s15, 0x8000
	s_addc_u32 s99, s17, 0
	global_load_dwordx4 v[164:167], v240, s[22:23]
	global_load_dwordx4 v[168:171], v241, s[22:23]
	global_load_dwordx4 v[172:175], v242, s[22:23]
	global_load_dwordx4 v[176:179], v243, s[22:23]
	global_load_dwordx4 v[196:199], v244, s[22:23]
	global_load_dwordx4 v[200:203], v245, s[22:23]
	global_load_dwordx4 v[204:207], v246, s[22:23]
	global_load_dwordx4 v[208:211], v247, s[22:23]
	global_load_dwordx4 v[212:215], v[82:83], off
	global_load_dwordx4 v[216:219], v240, s[100:101]
	global_load_dwordx4 v[220:223], v240, s[98:99]
	global_load_dwordx4 v[224:227], v[82:83], off offset:1024
	global_load_dwordx4 v[228:231], v241, s[100:101]
	global_load_dwordx4 v[232:235], v241, s[98:99]
	global_load_dwordx4 v[236:239], v[82:83], off offset:2048
	global_load_dwordx4 v[252:255], v242, s[100:101]
	v_lshlrev_b32_e32 v2, 16, v50
	v_and_b32_e32 v3, 0xffff0000, v50
	s_waitcnt vmcnt(15)
	v_pk_fma_f32 v[4:5], v[164:165], v[8:9], v[2:3]
	v_lshlrev_b32_e32 v2, 16, v51
	v_and_b32_e32 v3, 0xffff0000, v51
	v_lshlrev_b32_e32 v8, 16, v59
	v_and_b32_e32 v9, 0xffff0000, v59
	v_pk_fma_f32 v[10:11], v[166:167], v[8:9], v[2:3]
	v_cvt_pk_bf16_f32 v2, v4, v5
	v_cvt_pk_bf16_f32 v3, v10, v11
	global_store_dwordx2 v[98:99], v[2:3], off nt
	v_lshlrev_b32_e32 v2, 16, v52
	v_and_b32_e32 v3, 0xffff0000, v52
	v_mov_b32_e32 v100, v11
	s_waitcnt vmcnt(15)
	v_pk_fma_f32 v[2:3], v[168:169], v[12:13], v[2:3]
	v_lshlrev_b32_e32 v6, 16, v53
	v_and_b32_e32 v7, 0xffff0000, v53
	v_lshlrev_b32_e32 v12, 16, v61
	v_and_b32_e32 v13, 0xffff0000, v61
	v_pk_fma_f32 v[6:7], v[170:171], v[12:13], v[6:7]
	v_cvt_pk_bf16_f32 v8, v2, v3
	v_cvt_pk_bf16_f32 v9, v6, v7
	v_mov_b32_e32 v12, v5
	v_mov_b32_e32 v13, v3
	global_store_dwordx2 v[98:99], v[8:9], off offset:512 nt
	v_mov_b32_e32 v8, v4
	v_mov_b32_e32 v9, v2
	v_pk_mul_f32 v[12:13], v[12:13], v[12:13]
	v_mov_b32_e32 v101, v7
	v_pk_fma_f32 v[8:9], v[8:9], v[8:9], v[12:13]
	v_mov_b32_e32 v12, v10
	v_mov_b32_e32 v13, v6
	v_pk_mul_f32 v[100:101], v[100:101], v[100:101]
	s_nop 0
	v_pk_fma_f32 v[12:13], v[12:13], v[12:13], v[100:101]
	v_pk_add_f32 v[8:9], v[8:9], v[12:13]
	v_lshlrev_b32_e32 v12, 16, v62
	v_pk_add_f32 v[104:105], v[8:9], v[8:9] op_sel:[0,1] op_sel_hi:[1,0]
	v_lshlrev_b32_e32 v8, 16, v54
	v_and_b32_e32 v9, 0xffff0000, v54
	v_and_b32_e32 v13, 0xffff0000, v62
	s_waitcnt vmcnt(15)
	v_pk_fma_f32 v[12:13], v[172:173], v[12:13], v[8:9]
	v_lshlrev_b32_e32 v8, 16, v55
	v_and_b32_e32 v9, 0xffff0000, v55
	v_lshlrev_b32_e32 v100, 16, v63
	v_and_b32_e32 v101, 0xffff0000, v63
	v_pk_fma_f32 v[106:107], v[174:175], v[100:101], v[8:9]
	global_load_dwordx4 v[172:175], v242, s[98:99]
	v_cvt_pk_bf16_f32 v8, v12, v13
	v_cvt_pk_bf16_f32 v9, v106, v107
	v_mov_b32_e32 v100, v13
	v_mov_b32_e32 v101, v107
	global_store_dwordx2 v[98:99], v[8:9], off offset:1024 nt
	v_mov_b32_e32 v8, v12
	v_mov_b32_e32 v9, v106
	v_pk_mul_f32 v[100:101], v[100:101], v[100:101]
	s_nop 0
	v_pk_fma_f32 v[8:9], v[8:9], v[8:9], v[100:101]
	v_pk_add_f32 v[108:109], v[8:9], v[8:9] op_sel:[0,1] op_sel_hi:[1,0]
	v_lshlrev_b32_e32 v8, 16, v56
	v_and_b32_e32 v9, 0xffff0000, v56
	s_waitcnt vmcnt(16)
	v_pk_fma_f32 v[110:111], v[176:177], v[110:111], v[8:9]
	v_lshlrev_b32_e32 v8, 16, v57
	v_and_b32_e32 v9, 0xffff0000, v57
	v_lshlrev_b32_e32 v100, 16, v65
	v_and_b32_e32 v101, 0xffff0000, v65
	v_pk_fma_f32 v[112:113], v[178:179], v[100:101], v[8:9]
	global_load_dwordx4 v[176:179], v[82:83], off offset:3072
	v_cvt_pk_bf16_f32 v8, v110, v111
	v_cvt_pk_bf16_f32 v9, v112, v113
	global_store_dwordx2 v[98:99], v[8:9], off offset:1536 nt
	v_mul_f32_e32 v8, v111, v111
	v_pk_fma_f32 v[116:117], v[110:111], v[110:111], v[8:9] op_sel_hi:[1,1,0]
	v_mul_f32_e32 v8, v113, v113
	v_pk_fma_f32 v[118:119], v[112:113], v[112:113], v[8:9] op_sel_hi:[1,1,0]
	v_lshlrev_b32_e32 v8, 16, v66
	v_and_b32_e32 v9, 0xffff0000, v66
	s_waitcnt vmcnt(17)
	v_pk_fma_f32 v[8:9], v[196:197], v[114:115], v[8:9]
	v_lshlrev_b32_e32 v100, 16, v67
	v_and_b32_e32 v101, 0xffff0000, v67
	v_lshlrev_b32_e32 v114, 16, v75
	v_and_b32_e32 v115, 0xffff0000, v75
	v_pk_fma_f32 v[114:115], v[198:199], v[114:115], v[100:101]
	global_load_dwordx4 v[196:199], v243, s[100:101]
	v_cvt_pk_bf16_f32 v100, v8, v9
	v_cvt_pk_bf16_f32 v101, v114, v115
	global_store_dwordx2 v[98:99], v[100:101], off offset:2048 nt
	v_pk_mul_f32 v[100:101], v[8:9], v[8:9]
	v_pk_mul_f32 v[102:103], v[114:115], v[114:115]
	v_mov_b32_e32 v105, v100
	v_mov_b32_e32 v109, v101
	v_mov_b32_e32 v117, v102
	v_mov_b32_e32 v119, v103
	v_pk_add_f32 v[100:101], v[104:105], v[108:109]
	v_pk_add_f32 v[102:103], v[116:117], v[118:119]
	v_lshlrev_b32_e32 v108, 16, v68
	v_pk_add_f32 v[100:101], v[100:101], v[102:103]
	v_and_b32_e32 v109, 0xffff0000, v68
	v_pk_add_f32 v[104:105], v[100:101], v[100:101] op_sel:[0,1] op_sel_hi:[1,0]
	v_lshlrev_b32_e32 v116, 16, v76
	v_and_b32_e32 v117, 0xffff0000, v76
	s_waitcnt vmcnt(18)
	v_pk_fma_f32 v[118:119], v[200:201], v[116:117], v[108:109]
	v_lshlrev_b32_e32 v100, 16, v69
	v_and_b32_e32 v101, 0xffff0000, v69
	v_lshlrev_b32_e32 v108, 16, v77
	v_and_b32_e32 v109, 0xffff0000, v77
	v_pk_fma_f32 v[120:121], v[202:203], v[108:109], v[100:101]
	global_load_dwordx4 v[200:203], v243, s[98:99]
	v_cvt_pk_bf16_f32 v100, v118, v119
	v_cvt_pk_bf16_f32 v101, v120, v121
	v_mov_b32_e32 v102, v119
	v_mov_b32_e32 v103, v121
	global_store_dwordx2 v[98:99], v[100:101], off offset:2560 nt
	v_mov_b32_e32 v100, v118
	v_mov_b32_e32 v101, v120
	v_pk_mul_f32 v[102:103], v[102:103], v[102:103]
	v_lshlrev_b32_e32 v116, 16, v70
	v_pk_fma_f32 v[100:101], v[100:101], v[100:101], v[102:103]
	v_and_b32_e32 v117, 0xffff0000, v70
	v_pk_add_f32 v[108:109], v[100:101], v[100:101] op_sel:[0,1] op_sel_hi:[1,0]
	s_waitcnt vmcnt(19)
	v_pk_fma_f32 v[122:123], v[204:205], v[122:123], v[116:117]
	v_lshlrev_b32_e32 v100, 16, v71
	v_and_b32_e32 v101, 0xffff0000, v71
	v_lshlrev_b32_e32 v116, 16, v79
	v_and_b32_e32 v117, 0xffff0000, v79
	v_pk_fma_f32 v[124:125], v[206:207], v[116:117], v[100:101]
	global_load_dwordx4 v[204:207], v[84:85], off
	v_cvt_pk_bf16_f32 v100, v122, v123
	v_cvt_pk_bf16_f32 v101, v124, v125
	global_store_dwordx2 v[98:99], v[100:101], off offset:3072 nt
	v_mul_f32_e32 v16, v123, v123
	v_pk_fma_f32 v[116:117], v[122:123], v[122:123], v[16:17] op_sel_hi:[1,1,0]
	v_mul_f32_e32 v16, v125, v125
	v_pk_fma_f32 v[162:163], v[124:125], v[124:125], v[16:17] op_sel_hi:[1,1,0]
	s_add_u32 s22, s15, 0x8000
	s_addc_u32 s23, s17, 0
	s_waitcnt vmcnt(20)
	v_pk_fma_f32 v[158:159], v[208:209], v[160:161], v[158:159]
	v_lshlrev_b32_e32 v100, 16, v73
	v_and_b32_e32 v101, 0xffff0000, v73
	v_lshlrev_b32_e32 v160, 16, v81
	v_and_b32_e32 v161, 0xffff0000, v81
	v_pk_fma_f32 v[160:161], v[210:211], v[160:161], v[100:101]
	global_load_dwordx4 v[208:211], v244, s[100:101]
	v_cvt_pk_bf16_f32 v100, v158, v159
	v_cvt_pk_bf16_f32 v101, v160, v161
	global_store_dwordx2 v[98:99], v[100:101], off offset:3584 nt
	v_pk_mul_f32 v[98:99], v[158:159], v[158:159]
	v_pk_mul_f32 v[100:101], v[160:161], v[160:161]
	v_mov_b32_e32 v105, v98
	v_mov_b32_e32 v109, v99
	v_mov_b32_e32 v117, v100
	v_mov_b32_e32 v163, v101
	v_pk_add_f32 v[98:99], v[104:105], v[108:109]
	v_pk_add_f32 v[100:101], v[116:117], v[162:163]
	s_nop 0
	v_pk_add_f32 v[98:99], v[98:99], v[100:101]
	s_nop 0
	v_add_f32_e32 v16, v98, v99
	ds_bpermute_b32 v98, v1, v16
	s_waitcnt lgkmcnt(0)
	v_add_f32_e32 v16, v16, v98
	ds_bpermute_b32 v98, v15, v16
	s_waitcnt lgkmcnt(0)
	v_add_f32_e32 v16, v16, v98
	ds_bpermute_b32 v98, v180, v16
	s_waitcnt lgkmcnt(0)
	v_add_f32_e32 v16, v16, v98
	ds_bpermute_b32 v98, v181, v16
	s_waitcnt lgkmcnt(0)
	v_add_f32_e32 v16, v16, v98
	ds_bpermute_b32 v98, v182, v16
	s_waitcnt lgkmcnt(0)
	v_add_f32_e32 v16, v16, v98
	ds_bpermute_b32 v98, v183, v16
	s_waitcnt lgkmcnt(0)
	v_add_f32_e32 v16, v16, v98
	v_fmamk_f32 v16, v16, 0x3a000000, v248
	v_cmp_gt_f32_e32 vcc, s51, v16
	v_mul_f32_e32 v98, 0x4b800000, v16
	s_nop 0
	v_cndmask_b32_e32 v16, v16, v98, vcc
	v_rsq_f32_e32 v16, v16
	s_nop 0
	v_mul_f32_e32 v98, 0x45800000, v16
	v_cndmask_b32_e32 v16, v16, v98, vcc
	v_pk_mul_f32 v[10:11], v[10:11], v[16:17] op_sel_hi:[1,0]
	v_pk_mul_f32 v[4:5], v[4:5], v[16:17] op_sel_hi:[1,0]
	v_pk_mul_f32 v[2:3], v[2:3], v[16:17] op_sel_hi:[1,0]
	v_pk_mul_f32 v[110:111], v[110:111], v[16:17] op_sel_hi:[1,0]
	v_pk_mul_f32 v[8:9], v[8:9], v[16:17] op_sel_hi:[1,0]
	v_pk_mul_f32 v[120:121], v[120:121], v[16:17] op_sel_hi:[1,0]
	v_pk_mul_f32 v[118:119], v[118:119], v[16:17] op_sel_hi:[1,0]
	v_pk_mul_f32 v[124:125], v[124:125], v[16:17] op_sel_hi:[1,0]
	v_pk_mul_f32 v[122:123], v[122:123], v[16:17] op_sel_hi:[1,0]
	v_pk_mul_f32 v[160:161], v[160:161], v[16:17] op_sel_hi:[1,0]
	v_pk_mul_f32 v[158:159], v[158:159], v[16:17] op_sel_hi:[1,0]
	s_waitcnt vmcnt(21)
	v_pk_mul_f32 v[4:5], v[212:213], v[4:5]
	v_pk_mul_f32 v[10:11], v[214:215], v[10:11]
	global_load_dwordx4 v[212:215], v244, s[98:99]
	s_waitcnt vmcnt(20)
	v_pk_add_f32 v[98:99], v[222:223], 1.0 op_sel_hi:[1,0]
	v_pk_add_f32 v[100:101], v[220:221], 1.0 op_sel_hi:[1,0]
	global_load_dwordx4 v[220:223], v[86:87], off
	v_pk_fma_f32 v[98:99], v[98:99], v[10:11], v[218:219]
	v_pk_fma_f32 v[100:101], v[100:101], v[4:5], v[216:217]
	global_load_dwordx4 v[216:219], v245, s[100:101]
	v_max_f32_e64 v4, |v98|, |v99|
	v_max3_f32 v108, |v100|, |v101|, v4
	v_pk_mul_f32 v[4:5], v[6:7], v[16:17] op_sel_hi:[1,0]
	s_waitcnt vmcnt(21)
	v_pk_mul_f32 v[2:3], v[224:225], v[2:3]
	v_pk_mul_f32 v[4:5], v[226:227], v[4:5]
	global_load_dwordx4 v[224:227], v245, s[98:99]
	s_waitcnt vmcnt(20)
	v_pk_add_f32 v[6:7], v[234:235], 1.0 op_sel_hi:[1,0]
	v_pk_add_f32 v[10:11], v[232:233], 1.0 op_sel_hi:[1,0]
	global_load_dwordx4 v[232:235], v[88:89], off
	v_pk_fma_f32 v[102:103], v[6:7], v[4:5], v[230:231]
	v_pk_fma_f32 v[104:105], v[10:11], v[2:3], v[228:229]
	global_load_dwordx4 v[228:231], v246, s[100:101]
	v_max_f32_e64 v2, |v102|, |v103|
	v_max3_f32 v2, |v104|, |v105|, v2
	v_max3_f32 v116, v108, 0, v2
	v_pk_mul_f32 v[6:7], v[106:107], v[16:17] op_sel_hi:[1,0]
	v_pk_mul_f32 v[10:11], v[12:13], v[16:17] op_sel_hi:[1,0]
	s_waitcnt vmcnt(21)
	v_pk_mul_f32 v[4:5], v[238:239], v[6:7]
	v_pk_mul_f32 v[2:3], v[236:237], v[10:11]
	global_load_dwordx4 v[236:239], v246, s[98:99]
	s_waitcnt vmcnt(18)
	v_pk_add_f32 v[6:7], v[174:175], 1.0 op_sel_hi:[1,0]
	v_pk_add_f32 v[10:11], v[172:173], 1.0 op_sel_hi:[1,0]
	global_load_dwordx4 v[172:175], v[90:91], off
	v_pk_fma_f32 v[106:107], v[6:7], v[4:5], v[254:255]
	v_pk_fma_f32 v[108:109], v[10:11], v[2:3], v[252:253]
	global_load_dwordx4 v[252:255], v247, s[100:101]
	v_max_f32_e64 v2, |v106|, |v107|
	v_max3_f32 v117, |v108|, |v109|, v2
	v_pk_mul_f32 v[6:7], v[112:113], v[16:17] op_sel_hi:[1,0]
	s_waitcnt vmcnt(18)
	v_pk_mul_f32 v[2:3], v[176:177], v[110:111]
	v_pk_mul_f32 v[4:5], v[178:179], v[6:7]
	global_load_dwordx4 v[176:179], v247, s[98:99]
	s_waitcnt vmcnt(15)
	v_pk_add_f32 v[6:7], v[202:203], 1.0 op_sel_hi:[1,0]
	v_pk_add_f32 v[112:113], v[200:201], 1.0 op_sel_hi:[1,0]
	v_pk_fma_f32 v[110:111], v[6:7], v[4:5], v[198:199]
	v_pk_fma_f32 v[112:113], v[112:113], v[2:3], v[196:197]
	v_max_f32_e64 v2, |v110|, |v111|
	v_max3_f32 v2, |v112|, |v113|, v2
	v_max3_f32 v166, v116, v117, v2
	v_pk_mul_f32 v[6:7], v[114:115], v[16:17] op_sel_hi:[1,0]
	s_waitcnt vmcnt(13)
	v_pk_mul_f32 v[2:3], v[204:205], v[8:9]
	v_pk_mul_f32 v[4:5], v[206:207], v[6:7]
	s_waitcnt vmcnt(9)
	v_pk_add_f32 v[6:7], v[214:215], 1.0 op_sel_hi:[1,0]
	v_pk_add_f32 v[8:9], v[212:213], 1.0 op_sel_hi:[1,0]
	v_pk_fma_f32 v[114:115], v[6:7], v[4:5], v[210:211]
	v_pk_fma_f32 v[116:117], v[8:9], v[2:3], v[208:209]
	v_max_f32_e64 v2, |v114|, |v115|
	v_max3_f32 v162, |v116|, |v117|, v2
	s_waitcnt vmcnt(8)
	v_pk_mul_f32 v[4:5], v[120:121], v[222:223]
	v_pk_mul_f32 v[2:3], v[118:119], v[220:221]
	s_waitcnt vmcnt(6)
	v_pk_add_f32 v[12:13], v[226:227], 1.0 op_sel_hi:[1,0]
	v_pk_add_f32 v[10:11], v[224:225], 1.0 op_sel_hi:[1,0]
	v_pk_fma_f32 v[118:119], v[4:5], v[12:13], v[218:219]
	v_pk_fma_f32 v[120:121], v[2:3], v[10:11], v[216:217]
	v_max_f32_e64 v2, |v118|, |v119|
	v_max3_f32 v2, |v120|, |v121|, v2
	v_max3_f32 v162, v166, v162, v2
	s_waitcnt vmcnt(5)
	v_pk_mul_f32 v[4:5], v[124:125], v[234:235]
	v_pk_mul_f32 v[2:3], v[122:123], v[232:233]
	s_waitcnt vmcnt(3)
	v_pk_add_f32 v[12:13], v[238:239], 1.0 op_sel_hi:[1,0]
	v_pk_add_f32 v[10:11], v[236:237], 1.0 op_sel_hi:[1,0]
	v_pk_fma_f32 v[122:123], v[4:5], v[12:13], v[230:231]
	v_pk_fma_f32 v[124:125], v[2:3], v[10:11], v[228:229]
	v_max_f32_e64 v2, |v122|, |v123|
	v_max3_f32 v163, |v124|, |v125|, v2
	s_waitcnt vmcnt(2)
	v_pk_mul_f32 v[8:9], v[160:161], v[174:175]
	v_pk_mul_f32 v[6:7], v[158:159], v[172:173]
	s_waitcnt vmcnt(0)
	v_pk_add_f32 v[12:13], v[178:179], 1.0 op_sel_hi:[1,0]
	v_pk_add_f32 v[10:11], v[176:177], 1.0 op_sel_hi:[1,0]
	v_pk_fma_f32 v[4:5], v[8:9], v[12:13], v[254:255]
	v_pk_fma_f32 v[2:3], v[6:7], v[10:11], v[252:253]
	v_max_f32_e64 v6, |v4|, |v5|
	v_max3_f32 v6, |v2|, |v3|, v6
	v_max3_f32 v6, v162, v163, v6
	ds_bpermute_b32 v7, v1, v6
	s_waitcnt lgkmcnt(0)
	v_max_f32_e32 v7, v7, v7
	v_max_f32_e32 v6, v6, v7
	ds_bpermute_b32 v7, v15, v6
	s_waitcnt lgkmcnt(0)
	v_max_f32_e32 v7, v7, v7
	v_max_f32_e32 v6, v6, v7
	ds_bpermute_b32 v7, v180, v6
	s_waitcnt lgkmcnt(0)
	v_max_f32_e32 v7, v7, v7
	v_max_f32_e32 v6, v6, v7
	ds_bpermute_b32 v7, v181, v6
	s_waitcnt lgkmcnt(0)
	v_max_f32_e32 v7, v7, v7
	v_max_f32_e32 v6, v6, v7
	ds_bpermute_b32 v7, v182, v6
	s_waitcnt lgkmcnt(0)
	v_max_f32_e32 v7, v7, v7
	v_max_f32_e32 v6, v6, v7
	ds_bpermute_b32 v7, v183, v6
	s_and_saveexec_b64 s[22:23], s[4:5]
	s_cbranch_execz .LBB0_1697
	s_waitcnt lgkmcnt(0)
	v_max_f32_e32 v7, v7, v7
	v_max_f32_e32 v6, v6, v6
	s_lshl_b64 s[24:25], s[18:19], 2
	v_max_f32_e32 v6, v6, v7
	s_add_u32 s24, s35, s24
	v_mul_f32_e32 v6, 0x3c010204, v6
	s_addc_u32 s25, s38, s25
	global_store_dword v17, v6, s[24:25]

.LBB0_1699:
	ds_read_b128 v[8:11], v184
	ds_read_b128 v[158:161], v184 offset:5120
	v_mov_b32_e32 v6, v130
	v_mov_b32_e32 v7, v100
	v_mov_b32_e32 v100, v131
	s_waitcnt lgkmcnt(1)
	v_pk_fma_f32 v[12:13], v[6:7], v[8:9], 0 op_sel_hi:[1,0,0]
	s_nop 0
	v_pk_fma_f32 v[12:13], v[100:101], v[8:9], v[12:13] op_sel:[0,1,0]
	v_mov_b32_e32 v8, v128
	v_mov_b32_e32 v9, v98
	v_mov_b32_e32 v98, v129
	ds_read_b128 v[128:131], v184 offset:1024
	v_pk_fma_f32 v[12:13], v[8:9], v[10:11], v[12:13] op_sel_hi:[1,0,1]
	v_mov_b32_e32 v10, v11
	v_pk_fma_f32 v[12:13], v[98:99], v[10:11], v[12:13] op_sel_hi:[1,0,1]
	v_mov_b32_e32 v10, v132
	v_mov_b32_e32 v11, v104
	s_waitcnt lgkmcnt(0)
	v_pk_fma_f32 v[12:13], v[10:11], v[128:129], v[12:13] op_sel_hi:[1,0,1]
	v_mov_b32_e32 v104, v133
	v_pk_fma_f32 v[128:129], v[104:105], v[128:129], v[12:13] op_sel:[0,1,0]
	v_mov_b32_e32 v12, v126
	v_mov_b32_e32 v13, v102
	v_pk_fma_f32 v[128:129], v[12:13], v[130:131], v[128:129] op_sel_hi:[1,0,1]
	v_mov_b32_e32 v102, v127
	v_mov_b32_e32 v16, v131
	v_pk_fma_f32 v[132:133], v[102:103], v[16:17], v[128:129] op_sel_hi:[1,0,1]
	ds_read_b128 v[128:131], v184 offset:2048
	v_mov_b32_e32 v126, v140
	v_mov_b32_e32 v127, v108
	v_mov_b32_e32 v108, v141
	s_waitcnt lgkmcnt(0)
	v_pk_fma_f32 v[132:133], v[126:127], v[128:129], v[132:133] op_sel_hi:[1,0,1]
	s_nop 0
	v_pk_fma_f32 v[132:133], v[108:109], v[128:129], v[132:133] op_sel:[0,1,0]
	v_mov_b32_e32 v128, v138
	v_mov_b32_e32 v129, v106
	v_mov_b32_e32 v106, v139
	ds_read_b128 v[138:141], v184 offset:3072
	v_pk_fma_f32 v[132:133], v[128:129], v[130:131], v[132:133] op_sel_hi:[1,0,1]
	v_mov_b32_e32 v16, v131
	v_pk_fma_f32 v[132:133], v[106:107], v[16:17], v[132:133] op_sel_hi:[1,0,1]
	v_mov_b32_e32 v130, v136
	v_mov_b32_e32 v131, v112
	s_waitcnt lgkmcnt(0)
	v_pk_fma_f32 v[132:133], v[130:131], v[138:139], v[132:133] op_sel_hi:[1,0,1]
	v_mov_b32_e32 v112, v137
	v_pk_fma_f32 v[136:137], v[112:113], v[138:139], v[132:133] op_sel:[0,1,0]
	v_mov_b32_e32 v132, v134
	v_mov_b32_e32 v133, v110
	v_pk_fma_f32 v[136:137], v[132:133], v[140:141], v[136:137] op_sel_hi:[1,0,1]
	v_mov_b32_e32 v110, v135
	v_mov_b32_e32 v16, v141
	v_pk_fma_f32 v[140:141], v[110:111], v[16:17], v[136:137] op_sel_hi:[1,0,1]
	ds_read_b128 v[136:139], v184 offset:4096
	v_mov_b32_e32 v134, v148
	v_mov_b32_e32 v135, v116
	v_mov_b32_e32 v116, v149
	s_waitcnt lgkmcnt(0)
	v_pk_fma_f32 v[140:141], v[134:135], v[136:137], v[140:141] op_sel_hi:[1,0,1]
	s_nop 0
	v_pk_fma_f32 v[140:141], v[116:117], v[136:137], v[140:141] op_sel:[0,1,0]
	v_mov_b32_e32 v136, v144
	v_mov_b32_e32 v137, v114
	v_pk_fma_f32 v[140:141], v[136:137], v[138:139], v[140:141] op_sel_hi:[1,0,1]
	v_mov_b32_e32 v114, v145
	v_mov_b32_e32 v16, v139
	v_pk_fma_f32 v[140:141], v[114:115], v[16:17], v[140:141] op_sel_hi:[1,0,1]
	v_mov_b32_e32 v138, v146
	v_mov_b32_e32 v139, v120
	v_pk_fma_f32 v[140:141], v[138:139], v[158:159], v[140:141] op_sel_hi:[1,0,1]
	v_mov_b32_e32 v120, v147
	v_pk_fma_f32 v[144:145], v[120:121], v[158:159], v[140:141] op_sel:[0,1,0]
	v_mov_b32_e32 v140, v142
	v_mov_b32_e32 v141, v118
	v_pk_fma_f32 v[144:145], v[140:141], v[160:161], v[144:145] op_sel_hi:[1,0,1]
	v_mov_b32_e32 v118, v143
	v_mov_b32_e32 v16, v161
	v_pk_fma_f32 v[148:149], v[118:119], v[16:17], v[144:145] op_sel_hi:[1,0,1]
	ds_read_b128 v[144:147], v184 offset:6144
	v_mov_b32_e32 v142, v152
	v_mov_b32_e32 v143, v124
	v_mov_b32_e32 v124, v153
	s_waitcnt lgkmcnt(0)
	v_pk_fma_f32 v[148:149], v[142:143], v[144:145], v[148:149] op_sel_hi:[1,0,1]
	s_nop 0
	v_pk_fma_f32 v[148:149], v[124:125], v[144:145], v[148:149] op_sel:[0,1,0]
	v_mov_b32_e32 v144, v150
	v_mov_b32_e32 v145, v122
	v_mov_b32_e32 v122, v151
	ds_read_b128 v[150:153], v184 offset:7168
	v_pk_fma_f32 v[148:149], v[144:145], v[146:147], v[148:149] op_sel_hi:[1,0,1]
	v_mov_b32_e32 v16, v147
	v_pk_fma_f32 v[146:147], v[122:123], v[16:17], v[148:149] op_sel_hi:[1,0,1]
	v_mov_b32_e32 v148, v156
	v_mov_b32_e32 v149, v2
	s_waitcnt lgkmcnt(0)
	v_pk_fma_f32 v[146:147], v[148:149], v[150:151], v[146:147] op_sel_hi:[1,0,1]
	v_mov_b32_e32 v2, v157
	v_pk_fma_f32 v[146:147], v[2:3], v[150:151], v[146:147] op_sel:[0,1,0]
	v_mov_b32_e32 v150, v154
	v_mov_b32_e32 v151, v4
	v_pk_fma_f32 v[146:147], v[150:151], v[152:153], v[146:147] op_sel_hi:[1,0,1]
	v_mov_b32_e32 v4, v155
	v_mov_b32_e32 v16, v153
	v_pk_fma_f32 v[146:147], v[4:5], v[16:17], v[146:147] op_sel_hi:[1,0,1]
	s_nop 0
	v_mov_b32_e32 v16, v147
	ds_read_b128 v[152:155], v184 offset:8208
	s_waitcnt lgkmcnt(0)
	v_pk_fma_f32 v[156:157], v[6:7], v[152:153], 0 op_sel_hi:[1,0,0]
	s_nop 0
	v_pk_fma_f32 v[152:153], v[100:101], v[152:153], v[156:157] op_sel:[0,1,0]
	s_nop 0
	v_pk_fma_f32 v[152:153], v[8:9], v[154:155], v[152:153] op_sel_hi:[1,0,1]
	v_mov_b32_e32 v154, v155
	v_pk_fma_f32 v[156:157], v[98:99], v[154:155], v[152:153] op_sel_hi:[1,0,1]
	ds_read_b128 v[152:155], v184 offset:9232
	s_waitcnt lgkmcnt(0)
	v_pk_fma_f32 v[156:157], v[10:11], v[152:153], v[156:157] op_sel_hi:[1,0,1]
	s_nop 0
	v_pk_fma_f32 v[152:153], v[104:105], v[152:153], v[156:157] op_sel:[0,1,0]
	s_nop 0
	v_pk_fma_f32 v[152:153], v[12:13], v[154:155], v[152:153] op_sel_hi:[1,0,1]
	v_mov_b32_e32 v154, v155
	v_pk_fma_f32 v[156:157], v[102:103], v[154:155], v[152:153] op_sel_hi:[1,0,1]
	ds_read_b128 v[152:155], v184 offset:10256
	s_waitcnt lgkmcnt(0)
	v_pk_fma_f32 v[156:157], v[126:127], v[152:153], v[156:157] op_sel_hi:[1,0,1]
	s_nop 0
	v_pk_fma_f32 v[152:153], v[108:109], v[152:153], v[156:157] op_sel:[0,1,0]
	s_nop 0
	v_pk_fma_f32 v[152:153], v[128:129], v[154:155], v[152:153] op_sel_hi:[1,0,1]
	v_mov_b32_e32 v154, v155
	v_pk_fma_f32 v[156:157], v[106:107], v[154:155], v[152:153] op_sel_hi:[1,0,1]
	ds_read_b128 v[152:155], v184 offset:11280
	s_waitcnt lgkmcnt(0)
	v_pk_fma_f32 v[156:157], v[130:131], v[152:153], v[156:157] op_sel_hi:[1,0,1]
	s_nop 0
	v_pk_fma_f32 v[152:153], v[112:113], v[152:153], v[156:157] op_sel:[0,1,0]
	s_nop 0
	v_pk_fma_f32 v[152:153], v[132:133], v[154:155], v[152:153] op_sel_hi:[1,0,1]
	v_mov_b32_e32 v154, v155
	v_pk_fma_f32 v[156:157], v[110:111], v[154:155], v[152:153] op_sel_hi:[1,0,1]
	ds_read_b128 v[152:155], v184 offset:12304
	s_waitcnt lgkmcnt(0)
	v_pk_fma_f32 v[156:157], v[134:135], v[152:153], v[156:157] op_sel_hi:[1,0,1]
	s_nop 0
	v_pk_fma_f32 v[152:153], v[116:117], v[152:153], v[156:157] op_sel:[0,1,0]
	s_nop 0
	v_pk_fma_f32 v[152:153], v[136:137], v[154:155], v[152:153] op_sel_hi:[1,0,1]
	v_mov_b32_e32 v154, v155
	v_pk_fma_f32 v[156:157], v[114:115], v[154:155], v[152:153] op_sel_hi:[1,0,1]
	ds_read_b128 v[152:155], v184 offset:13328
	s_waitcnt lgkmcnt(0)
	v_pk_fma_f32 v[156:157], v[138:139], v[152:153], v[156:157] op_sel_hi:[1,0,1]
	s_nop 0
	v_pk_fma_f32 v[152:153], v[120:121], v[152:153], v[156:157] op_sel:[0,1,0]
	s_nop 0
	v_pk_fma_f32 v[152:153], v[140:141], v[154:155], v[152:153] op_sel_hi:[1,0,1]
	v_mov_b32_e32 v154, v155
	v_pk_fma_f32 v[156:157], v[118:119], v[154:155], v[152:153] op_sel_hi:[1,0,1]
	ds_read_b128 v[152:155], v184 offset:14352
	s_waitcnt lgkmcnt(0)
	v_pk_fma_f32 v[156:157], v[142:143], v[152:153], v[156:157] op_sel_hi:[1,0,1]
	s_nop 0
	v_pk_fma_f32 v[152:153], v[124:125], v[152:153], v[156:157] op_sel:[0,1,0]
	s_nop 0
	v_pk_fma_f32 v[152:153], v[144:145], v[154:155], v[152:153] op_sel_hi:[1,0,1]
	v_mov_b32_e32 v154, v155
	v_pk_fma_f32 v[156:157], v[122:123], v[154:155], v[152:153] op_sel_hi:[1,0,1]
	ds_read_b128 v[152:155], v184 offset:15376
	s_waitcnt lgkmcnt(0)
	v_pk_fma_f32 v[156:157], v[148:149], v[152:153], v[156:157] op_sel_hi:[1,0,1]
	s_nop 0
	v_pk_fma_f32 v[152:153], v[2:3], v[152:153], v[156:157] op_sel:[0,1,0]
	s_nop 0
	v_pk_fma_f32 v[152:153], v[150:151], v[154:155], v[152:153] op_sel_hi:[1,0,1]
	v_mov_b32_e32 v154, v155
	v_pk_fma_f32 v[152:153], v[4:5], v[154:155], v[152:153] op_sel_hi:[1,0,1]
	s_nop 0
	v_mov_b32_e32 v147, v153
	ds_read_b128 v[154:157], v184 offset:16416
	s_waitcnt lgkmcnt(0)
	v_pk_fma_f32 v[158:159], v[6:7], v[154:155], 0 op_sel_hi:[1,0,0]
	s_nop 0
	v_pk_fma_f32 v[154:155], v[100:101], v[154:155], v[158:159] op_sel:[0,1,0]
	s_nop 0
	v_pk_fma_f32 v[154:155], v[8:9], v[156:157], v[154:155] op_sel_hi:[1,0,1]
	v_mov_b32_e32 v156, v157
	v_pk_fma_f32 v[158:159], v[98:99], v[156:157], v[154:155] op_sel_hi:[1,0,1]
	ds_read_b128 v[154:157], v184 offset:17440
	s_waitcnt lgkmcnt(0)
	v_pk_fma_f32 v[158:159], v[10:11], v[154:155], v[158:159] op_sel_hi:[1,0,1]
	s_nop 0
	v_pk_fma_f32 v[154:155], v[104:105], v[154:155], v[158:159] op_sel:[0,1,0]
	s_nop 0
	v_pk_fma_f32 v[154:155], v[12:13], v[156:157], v[154:155] op_sel_hi:[1,0,1]
	v_mov_b32_e32 v156, v157
	v_pk_fma_f32 v[158:159], v[102:103], v[156:157], v[154:155] op_sel_hi:[1,0,1]
	ds_read_b128 v[154:157], v184 offset:18464
	s_waitcnt lgkmcnt(0)
	v_pk_fma_f32 v[158:159], v[126:127], v[154:155], v[158:159] op_sel_hi:[1,0,1]
	s_nop 0
	v_pk_fma_f32 v[154:155], v[108:109], v[154:155], v[158:159] op_sel:[0,1,0]
	s_nop 0
	v_pk_fma_f32 v[154:155], v[128:129], v[156:157], v[154:155] op_sel_hi:[1,0,1]
	v_mov_b32_e32 v156, v157
	v_pk_fma_f32 v[158:159], v[106:107], v[156:157], v[154:155] op_sel_hi:[1,0,1]
	ds_read_b128 v[154:157], v184 offset:19488
	s_waitcnt lgkmcnt(0)
	v_pk_fma_f32 v[158:159], v[130:131], v[154:155], v[158:159] op_sel_hi:[1,0,1]
	s_nop 0
	v_pk_fma_f32 v[154:155], v[112:113], v[154:155], v[158:159] op_sel:[0,1,0]
	s_nop 0
	v_pk_fma_f32 v[154:155], v[132:133], v[156:157], v[154:155] op_sel_hi:[1,0,1]
	v_mov_b32_e32 v156, v157
	v_pk_fma_f32 v[158:159], v[110:111], v[156:157], v[154:155] op_sel_hi:[1,0,1]
	ds_read_b128 v[154:157], v184 offset:20512
	s_waitcnt lgkmcnt(0)
	v_pk_fma_f32 v[158:159], v[134:135], v[154:155], v[158:159] op_sel_hi:[1,0,1]
	s_nop 0
	v_pk_fma_f32 v[154:155], v[116:117], v[154:155], v[158:159] op_sel:[0,1,0]
	s_nop 0
	v_pk_fma_f32 v[154:155], v[136:137], v[156:157], v[154:155] op_sel_hi:[1,0,1]
	v_mov_b32_e32 v156, v157
	v_pk_fma_f32 v[158:159], v[114:115], v[156:157], v[154:155] op_sel_hi:[1,0,1]
	ds_read_b128 v[154:157], v184 offset:21536
	s_waitcnt lgkmcnt(0)
	v_pk_fma_f32 v[158:159], v[138:139], v[154:155], v[158:159] op_sel_hi:[1,0,1]
	s_nop 0
	v_pk_fma_f32 v[154:155], v[120:121], v[154:155], v[158:159] op_sel:[0,1,0]
	s_nop 0
	v_pk_fma_f32 v[154:155], v[140:141], v[156:157], v[154:155] op_sel_hi:[1,0,1]
	v_mov_b32_e32 v156, v157
	v_pk_fma_f32 v[158:159], v[118:119], v[156:157], v[154:155] op_sel_hi:[1,0,1]
	ds_read_b128 v[154:157], v184 offset:22560
	s_waitcnt lgkmcnt(0)
	v_pk_fma_f32 v[158:159], v[142:143], v[154:155], v[158:159] op_sel_hi:[1,0,1]
	s_nop 0
	v_pk_fma_f32 v[154:155], v[124:125], v[154:155], v[158:159] op_sel:[0,1,0]
	s_nop 0
	v_pk_fma_f32 v[154:155], v[144:145], v[156:157], v[154:155] op_sel_hi:[1,0,1]
	v_mov_b32_e32 v156, v157
	v_pk_fma_f32 v[158:159], v[122:123], v[156:157], v[154:155] op_sel_hi:[1,0,1]
	ds_read_b128 v[154:157], v184 offset:23584
	s_waitcnt lgkmcnt(0)
	v_pk_fma_f32 v[158:159], v[148:149], v[154:155], v[158:159] op_sel_hi:[1,0,1]
	s_nop 0
	v_pk_fma_f32 v[154:155], v[2:3], v[154:155], v[158:159] op_sel:[0,1,0]
	s_nop 0
	v_pk_fma_f32 v[154:155], v[150:151], v[156:157], v[154:155] op_sel_hi:[1,0,1]
	v_mov_b32_e32 v156, v157
	v_pk_fma_f32 v[154:155], v[4:5], v[156:157], v[154:155] op_sel_hi:[1,0,1]
	s_nop 0
	v_mov_b32_e32 v153, v155
	ds_read_b128 v[156:159], v184 offset:24624
	s_waitcnt lgkmcnt(0)
	v_pk_fma_f32 v[160:161], v[6:7], v[156:157], 0 op_sel_hi:[1,0,0]
	s_nop 0
	v_pk_fma_f32 v[156:157], v[100:101], v[156:157], v[160:161] op_sel:[0,1,0]
	s_nop 0
	v_pk_fma_f32 v[156:157], v[8:9], v[158:159], v[156:157] op_sel_hi:[1,0,1]
	v_mov_b32_e32 v158, v159
	v_pk_fma_f32 v[160:161], v[98:99], v[158:159], v[156:157] op_sel_hi:[1,0,1]
	ds_read_b128 v[156:159], v184 offset:25648
	s_waitcnt lgkmcnt(0)
	v_pk_fma_f32 v[160:161], v[10:11], v[156:157], v[160:161] op_sel_hi:[1,0,1]
	s_nop 0
	v_pk_fma_f32 v[156:157], v[104:105], v[156:157], v[160:161] op_sel:[0,1,0]
	s_nop 0
	v_pk_fma_f32 v[156:157], v[12:13], v[158:159], v[156:157] op_sel_hi:[1,0,1]
	v_mov_b32_e32 v158, v159
	v_pk_fma_f32 v[160:161], v[102:103], v[158:159], v[156:157] op_sel_hi:[1,0,1]
	ds_read_b128 v[156:159], v184 offset:26672
	s_waitcnt lgkmcnt(0)
	v_pk_fma_f32 v[160:161], v[126:127], v[156:157], v[160:161] op_sel_hi:[1,0,1]
	s_nop 0
	v_pk_fma_f32 v[156:157], v[108:109], v[156:157], v[160:161] op_sel:[0,1,0]
	s_nop 0
	v_pk_fma_f32 v[156:157], v[128:129], v[158:159], v[156:157] op_sel_hi:[1,0,1]
	v_mov_b32_e32 v158, v159
	v_pk_fma_f32 v[160:161], v[106:107], v[158:159], v[156:157] op_sel_hi:[1,0,1]
	ds_read_b128 v[156:159], v184 offset:27696
	s_waitcnt lgkmcnt(0)
	v_pk_fma_f32 v[160:161], v[130:131], v[156:157], v[160:161] op_sel_hi:[1,0,1]
	s_nop 0
	v_pk_fma_f32 v[156:157], v[112:113], v[156:157], v[160:161] op_sel:[0,1,0]
	s_nop 0
	v_pk_fma_f32 v[156:157], v[132:133], v[158:159], v[156:157] op_sel_hi:[1,0,1]
	v_mov_b32_e32 v158, v159
	v_pk_fma_f32 v[160:161], v[110:111], v[158:159], v[156:157] op_sel_hi:[1,0,1]
	ds_read_b128 v[156:159], v184 offset:28720
	s_waitcnt lgkmcnt(0)
	v_pk_fma_f32 v[160:161], v[134:135], v[156:157], v[160:161] op_sel_hi:[1,0,1]
	s_nop 0
	v_pk_fma_f32 v[156:157], v[116:117], v[156:157], v[160:161] op_sel:[0,1,0]
	s_nop 0
	v_pk_fma_f32 v[156:157], v[136:137], v[158:159], v[156:157] op_sel_hi:[1,0,1]
	v_mov_b32_e32 v158, v159
	v_pk_fma_f32 v[160:161], v[114:115], v[158:159], v[156:157] op_sel_hi:[1,0,1]
	ds_read_b128 v[156:159], v184 offset:29744
	s_waitcnt lgkmcnt(0)
	v_pk_fma_f32 v[160:161], v[138:139], v[156:157], v[160:161] op_sel_hi:[1,0,1]
	s_nop 0
	v_pk_fma_f32 v[156:157], v[120:121], v[156:157], v[160:161] op_sel:[0,1,0]
	s_nop 0
	v_pk_fma_f32 v[156:157], v[140:141], v[158:159], v[156:157] op_sel_hi:[1,0,1]
	v_mov_b32_e32 v158, v159
	v_pk_fma_f32 v[160:161], v[118:119], v[158:159], v[156:157] op_sel_hi:[1,0,1]
	ds_read_b128 v[156:159], v184 offset:30768
	s_waitcnt lgkmcnt(0)
	v_pk_fma_f32 v[160:161], v[142:143], v[156:157], v[160:161] op_sel_hi:[1,0,1]
	s_nop 0
	v_pk_fma_f32 v[156:157], v[124:125], v[156:157], v[160:161] op_sel:[0,1,0]
	s_nop 0
	v_pk_fma_f32 v[156:157], v[144:145], v[158:159], v[156:157] op_sel_hi:[1,0,1]
	v_mov_b32_e32 v158, v159
	v_pk_fma_f32 v[160:161], v[122:123], v[158:159], v[156:157] op_sel_hi:[1,0,1]
	ds_read_b128 v[156:159], v184 offset:31792
	s_waitcnt lgkmcnt(0)
	v_pk_fma_f32 v[160:161], v[148:149], v[156:157], v[160:161] op_sel_hi:[1,0,1]
	s_nop 0
	v_pk_fma_f32 v[156:157], v[2:3], v[156:157], v[160:161] op_sel:[0,1,0]
	s_nop 0
	v_pk_fma_f32 v[156:157], v[150:151], v[158:159], v[156:157] op_sel_hi:[1,0,1]
	v_mov_b32_e32 v158, v159
	v_pk_fma_f32 v[156:157], v[4:5], v[158:159], v[156:157] op_sel_hi:[1,0,1]
	s_nop 0
	v_mov_b32_e32 v155, v157
	ds_read_b128 v[158:161], v184 offset:32832
	s_waitcnt lgkmcnt(0)
	v_pk_fma_f32 v[162:163], v[6:7], v[158:159], 0 op_sel_hi:[1,0,0]
	s_nop 0
	v_pk_fma_f32 v[158:159], v[100:101], v[158:159], v[162:163] op_sel:[0,1,0]
	s_nop 0
	v_pk_fma_f32 v[158:159], v[8:9], v[160:161], v[158:159] op_sel_hi:[1,0,1]
	v_mov_b32_e32 v160, v161
	v_pk_fma_f32 v[162:163], v[98:99], v[160:161], v[158:159] op_sel_hi:[1,0,1]
	ds_read_b128 v[158:161], v184 offset:33856
	s_waitcnt lgkmcnt(0)
	v_pk_fma_f32 v[162:163], v[10:11], v[158:159], v[162:163] op_sel_hi:[1,0,1]
	s_nop 0
	v_pk_fma_f32 v[158:159], v[104:105], v[158:159], v[162:163] op_sel:[0,1,0]
	s_nop 0
	v_pk_fma_f32 v[158:159], v[12:13], v[160:161], v[158:159] op_sel_hi:[1,0,1]
	v_mov_b32_e32 v160, v161
	v_pk_fma_f32 v[162:163], v[102:103], v[160:161], v[158:159] op_sel_hi:[1,0,1]
	ds_read_b128 v[158:161], v184 offset:34880
	s_waitcnt lgkmcnt(0)
	v_pk_fma_f32 v[162:163], v[126:127], v[158:159], v[162:163] op_sel_hi:[1,0,1]
	s_nop 0
	v_pk_fma_f32 v[158:159], v[108:109], v[158:159], v[162:163] op_sel:[0,1,0]
	s_nop 0
	v_pk_fma_f32 v[158:159], v[128:129], v[160:161], v[158:159] op_sel_hi:[1,0,1]
	v_mov_b32_e32 v160, v161
	v_pk_fma_f32 v[162:163], v[106:107], v[160:161], v[158:159] op_sel_hi:[1,0,1]
	ds_read_b128 v[158:161], v184 offset:35904
	s_waitcnt lgkmcnt(0)
	v_pk_fma_f32 v[162:163], v[130:131], v[158:159], v[162:163] op_sel_hi:[1,0,1]
	s_nop 0
	v_pk_fma_f32 v[158:159], v[112:113], v[158:159], v[162:163] op_sel:[0,1,0]
	s_nop 0
	v_pk_fma_f32 v[158:159], v[132:133], v[160:161], v[158:159] op_sel_hi:[1,0,1]
	v_mov_b32_e32 v160, v161
	v_pk_fma_f32 v[162:163], v[110:111], v[160:161], v[158:159] op_sel_hi:[1,0,1]
	ds_read_b128 v[158:161], v184 offset:36928
	s_waitcnt lgkmcnt(0)
	v_pk_fma_f32 v[162:163], v[134:135], v[158:159], v[162:163] op_sel_hi:[1,0,1]
	s_nop 0
	v_pk_fma_f32 v[158:159], v[116:117], v[158:159], v[162:163] op_sel:[0,1,0]
	s_nop 0
	v_pk_fma_f32 v[158:159], v[136:137], v[160:161], v[158:159] op_sel_hi:[1,0,1]
	v_mov_b32_e32 v160, v161
	v_pk_fma_f32 v[162:163], v[114:115], v[160:161], v[158:159] op_sel_hi:[1,0,1]
	ds_read_b128 v[158:161], v184 offset:37952
	s_waitcnt lgkmcnt(0)
	v_pk_fma_f32 v[162:163], v[138:139], v[158:159], v[162:163] op_sel_hi:[1,0,1]
	s_nop 0
	v_pk_fma_f32 v[158:159], v[120:121], v[158:159], v[162:163] op_sel:[0,1,0]
	s_nop 0
	v_pk_fma_f32 v[158:159], v[140:141], v[160:161], v[158:159] op_sel_hi:[1,0,1]
	v_mov_b32_e32 v160, v161
	v_pk_fma_f32 v[162:163], v[118:119], v[160:161], v[158:159] op_sel_hi:[1,0,1]
	ds_read_b128 v[158:161], v184 offset:38976
	s_waitcnt lgkmcnt(0)
	v_pk_fma_f32 v[162:163], v[142:143], v[158:159], v[162:163] op_sel_hi:[1,0,1]
	s_nop 0
	v_pk_fma_f32 v[158:159], v[124:125], v[158:159], v[162:163] op_sel:[0,1,0]
	s_nop 0
	v_pk_fma_f32 v[158:159], v[144:145], v[160:161], v[158:159] op_sel_hi:[1,0,1]
	v_mov_b32_e32 v160, v161
	v_pk_fma_f32 v[162:163], v[122:123], v[160:161], v[158:159] op_sel_hi:[1,0,1]
	ds_read_b128 v[158:161], v184 offset:40000
	s_waitcnt lgkmcnt(0)
	v_pk_fma_f32 v[162:163], v[148:149], v[158:159], v[162:163] op_sel_hi:[1,0,1]
	s_nop 0
	v_pk_fma_f32 v[158:159], v[2:3], v[158:159], v[162:163] op_sel:[0,1,0]
	s_nop 0
	v_pk_fma_f32 v[158:159], v[150:151], v[160:161], v[158:159] op_sel_hi:[1,0,1]
	v_mov_b32_e32 v160, v161
	v_pk_fma_f32 v[158:159], v[4:5], v[160:161], v[158:159] op_sel_hi:[1,0,1]
	s_nop 0
	v_mov_b32_e32 v157, v159
	ds_read_b128 v[160:163], v184 offset:41040
	s_waitcnt lgkmcnt(0)
	v_pk_fma_f32 v[164:165], v[6:7], v[160:161], 0 op_sel_hi:[1,0,0]
	s_nop 0
	v_pk_fma_f32 v[160:161], v[100:101], v[160:161], v[164:165] op_sel:[0,1,0]
	s_nop 0
	v_pk_fma_f32 v[160:161], v[8:9], v[162:163], v[160:161] op_sel_hi:[1,0,1]
	v_mov_b32_e32 v162, v163
	v_pk_fma_f32 v[164:165], v[98:99], v[162:163], v[160:161] op_sel_hi:[1,0,1]
	ds_read_b128 v[160:163], v184 offset:42064
	s_waitcnt lgkmcnt(0)
	v_pk_fma_f32 v[164:165], v[10:11], v[160:161], v[164:165] op_sel_hi:[1,0,1]
	s_nop 0
	v_pk_fma_f32 v[160:161], v[104:105], v[160:161], v[164:165] op_sel:[0,1,0]
	s_nop 0
	v_pk_fma_f32 v[160:161], v[12:13], v[162:163], v[160:161] op_sel_hi:[1,0,1]
	v_mov_b32_e32 v162, v163
	v_pk_fma_f32 v[164:165], v[102:103], v[162:163], v[160:161] op_sel_hi:[1,0,1]
	ds_read_b128 v[160:163], v184 offset:43088
	s_waitcnt lgkmcnt(0)
	v_pk_fma_f32 v[164:165], v[126:127], v[160:161], v[164:165] op_sel_hi:[1,0,1]
	s_nop 0
	v_pk_fma_f32 v[160:161], v[108:109], v[160:161], v[164:165] op_sel:[0,1,0]
	s_nop 0
	v_pk_fma_f32 v[160:161], v[128:129], v[162:163], v[160:161] op_sel_hi:[1,0,1]
	v_mov_b32_e32 v162, v163
	v_pk_fma_f32 v[164:165], v[106:107], v[162:163], v[160:161] op_sel_hi:[1,0,1]
	ds_read_b128 v[160:163], v184 offset:44112
	s_waitcnt lgkmcnt(0)
	v_pk_fma_f32 v[164:165], v[130:131], v[160:161], v[164:165] op_sel_hi:[1,0,1]
	s_nop 0
	v_pk_fma_f32 v[160:161], v[112:113], v[160:161], v[164:165] op_sel:[0,1,0]
	s_nop 0
	v_pk_fma_f32 v[160:161], v[132:133], v[162:163], v[160:161] op_sel_hi:[1,0,1]
	v_mov_b32_e32 v162, v163
	v_pk_fma_f32 v[164:165], v[110:111], v[162:163], v[160:161] op_sel_hi:[1,0,1]
	ds_read_b128 v[160:163], v184 offset:45136
	s_waitcnt lgkmcnt(0)
	v_pk_fma_f32 v[164:165], v[134:135], v[160:161], v[164:165] op_sel_hi:[1,0,1]
	s_nop 0
	v_pk_fma_f32 v[160:161], v[116:117], v[160:161], v[164:165] op_sel:[0,1,0]
	s_nop 0
	v_pk_fma_f32 v[160:161], v[136:137], v[162:163], v[160:161] op_sel_hi:[1,0,1]
	v_mov_b32_e32 v162, v163
	v_pk_fma_f32 v[164:165], v[114:115], v[162:163], v[160:161] op_sel_hi:[1,0,1]
	ds_read_b128 v[160:163], v184 offset:46160
	s_waitcnt lgkmcnt(0)
	v_pk_fma_f32 v[164:165], v[138:139], v[160:161], v[164:165] op_sel_hi:[1,0,1]
	s_nop 0
	v_pk_fma_f32 v[160:161], v[120:121], v[160:161], v[164:165] op_sel:[0,1,0]
	s_nop 0
	v_pk_fma_f32 v[160:161], v[140:141], v[162:163], v[160:161] op_sel_hi:[1,0,1]
	v_mov_b32_e32 v162, v163
	v_pk_fma_f32 v[164:165], v[118:119], v[162:163], v[160:161] op_sel_hi:[1,0,1]
	ds_read_b128 v[160:163], v184 offset:47184
	s_waitcnt lgkmcnt(0)
	v_pk_fma_f32 v[164:165], v[142:143], v[160:161], v[164:165] op_sel_hi:[1,0,1]
	s_nop 0
	v_pk_fma_f32 v[160:161], v[124:125], v[160:161], v[164:165] op_sel:[0,1,0]
	s_nop 0
	v_pk_fma_f32 v[160:161], v[144:145], v[162:163], v[160:161] op_sel_hi:[1,0,1]
	v_mov_b32_e32 v162, v163
	v_pk_fma_f32 v[164:165], v[122:123], v[162:163], v[160:161] op_sel_hi:[1,0,1]
	ds_read_b128 v[160:163], v184 offset:48208
	s_waitcnt lgkmcnt(0)
	v_pk_fma_f32 v[164:165], v[148:149], v[160:161], v[164:165] op_sel_hi:[1,0,1]
	s_nop 0
	v_pk_fma_f32 v[160:161], v[2:3], v[160:161], v[164:165] op_sel:[0,1,0]
	s_nop 0
	v_pk_fma_f32 v[160:161], v[150:151], v[162:163], v[160:161] op_sel_hi:[1,0,1]
	v_mov_b32_e32 v162, v163
	v_pk_fma_f32 v[160:161], v[4:5], v[162:163], v[160:161] op_sel_hi:[1,0,1]
	s_nop 0
	v_mov_b32_e32 v159, v161
	ds_read_b128 v[162:165], v184 offset:49248
	s_waitcnt lgkmcnt(0)
	v_pk_fma_f32 v[166:167], v[6:7], v[162:163], 0 op_sel_hi:[1,0,0]
	s_nop 0
	v_pk_fma_f32 v[162:163], v[100:101], v[162:163], v[166:167] op_sel:[0,1,0]
	s_nop 0
	v_pk_fma_f32 v[162:163], v[8:9], v[164:165], v[162:163] op_sel_hi:[1,0,1]
	v_mov_b32_e32 v164, v165
	v_pk_fma_f32 v[166:167], v[98:99], v[164:165], v[162:163] op_sel_hi:[1,0,1]
	ds_read_b128 v[162:165], v184 offset:50272
	s_waitcnt lgkmcnt(0)
	v_pk_fma_f32 v[166:167], v[10:11], v[162:163], v[166:167] op_sel_hi:[1,0,1]
	s_nop 0
	v_pk_fma_f32 v[162:163], v[104:105], v[162:163], v[166:167] op_sel:[0,1,0]
	s_nop 0
	v_pk_fma_f32 v[162:163], v[12:13], v[164:165], v[162:163] op_sel_hi:[1,0,1]
	v_mov_b32_e32 v164, v165
	v_pk_fma_f32 v[166:167], v[102:103], v[164:165], v[162:163] op_sel_hi:[1,0,1]
	ds_read_b128 v[162:165], v184 offset:51296
	s_waitcnt lgkmcnt(0)
	v_pk_fma_f32 v[166:167], v[126:127], v[162:163], v[166:167] op_sel_hi:[1,0,1]
	s_nop 0
	v_pk_fma_f32 v[162:163], v[108:109], v[162:163], v[166:167] op_sel:[0,1,0]
	s_nop 0
	v_pk_fma_f32 v[162:163], v[128:129], v[164:165], v[162:163] op_sel_hi:[1,0,1]
	v_mov_b32_e32 v164, v165
	v_pk_fma_f32 v[166:167], v[106:107], v[164:165], v[162:163] op_sel_hi:[1,0,1]
	ds_read_b128 v[162:165], v184 offset:52320
	s_waitcnt lgkmcnt(0)
	v_pk_fma_f32 v[166:167], v[130:131], v[162:163], v[166:167] op_sel_hi:[1,0,1]
	s_nop 0
	v_pk_fma_f32 v[162:163], v[112:113], v[162:163], v[166:167] op_sel:[0,1,0]
	s_nop 0
	v_pk_fma_f32 v[162:163], v[132:133], v[164:165], v[162:163] op_sel_hi:[1,0,1]
	v_mov_b32_e32 v164, v165
	v_pk_fma_f32 v[166:167], v[110:111], v[164:165], v[162:163] op_sel_hi:[1,0,1]
	ds_read_b128 v[162:165], v184 offset:53344
	s_waitcnt lgkmcnt(0)
	v_pk_fma_f32 v[166:167], v[134:135], v[162:163], v[166:167] op_sel_hi:[1,0,1]
	s_nop 0
	v_pk_fma_f32 v[162:163], v[116:117], v[162:163], v[166:167] op_sel:[0,1,0]
	s_nop 0
	v_pk_fma_f32 v[162:163], v[136:137], v[164:165], v[162:163] op_sel_hi:[1,0,1]
	v_mov_b32_e32 v164, v165
	v_pk_fma_f32 v[166:167], v[114:115], v[164:165], v[162:163] op_sel_hi:[1,0,1]
	ds_read_b128 v[162:165], v184 offset:54368
	s_waitcnt lgkmcnt(0)
	v_pk_fma_f32 v[166:167], v[138:139], v[162:163], v[166:167] op_sel_hi:[1,0,1]
	s_nop 0
	v_pk_fma_f32 v[162:163], v[120:121], v[162:163], v[166:167] op_sel:[0,1,0]
	s_nop 0
	v_pk_fma_f32 v[162:163], v[140:141], v[164:165], v[162:163] op_sel_hi:[1,0,1]
	v_mov_b32_e32 v164, v165
	v_pk_fma_f32 v[166:167], v[118:119], v[164:165], v[162:163] op_sel_hi:[1,0,1]
	ds_read_b128 v[162:165], v184 offset:55392
	s_waitcnt lgkmcnt(0)
	v_pk_fma_f32 v[166:167], v[142:143], v[162:163], v[166:167] op_sel_hi:[1,0,1]
	s_nop 0
	v_pk_fma_f32 v[162:163], v[124:125], v[162:163], v[166:167] op_sel:[0,1,0]
	s_nop 0
	v_pk_fma_f32 v[162:163], v[144:145], v[164:165], v[162:163] op_sel_hi:[1,0,1]
	v_mov_b32_e32 v164, v165
	v_pk_fma_f32 v[166:167], v[122:123], v[164:165], v[162:163] op_sel_hi:[1,0,1]
	ds_read_b128 v[162:165], v184 offset:56416
	s_waitcnt lgkmcnt(0)
	v_pk_fma_f32 v[166:167], v[148:149], v[162:163], v[166:167] op_sel_hi:[1,0,1]
	s_nop 0
	v_pk_fma_f32 v[162:163], v[2:3], v[162:163], v[166:167] op_sel:[0,1,0]
	s_nop 0
	v_pk_fma_f32 v[162:163], v[150:151], v[164:165], v[162:163] op_sel_hi:[1,0,1]
	v_mov_b32_e32 v164, v165
	v_pk_fma_f32 v[162:163], v[4:5], v[164:165], v[162:163] op_sel_hi:[1,0,1]
	s_nop 0
	v_mov_b32_e32 v161, v163
	ds_read_b128 v[164:167], v184 offset:57456
	s_waitcnt lgkmcnt(0)
	v_pk_fma_f32 v[168:169], v[6:7], v[164:165], 0 op_sel_hi:[1,0,0]
	s_nop 0
	v_pk_fma_f32 v[164:165], v[100:101], v[164:165], v[168:169] op_sel:[0,1,0]
	s_nop 0
	v_pk_fma_f32 v[164:165], v[8:9], v[166:167], v[164:165] op_sel_hi:[1,0,1]
	v_mov_b32_e32 v166, v167
	v_pk_fma_f32 v[168:169], v[98:99], v[166:167], v[164:165] op_sel_hi:[1,0,1]
	ds_read_b128 v[164:167], v184 offset:58480
	s_waitcnt lgkmcnt(0)
	v_pk_fma_f32 v[168:169], v[10:11], v[164:165], v[168:169] op_sel_hi:[1,0,1]
	s_nop 0
	v_pk_fma_f32 v[164:165], v[104:105], v[164:165], v[168:169] op_sel:[0,1,0]
	s_nop 0
	v_pk_fma_f32 v[164:165], v[12:13], v[166:167], v[164:165] op_sel_hi:[1,0,1]
	v_mov_b32_e32 v166, v167
	v_pk_fma_f32 v[168:169], v[102:103], v[166:167], v[164:165] op_sel_hi:[1,0,1]
	ds_read_b128 v[164:167], v184 offset:59504
	s_waitcnt lgkmcnt(0)
	v_pk_fma_f32 v[168:169], v[126:127], v[164:165], v[168:169] op_sel_hi:[1,0,1]
	s_nop 0
	v_pk_fma_f32 v[164:165], v[108:109], v[164:165], v[168:169] op_sel:[0,1,0]
	s_nop 0
	v_pk_fma_f32 v[164:165], v[128:129], v[166:167], v[164:165] op_sel_hi:[1,0,1]
	v_mov_b32_e32 v166, v167
	v_pk_fma_f32 v[168:169], v[106:107], v[166:167], v[164:165] op_sel_hi:[1,0,1]
	ds_read_b128 v[164:167], v184 offset:60528
	s_waitcnt lgkmcnt(0)
	v_pk_fma_f32 v[168:169], v[130:131], v[164:165], v[168:169] op_sel_hi:[1,0,1]
	s_nop 0
	v_pk_fma_f32 v[164:165], v[112:113], v[164:165], v[168:169] op_sel:[0,1,0]
	s_nop 0
	v_pk_fma_f32 v[164:165], v[132:133], v[166:167], v[164:165] op_sel_hi:[1,0,1]
	v_mov_b32_e32 v166, v167
	v_pk_fma_f32 v[168:169], v[110:111], v[166:167], v[164:165] op_sel_hi:[1,0,1]
	ds_read_b128 v[164:167], v184 offset:61552
	s_waitcnt lgkmcnt(0)
	v_pk_fma_f32 v[168:169], v[134:135], v[164:165], v[168:169] op_sel_hi:[1,0,1]
	s_nop 0
	v_pk_fma_f32 v[164:165], v[116:117], v[164:165], v[168:169] op_sel:[0,1,0]
	s_nop 0
	v_pk_fma_f32 v[164:165], v[136:137], v[166:167], v[164:165] op_sel_hi:[1,0,1]
	v_mov_b32_e32 v166, v167
	v_pk_fma_f32 v[168:169], v[114:115], v[166:167], v[164:165] op_sel_hi:[1,0,1]
	ds_read_b128 v[164:167], v184 offset:62576
	s_waitcnt lgkmcnt(0)
	v_pk_fma_f32 v[168:169], v[138:139], v[164:165], v[168:169] op_sel_hi:[1,0,1]
	s_nop 0
	v_pk_fma_f32 v[164:165], v[120:121], v[164:165], v[168:169] op_sel:[0,1,0]
	s_nop 0
	v_pk_fma_f32 v[164:165], v[140:141], v[166:167], v[164:165] op_sel_hi:[1,0,1]
	v_mov_b32_e32 v166, v167
	v_pk_fma_f32 v[168:169], v[118:119], v[166:167], v[164:165] op_sel_hi:[1,0,1]
	ds_read_b128 v[164:167], v184 offset:63600
	s_waitcnt lgkmcnt(0)
	v_pk_fma_f32 v[168:169], v[142:143], v[164:165], v[168:169] op_sel_hi:[1,0,1]
	s_nop 0
	v_pk_fma_f32 v[164:165], v[124:125], v[164:165], v[168:169] op_sel:[0,1,0]
	s_nop 0
	v_pk_fma_f32 v[164:165], v[144:145], v[166:167], v[164:165] op_sel_hi:[1,0,1]
	v_mov_b32_e32 v166, v167
	v_pk_fma_f32 v[168:169], v[122:123], v[166:167], v[164:165] op_sel_hi:[1,0,1]
	ds_read_b128 v[164:167], v184 offset:64624
	s_waitcnt lgkmcnt(0)
	v_pk_fma_f32 v[168:169], v[148:149], v[164:165], v[168:169] op_sel_hi:[1,0,1]
	s_nop 0
	v_pk_fma_f32 v[164:165], v[2:3], v[164:165], v[168:169] op_sel:[0,1,0]
	s_nop 0
	v_pk_fma_f32 v[164:165], v[150:151], v[166:167], v[164:165] op_sel_hi:[1,0,1]
	v_mov_b32_e32 v166, v167
	v_pk_fma_f32 v[164:165], v[4:5], v[166:167], v[164:165] op_sel_hi:[1,0,1]
	s_nop 0
	v_mov_b32_e32 v163, v165
	v_add_u32_e32 v165, 0x10080, v184
	ds_read_b128 v[166:169], v165
	v_add_u32_e32 v165, 0x10480, v184
	s_waitcnt lgkmcnt(0)
	v_pk_fma_f32 v[170:171], v[6:7], v[166:167], 0 op_sel_hi:[1,0,0]
	s_nop 0
	v_pk_fma_f32 v[166:167], v[100:101], v[166:167], v[170:171] op_sel:[0,1,0]
	s_nop 0
	v_pk_fma_f32 v[166:167], v[8:9], v[168:169], v[166:167] op_sel_hi:[1,0,1]
	v_mov_b32_e32 v168, v169
	v_pk_fma_f32 v[170:171], v[98:99], v[168:169], v[166:167] op_sel_hi:[1,0,1]
	ds_read_b128 v[166:169], v165
	v_add_u32_e32 v165, 0x10880, v184
	s_waitcnt lgkmcnt(0)
	v_pk_fma_f32 v[170:171], v[10:11], v[166:167], v[170:171] op_sel_hi:[1,0,1]
	s_nop 0
	v_pk_fma_f32 v[166:167], v[104:105], v[166:167], v[170:171] op_sel:[0,1,0]
	s_nop 0
	v_pk_fma_f32 v[166:167], v[12:13], v[168:169], v[166:167] op_sel_hi:[1,0,1]
	v_mov_b32_e32 v168, v169
	v_pk_fma_f32 v[170:171], v[102:103], v[168:169], v[166:167] op_sel_hi:[1,0,1]
	ds_read_b128 v[166:169], v165
	v_add_u32_e32 v165, 0x10c80, v184
	s_waitcnt lgkmcnt(0)
	v_pk_fma_f32 v[170:171], v[126:127], v[166:167], v[170:171] op_sel_hi:[1,0,1]
	s_nop 0
	v_pk_fma_f32 v[166:167], v[108:109], v[166:167], v[170:171] op_sel:[0,1,0]
	s_nop 0
	v_pk_fma_f32 v[166:167], v[128:129], v[168:169], v[166:167] op_sel_hi:[1,0,1]
	v_mov_b32_e32 v168, v169
	v_pk_fma_f32 v[170:171], v[106:107], v[168:169], v[166:167] op_sel_hi:[1,0,1]
	ds_read_b128 v[166:169], v165
	v_add_u32_e32 v165, 0x11080, v184
	s_waitcnt lgkmcnt(0)
	v_pk_fma_f32 v[170:171], v[130:131], v[166:167], v[170:171] op_sel_hi:[1,0,1]
	s_nop 0
	v_pk_fma_f32 v[166:167], v[112:113], v[166:167], v[170:171] op_sel:[0,1,0]
	s_nop 0
	v_pk_fma_f32 v[166:167], v[132:133], v[168:169], v[166:167] op_sel_hi:[1,0,1]
	v_mov_b32_e32 v168, v169
	v_pk_fma_f32 v[170:171], v[110:111], v[168:169], v[166:167] op_sel_hi:[1,0,1]
	ds_read_b128 v[166:169], v165
	v_add_u32_e32 v165, 0x11480, v184
	s_waitcnt lgkmcnt(0)
	v_pk_fma_f32 v[170:171], v[134:135], v[166:167], v[170:171] op_sel_hi:[1,0,1]
	s_nop 0
	v_pk_fma_f32 v[166:167], v[116:117], v[166:167], v[170:171] op_sel:[0,1,0]
	s_nop 0
	v_pk_fma_f32 v[166:167], v[136:137], v[168:169], v[166:167] op_sel_hi:[1,0,1]
	v_mov_b32_e32 v168, v169
	v_pk_fma_f32 v[170:171], v[114:115], v[168:169], v[166:167] op_sel_hi:[1,0,1]
	ds_read_b128 v[166:169], v165
	v_add_u32_e32 v165, 0x11880, v184
	s_waitcnt lgkmcnt(0)
	v_pk_fma_f32 v[170:171], v[138:139], v[166:167], v[170:171] op_sel_hi:[1,0,1]
	s_nop 0
	v_pk_fma_f32 v[166:167], v[120:121], v[166:167], v[170:171] op_sel:[0,1,0]
	s_nop 0
	v_pk_fma_f32 v[166:167], v[140:141], v[168:169], v[166:167] op_sel_hi:[1,0,1]
	v_mov_b32_e32 v168, v169
	v_pk_fma_f32 v[170:171], v[118:119], v[168:169], v[166:167] op_sel_hi:[1,0,1]
	ds_read_b128 v[166:169], v165
	v_add_u32_e32 v165, 0x11c80, v184
	s_waitcnt lgkmcnt(0)
	v_pk_fma_f32 v[170:171], v[142:143], v[166:167], v[170:171] op_sel_hi:[1,0,1]
	s_nop 0
	v_pk_fma_f32 v[166:167], v[124:125], v[166:167], v[170:171] op_sel:[0,1,0]
	s_nop 0
	v_pk_fma_f32 v[166:167], v[144:145], v[168:169], v[166:167] op_sel_hi:[1,0,1]
	v_mov_b32_e32 v168, v169
	v_pk_fma_f32 v[170:171], v[122:123], v[168:169], v[166:167] op_sel_hi:[1,0,1]
	ds_read_b128 v[166:169], v165
	s_waitcnt lgkmcnt(0)
	v_pk_fma_f32 v[170:171], v[148:149], v[166:167], v[170:171] op_sel_hi:[1,0,1]
	s_nop 0
	v_pk_fma_f32 v[166:167], v[2:3], v[166:167], v[170:171] op_sel:[0,1,0]
	s_nop 0
	v_pk_fma_f32 v[166:167], v[150:151], v[168:169], v[166:167] op_sel_hi:[1,0,1]
	v_mov_b32_e32 v168, v169
	v_pk_fma_f32 v[166:167], v[4:5], v[168:169], v[166:167] op_sel_hi:[1,0,1]
	s_nop 0
	v_mov_b32_e32 v165, v167
	v_add_u32_e32 v167, 0x12090, v184
	ds_read_b128 v[168:171], v167
	v_add_u32_e32 v167, 0x12490, v184
	s_waitcnt lgkmcnt(0)
	v_pk_fma_f32 v[172:173], v[6:7], v[168:169], 0 op_sel_hi:[1,0,0]
	s_nop 0
	v_pk_fma_f32 v[168:169], v[100:101], v[168:169], v[172:173] op_sel:[0,1,0]
	s_nop 0
	v_pk_fma_f32 v[168:169], v[8:9], v[170:171], v[168:169] op_sel_hi:[1,0,1]
	v_mov_b32_e32 v170, v171
	v_pk_fma_f32 v[172:173], v[98:99], v[170:171], v[168:169] op_sel_hi:[1,0,1]
	ds_read_b128 v[168:171], v167
	v_add_u32_e32 v167, 0x12890, v184
	s_waitcnt lgkmcnt(0)
	v_pk_fma_f32 v[172:173], v[10:11], v[168:169], v[172:173] op_sel_hi:[1,0,1]
	s_nop 0
	v_pk_fma_f32 v[168:169], v[104:105], v[168:169], v[172:173] op_sel:[0,1,0]
	s_nop 0
	v_pk_fma_f32 v[168:169], v[12:13], v[170:171], v[168:169] op_sel_hi:[1,0,1]
	v_mov_b32_e32 v170, v171
	v_pk_fma_f32 v[172:173], v[102:103], v[170:171], v[168:169] op_sel_hi:[1,0,1]
	ds_read_b128 v[168:171], v167
	v_add_u32_e32 v167, 0x12c90, v184
	s_waitcnt lgkmcnt(0)
	v_pk_fma_f32 v[172:173], v[126:127], v[168:169], v[172:173] op_sel_hi:[1,0,1]
	s_nop 0
	v_pk_fma_f32 v[168:169], v[108:109], v[168:169], v[172:173] op_sel:[0,1,0]
	s_nop 0
	v_pk_fma_f32 v[168:169], v[128:129], v[170:171], v[168:169] op_sel_hi:[1,0,1]
	v_mov_b32_e32 v170, v171
	v_pk_fma_f32 v[172:173], v[106:107], v[170:171], v[168:169] op_sel_hi:[1,0,1]
	ds_read_b128 v[168:171], v167
	v_add_u32_e32 v167, 0x13090, v184
	s_waitcnt lgkmcnt(0)
	v_pk_fma_f32 v[172:173], v[130:131], v[168:169], v[172:173] op_sel_hi:[1,0,1]
	s_nop 0
	v_pk_fma_f32 v[168:169], v[112:113], v[168:169], v[172:173] op_sel:[0,1,0]
	s_nop 0
	v_pk_fma_f32 v[168:169], v[132:133], v[170:171], v[168:169] op_sel_hi:[1,0,1]
	v_mov_b32_e32 v170, v171
	v_pk_fma_f32 v[172:173], v[110:111], v[170:171], v[168:169] op_sel_hi:[1,0,1]
	ds_read_b128 v[168:171], v167
	v_add_u32_e32 v167, 0x13490, v184
	s_waitcnt lgkmcnt(0)
	v_pk_fma_f32 v[172:173], v[134:135], v[168:169], v[172:173] op_sel_hi:[1,0,1]
	s_nop 0
	v_pk_fma_f32 v[168:169], v[116:117], v[168:169], v[172:173] op_sel:[0,1,0]
	s_nop 0
	v_pk_fma_f32 v[168:169], v[136:137], v[170:171], v[168:169] op_sel_hi:[1,0,1]
	v_mov_b32_e32 v170, v171
	v_pk_fma_f32 v[172:173], v[114:115], v[170:171], v[168:169] op_sel_hi:[1,0,1]
	ds_read_b128 v[168:171], v167
	v_add_u32_e32 v167, 0x13890, v184
	s_waitcnt lgkmcnt(0)
	v_pk_fma_f32 v[172:173], v[138:139], v[168:169], v[172:173] op_sel_hi:[1,0,1]
	s_nop 0
	v_pk_fma_f32 v[168:169], v[120:121], v[168:169], v[172:173] op_sel:[0,1,0]
	s_nop 0
	v_pk_fma_f32 v[168:169], v[140:141], v[170:171], v[168:169] op_sel_hi:[1,0,1]
	v_mov_b32_e32 v170, v171
	v_pk_fma_f32 v[172:173], v[118:119], v[170:171], v[168:169] op_sel_hi:[1,0,1]
	ds_read_b128 v[168:171], v167
	v_add_u32_e32 v167, 0x13c90, v184
	s_waitcnt lgkmcnt(0)
	v_pk_fma_f32 v[172:173], v[142:143], v[168:169], v[172:173] op_sel_hi:[1,0,1]
	s_nop 0
	v_pk_fma_f32 v[168:169], v[124:125], v[168:169], v[172:173] op_sel:[0,1,0]
	s_nop 0
	v_pk_fma_f32 v[168:169], v[144:145], v[170:171], v[168:169] op_sel_hi:[1,0,1]
	v_mov_b32_e32 v170, v171
	v_pk_fma_f32 v[172:173], v[122:123], v[170:171], v[168:169] op_sel_hi:[1,0,1]
	ds_read_b128 v[168:171], v167
	s_waitcnt lgkmcnt(0)
	v_pk_fma_f32 v[172:173], v[148:149], v[168:169], v[172:173] op_sel_hi:[1,0,1]
	s_nop 0
	v_pk_fma_f32 v[168:169], v[2:3], v[168:169], v[172:173] op_sel:[0,1,0]
	s_nop 0
	v_pk_fma_f32 v[168:169], v[150:151], v[170:171], v[168:169] op_sel_hi:[1,0,1]
	v_mov_b32_e32 v170, v171
	v_pk_fma_f32 v[168:169], v[4:5], v[170:171], v[168:169] op_sel_hi:[1,0,1]
	s_nop 0
	v_mov_b32_e32 v167, v169
	v_add_u32_e32 v169, 0x140a0, v184
	ds_read_b128 v[170:173], v169
	s_waitcnt lgkmcnt(0)
	v_pk_fma_f32 v[174:175], v[6:7], v[170:171], 0 op_sel_hi:[1,0,0]
	s_nop 0
	v_pk_fma_f32 v[170:171], v[100:101], v[170:171], v[174:175] op_sel:[0,1,0]
	s_nop 0
	v_pk_fma_f32 v[170:171], v[8:9], v[172:173], v[170:171] op_sel_hi:[1,0,1]
	v_mov_b32_e32 v172, v173
	v_pk_fma_f32 v[174:175], v[98:99], v[172:173], v[170:171] op_sel_hi:[1,0,1]
	ds_read_b128 v[170:173], v193 offset:17568
	s_waitcnt lgkmcnt(0)
	v_pk_fma_f32 v[174:175], v[10:11], v[170:171], v[174:175] op_sel_hi:[1,0,1]
	s_nop 0
	v_pk_fma_f32 v[170:171], v[104:105], v[170:171], v[174:175] op_sel:[0,1,0]
	s_nop 0
	v_pk_fma_f32 v[170:171], v[12:13], v[172:173], v[170:171] op_sel_hi:[1,0,1]
	v_mov_b32_e32 v172, v173
	v_pk_fma_f32 v[174:175], v[102:103], v[172:173], v[170:171] op_sel_hi:[1,0,1]
	ds_read_b128 v[170:173], v193 offset:18592
	s_waitcnt lgkmcnt(0)
	v_pk_fma_f32 v[174:175], v[126:127], v[170:171], v[174:175] op_sel_hi:[1,0,1]
	s_nop 0
	v_pk_fma_f32 v[170:171], v[108:109], v[170:171], v[174:175] op_sel:[0,1,0]
	s_nop 0
	v_pk_fma_f32 v[170:171], v[128:129], v[172:173], v[170:171] op_sel_hi:[1,0,1]
	v_mov_b32_e32 v172, v173
	v_pk_fma_f32 v[174:175], v[106:107], v[172:173], v[170:171] op_sel_hi:[1,0,1]
	ds_read_b128 v[170:173], v193 offset:19616
	s_waitcnt lgkmcnt(0)
	v_pk_fma_f32 v[174:175], v[130:131], v[170:171], v[174:175] op_sel_hi:[1,0,1]
	s_nop 0
	v_pk_fma_f32 v[170:171], v[112:113], v[170:171], v[174:175] op_sel:[0,1,0]
	s_nop 0
	v_pk_fma_f32 v[170:171], v[132:133], v[172:173], v[170:171] op_sel_hi:[1,0,1]
	v_mov_b32_e32 v172, v173
	v_pk_fma_f32 v[174:175], v[110:111], v[172:173], v[170:171] op_sel_hi:[1,0,1]
	ds_read_b128 v[170:173], v193 offset:20640
	s_waitcnt lgkmcnt(0)
	v_pk_fma_f32 v[174:175], v[134:135], v[170:171], v[174:175] op_sel_hi:[1,0,1]
	s_nop 0
	v_pk_fma_f32 v[170:171], v[116:117], v[170:171], v[174:175] op_sel:[0,1,0]
	s_nop 0
	v_pk_fma_f32 v[170:171], v[136:137], v[172:173], v[170:171] op_sel_hi:[1,0,1]
	v_mov_b32_e32 v172, v173
	v_pk_fma_f32 v[174:175], v[114:115], v[172:173], v[170:171] op_sel_hi:[1,0,1]
	ds_read_b128 v[170:173], v193 offset:21664
	s_waitcnt lgkmcnt(0)
	v_pk_fma_f32 v[174:175], v[138:139], v[170:171], v[174:175] op_sel_hi:[1,0,1]
	s_nop 0
	v_pk_fma_f32 v[170:171], v[120:121], v[170:171], v[174:175] op_sel:[0,1,0]
	s_nop 0
	v_pk_fma_f32 v[170:171], v[140:141], v[172:173], v[170:171] op_sel_hi:[1,0,1]
	v_mov_b32_e32 v172, v173
	v_pk_fma_f32 v[174:175], v[118:119], v[172:173], v[170:171] op_sel_hi:[1,0,1]
	ds_read_b128 v[170:173], v193 offset:22688
	s_waitcnt lgkmcnt(0)
	v_pk_fma_f32 v[174:175], v[142:143], v[170:171], v[174:175] op_sel_hi:[1,0,1]
	s_nop 0
	v_pk_fma_f32 v[170:171], v[124:125], v[170:171], v[174:175] op_sel:[0,1,0]
	s_nop 0
	v_pk_fma_f32 v[170:171], v[144:145], v[172:173], v[170:171] op_sel_hi:[1,0,1]
	v_mov_b32_e32 v172, v173
	v_pk_fma_f32 v[174:175], v[122:123], v[172:173], v[170:171] op_sel_hi:[1,0,1]
	ds_read_b128 v[170:173], v193 offset:23712
	s_waitcnt lgkmcnt(0)
	v_pk_fma_f32 v[174:175], v[148:149], v[170:171], v[174:175] op_sel_hi:[1,0,1]
	s_nop 0
	v_pk_fma_f32 v[170:171], v[2:3], v[170:171], v[174:175] op_sel:[0,1,0]
	s_nop 0
	v_pk_fma_f32 v[170:171], v[150:151], v[172:173], v[170:171] op_sel_hi:[1,0,1]
	v_mov_b32_e32 v172, v173
	v_pk_fma_f32 v[170:171], v[4:5], v[172:173], v[170:171] op_sel_hi:[1,0,1]
	s_nop 0
	v_mov_b32_e32 v169, v171
	ds_read_b128 v[172:175], v193 offset:24752
	s_waitcnt lgkmcnt(0)
	v_pk_fma_f32 v[176:177], v[6:7], v[172:173], 0 op_sel_hi:[1,0,0]
	s_nop 0
	v_pk_fma_f32 v[172:173], v[100:101], v[172:173], v[176:177] op_sel:[0,1,0]
	s_nop 0
	v_pk_fma_f32 v[172:173], v[8:9], v[174:175], v[172:173] op_sel_hi:[1,0,1]
	v_mov_b32_e32 v174, v175
	v_pk_fma_f32 v[176:177], v[98:99], v[174:175], v[172:173] op_sel_hi:[1,0,1]
	ds_read_b128 v[172:175], v193 offset:25776
	s_waitcnt lgkmcnt(0)
	v_pk_fma_f32 v[176:177], v[10:11], v[172:173], v[176:177] op_sel_hi:[1,0,1]
	s_nop 0
	v_pk_fma_f32 v[172:173], v[104:105], v[172:173], v[176:177] op_sel:[0,1,0]
	s_nop 0
	v_pk_fma_f32 v[172:173], v[12:13], v[174:175], v[172:173] op_sel_hi:[1,0,1]
	v_mov_b32_e32 v174, v175
	v_pk_fma_f32 v[176:177], v[102:103], v[174:175], v[172:173] op_sel_hi:[1,0,1]
	ds_read_b128 v[172:175], v193 offset:26800
	s_waitcnt lgkmcnt(0)
	v_pk_fma_f32 v[176:177], v[126:127], v[172:173], v[176:177] op_sel_hi:[1,0,1]
	s_nop 0
	v_pk_fma_f32 v[172:173], v[108:109], v[172:173], v[176:177] op_sel:[0,1,0]
	s_nop 0
	v_pk_fma_f32 v[172:173], v[128:129], v[174:175], v[172:173] op_sel_hi:[1,0,1]
	v_mov_b32_e32 v174, v175
	v_pk_fma_f32 v[176:177], v[106:107], v[174:175], v[172:173] op_sel_hi:[1,0,1]
	ds_read_b128 v[172:175], v193 offset:27824
	s_waitcnt lgkmcnt(0)
	v_pk_fma_f32 v[176:177], v[130:131], v[172:173], v[176:177] op_sel_hi:[1,0,1]
	s_nop 0
	v_pk_fma_f32 v[172:173], v[112:113], v[172:173], v[176:177] op_sel:[0,1,0]
	s_nop 0
	v_pk_fma_f32 v[172:173], v[132:133], v[174:175], v[172:173] op_sel_hi:[1,0,1]
	v_mov_b32_e32 v174, v175
	v_pk_fma_f32 v[176:177], v[110:111], v[174:175], v[172:173] op_sel_hi:[1,0,1]
	ds_read_b128 v[172:175], v193 offset:28848
	s_waitcnt lgkmcnt(0)
	v_pk_fma_f32 v[176:177], v[134:135], v[172:173], v[176:177] op_sel_hi:[1,0,1]
	s_nop 0
	v_pk_fma_f32 v[172:173], v[116:117], v[172:173], v[176:177] op_sel:[0,1,0]
	s_nop 0
	v_pk_fma_f32 v[172:173], v[136:137], v[174:175], v[172:173] op_sel_hi:[1,0,1]
	v_mov_b32_e32 v174, v175
	v_pk_fma_f32 v[176:177], v[114:115], v[174:175], v[172:173] op_sel_hi:[1,0,1]
	ds_read_b128 v[172:175], v193 offset:29872
	s_waitcnt lgkmcnt(0)
	v_pk_fma_f32 v[176:177], v[138:139], v[172:173], v[176:177] op_sel_hi:[1,0,1]
	s_nop 0
	v_pk_fma_f32 v[172:173], v[120:121], v[172:173], v[176:177] op_sel:[0,1,0]
	s_nop 0
	v_pk_fma_f32 v[172:173], v[140:141], v[174:175], v[172:173] op_sel_hi:[1,0,1]
	v_mov_b32_e32 v174, v175
	v_pk_fma_f32 v[176:177], v[118:119], v[174:175], v[172:173] op_sel_hi:[1,0,1]
	ds_read_b128 v[172:175], v193 offset:30896
	s_waitcnt lgkmcnt(0)
	v_pk_fma_f32 v[176:177], v[142:143], v[172:173], v[176:177] op_sel_hi:[1,0,1]
	s_nop 0
	v_pk_fma_f32 v[172:173], v[124:125], v[172:173], v[176:177] op_sel:[0,1,0]
	s_nop 0
	v_pk_fma_f32 v[172:173], v[144:145], v[174:175], v[172:173] op_sel_hi:[1,0,1]
	v_mov_b32_e32 v174, v175
	v_pk_fma_f32 v[176:177], v[122:123], v[174:175], v[172:173] op_sel_hi:[1,0,1]
	ds_read_b128 v[172:175], v193 offset:31920
	s_waitcnt lgkmcnt(0)
	v_pk_fma_f32 v[176:177], v[148:149], v[172:173], v[176:177] op_sel_hi:[1,0,1]
	s_nop 0
	v_pk_fma_f32 v[172:173], v[2:3], v[172:173], v[176:177] op_sel:[0,1,0]
	s_nop 0
	v_pk_fma_f32 v[172:173], v[150:151], v[174:175], v[172:173] op_sel_hi:[1,0,1]
	v_mov_b32_e32 v174, v175
	v_pk_fma_f32 v[172:173], v[4:5], v[174:175], v[172:173] op_sel_hi:[1,0,1]
	s_nop 0
	v_mov_b32_e32 v171, v173
	ds_read_b128 v[174:177], v193 offset:32960
	s_waitcnt lgkmcnt(0)
	v_pk_fma_f32 v[178:179], v[6:7], v[174:175], 0 op_sel_hi:[1,0,0]
	s_nop 0
	v_pk_fma_f32 v[174:175], v[100:101], v[174:175], v[178:179] op_sel:[0,1,0]
	s_nop 0
	v_pk_fma_f32 v[174:175], v[8:9], v[176:177], v[174:175] op_sel_hi:[1,0,1]
	v_mov_b32_e32 v176, v177
	v_pk_fma_f32 v[178:179], v[98:99], v[176:177], v[174:175] op_sel_hi:[1,0,1]
	ds_read_b128 v[174:177], v193 offset:33984
	s_waitcnt lgkmcnt(0)
	v_pk_fma_f32 v[178:179], v[10:11], v[174:175], v[178:179] op_sel_hi:[1,0,1]
	s_nop 0
	v_pk_fma_f32 v[174:175], v[104:105], v[174:175], v[178:179] op_sel:[0,1,0]
	s_nop 0
	v_pk_fma_f32 v[174:175], v[12:13], v[176:177], v[174:175] op_sel_hi:[1,0,1]
	v_mov_b32_e32 v176, v177
	v_pk_fma_f32 v[178:179], v[102:103], v[176:177], v[174:175] op_sel_hi:[1,0,1]
	ds_read_b128 v[174:177], v193 offset:35008
	s_waitcnt lgkmcnt(0)
	v_pk_fma_f32 v[178:179], v[126:127], v[174:175], v[178:179] op_sel_hi:[1,0,1]
	s_nop 0
	v_pk_fma_f32 v[174:175], v[108:109], v[174:175], v[178:179] op_sel:[0,1,0]
	s_nop 0
	v_pk_fma_f32 v[174:175], v[128:129], v[176:177], v[174:175] op_sel_hi:[1,0,1]
	v_mov_b32_e32 v176, v177
	v_pk_fma_f32 v[178:179], v[106:107], v[176:177], v[174:175] op_sel_hi:[1,0,1]
	ds_read_b128 v[174:177], v193 offset:36032
	s_waitcnt lgkmcnt(0)
	v_pk_fma_f32 v[178:179], v[130:131], v[174:175], v[178:179] op_sel_hi:[1,0,1]
	s_nop 0
	v_pk_fma_f32 v[174:175], v[112:113], v[174:175], v[178:179] op_sel:[0,1,0]
	s_nop 0
	v_pk_fma_f32 v[174:175], v[132:133], v[176:177], v[174:175] op_sel_hi:[1,0,1]
	v_mov_b32_e32 v176, v177
	v_pk_fma_f32 v[178:179], v[110:111], v[176:177], v[174:175] op_sel_hi:[1,0,1]
	ds_read_b128 v[174:177], v193 offset:37056
	s_waitcnt lgkmcnt(0)
	v_pk_fma_f32 v[178:179], v[134:135], v[174:175], v[178:179] op_sel_hi:[1,0,1]
	s_nop 0
	v_pk_fma_f32 v[174:175], v[116:117], v[174:175], v[178:179] op_sel:[0,1,0]
	s_nop 0
	v_pk_fma_f32 v[174:175], v[136:137], v[176:177], v[174:175] op_sel_hi:[1,0,1]
	v_mov_b32_e32 v176, v177
	v_pk_fma_f32 v[178:179], v[114:115], v[176:177], v[174:175] op_sel_hi:[1,0,1]
	ds_read_b128 v[174:177], v193 offset:38080
	s_waitcnt lgkmcnt(0)
	v_pk_fma_f32 v[178:179], v[138:139], v[174:175], v[178:179] op_sel_hi:[1,0,1]
	s_nop 0
	v_pk_fma_f32 v[174:175], v[120:121], v[174:175], v[178:179] op_sel:[0,1,0]
	s_nop 0
	v_pk_fma_f32 v[174:175], v[140:141], v[176:177], v[174:175] op_sel_hi:[1,0,1]
	v_mov_b32_e32 v176, v177
	v_pk_fma_f32 v[178:179], v[118:119], v[176:177], v[174:175] op_sel_hi:[1,0,1]
	ds_read_b128 v[174:177], v193 offset:39104
	s_waitcnt lgkmcnt(0)
	v_pk_fma_f32 v[178:179], v[142:143], v[174:175], v[178:179] op_sel_hi:[1,0,1]
	s_nop 0
	v_pk_fma_f32 v[174:175], v[124:125], v[174:175], v[178:179] op_sel:[0,1,0]
	s_nop 0
	v_pk_fma_f32 v[174:175], v[144:145], v[176:177], v[174:175] op_sel_hi:[1,0,1]
	v_mov_b32_e32 v176, v177
	v_pk_fma_f32 v[178:179], v[122:123], v[176:177], v[174:175] op_sel_hi:[1,0,1]
	ds_read_b128 v[174:177], v193 offset:40128
	s_waitcnt lgkmcnt(0)
	v_pk_fma_f32 v[178:179], v[148:149], v[174:175], v[178:179] op_sel_hi:[1,0,1]
	s_nop 0
	v_pk_fma_f32 v[174:175], v[2:3], v[174:175], v[178:179] op_sel:[0,1,0]
	s_nop 0
	v_pk_fma_f32 v[174:175], v[150:151], v[176:177], v[174:175] op_sel_hi:[1,0,1]
	v_mov_b32_e32 v176, v177
	v_pk_fma_f32 v[174:175], v[4:5], v[176:177], v[174:175] op_sel_hi:[1,0,1]
	s_nop 0
	v_mov_b32_e32 v173, v175
	ds_read_b128 v[176:179], v193 offset:41168
	s_waitcnt lgkmcnt(0)
	v_pk_fma_f32 v[252:253], v[6:7], v[176:177], 0 op_sel_hi:[1,0,0]
	s_nop 0
	v_pk_fma_f32 v[176:177], v[100:101], v[176:177], v[252:253] op_sel:[0,1,0]
	s_nop 0
	v_pk_fma_f32 v[176:177], v[8:9], v[178:179], v[176:177] op_sel_hi:[1,0,1]
	v_mov_b32_e32 v178, v179
	v_pk_fma_f32 v[252:253], v[98:99], v[178:179], v[176:177] op_sel_hi:[1,0,1]
	ds_read_b128 v[176:179], v193 offset:42192
	s_waitcnt lgkmcnt(0)
	v_pk_fma_f32 v[252:253], v[10:11], v[176:177], v[252:253] op_sel_hi:[1,0,1]
	s_nop 0
	v_pk_fma_f32 v[176:177], v[104:105], v[176:177], v[252:253] op_sel:[0,1,0]
	s_nop 0
	v_pk_fma_f32 v[176:177], v[12:13], v[178:179], v[176:177] op_sel_hi:[1,0,1]
	v_mov_b32_e32 v178, v179
	v_pk_fma_f32 v[252:253], v[102:103], v[178:179], v[176:177] op_sel_hi:[1,0,1]
	ds_read_b128 v[176:179], v193 offset:43216
	s_waitcnt lgkmcnt(0)
	v_pk_fma_f32 v[252:253], v[126:127], v[176:177], v[252:253] op_sel_hi:[1,0,1]
	s_nop 0
	v_pk_fma_f32 v[176:177], v[108:109], v[176:177], v[252:253] op_sel:[0,1,0]
	s_nop 0
	v_pk_fma_f32 v[176:177], v[128:129], v[178:179], v[176:177] op_sel_hi:[1,0,1]
	v_mov_b32_e32 v178, v179
	v_pk_fma_f32 v[252:253], v[106:107], v[178:179], v[176:177] op_sel_hi:[1,0,1]
	ds_read_b128 v[176:179], v193 offset:44240
	s_waitcnt lgkmcnt(0)
	v_pk_fma_f32 v[252:253], v[130:131], v[176:177], v[252:253] op_sel_hi:[1,0,1]
	s_nop 0
	v_pk_fma_f32 v[176:177], v[112:113], v[176:177], v[252:253] op_sel:[0,1,0]
	s_nop 0
	v_pk_fma_f32 v[176:177], v[132:133], v[178:179], v[176:177] op_sel_hi:[1,0,1]
	v_mov_b32_e32 v178, v179
	v_pk_fma_f32 v[252:253], v[110:111], v[178:179], v[176:177] op_sel_hi:[1,0,1]
	ds_read_b128 v[176:179], v193 offset:45264
	s_waitcnt lgkmcnt(0)
	v_pk_fma_f32 v[252:253], v[134:135], v[176:177], v[252:253] op_sel_hi:[1,0,1]
	s_nop 0
	v_pk_fma_f32 v[176:177], v[116:117], v[176:177], v[252:253] op_sel:[0,1,0]
	s_nop 0
	v_pk_fma_f32 v[176:177], v[136:137], v[178:179], v[176:177] op_sel_hi:[1,0,1]
	v_mov_b32_e32 v178, v179
	v_pk_fma_f32 v[252:253], v[114:115], v[178:179], v[176:177] op_sel_hi:[1,0,1]
	ds_read_b128 v[176:179], v193 offset:46288
	s_waitcnt lgkmcnt(0)
	v_pk_fma_f32 v[252:253], v[138:139], v[176:177], v[252:253] op_sel_hi:[1,0,1]
	s_nop 0
	v_pk_fma_f32 v[176:177], v[120:121], v[176:177], v[252:253] op_sel:[0,1,0]
	s_nop 0
	v_pk_fma_f32 v[176:177], v[140:141], v[178:179], v[176:177] op_sel_hi:[1,0,1]
	v_mov_b32_e32 v178, v179
	v_pk_fma_f32 v[252:253], v[118:119], v[178:179], v[176:177] op_sel_hi:[1,0,1]
	ds_read_b128 v[176:179], v193 offset:47312
	s_waitcnt lgkmcnt(0)
	v_pk_fma_f32 v[252:253], v[142:143], v[176:177], v[252:253] op_sel_hi:[1,0,1]
	s_nop 0
	v_pk_fma_f32 v[176:177], v[124:125], v[176:177], v[252:253] op_sel:[0,1,0]
	s_nop 0
	v_pk_fma_f32 v[176:177], v[144:145], v[178:179], v[176:177] op_sel_hi:[1,0,1]
	v_mov_b32_e32 v178, v179
	v_pk_fma_f32 v[252:253], v[122:123], v[178:179], v[176:177] op_sel_hi:[1,0,1]
	ds_read_b128 v[176:179], v193 offset:48336
	s_waitcnt lgkmcnt(0)
	v_pk_fma_f32 v[252:253], v[148:149], v[176:177], v[252:253] op_sel_hi:[1,0,1]
	s_nop 0
	v_pk_fma_f32 v[176:177], v[2:3], v[176:177], v[252:253] op_sel:[0,1,0]
	s_nop 0
	v_pk_fma_f32 v[176:177], v[150:151], v[178:179], v[176:177] op_sel_hi:[1,0,1]
	v_mov_b32_e32 v178, v179
	v_pk_fma_f32 v[176:177], v[4:5], v[178:179], v[176:177] op_sel_hi:[1,0,1]
	s_nop 0
	v_mov_b32_e32 v175, v177
	ds_read_b128 v[252:255], v193 offset:49376
	s_waitcnt lgkmcnt(0)
	v_pk_fma_f32 v[178:179], v[6:7], v[252:253], 0 op_sel_hi:[1,0,0]
	s_nop 0
	v_pk_fma_f32 v[178:179], v[100:101], v[252:253], v[178:179] op_sel:[0,1,0]
	v_mov_b32_e32 v252, v255
	v_pk_fma_f32 v[178:179], v[8:9], v[254:255], v[178:179] op_sel_hi:[1,0,1]
	s_nop 0
	v_pk_fma_f32 v[178:179], v[98:99], v[252:253], v[178:179] op_sel_hi:[1,0,1]
	ds_read_b128 v[252:255], v193 offset:50400
	s_waitcnt lgkmcnt(0)
	v_pk_fma_f32 v[178:179], v[10:11], v[252:253], v[178:179] op_sel_hi:[1,0,1]
	s_nop 0
	v_pk_fma_f32 v[178:179], v[104:105], v[252:253], v[178:179] op_sel:[0,1,0]
	v_mov_b32_e32 v252, v255
	v_pk_fma_f32 v[178:179], v[12:13], v[254:255], v[178:179] op_sel_hi:[1,0,1]
	s_nop 0
	v_pk_fma_f32 v[178:179], v[102:103], v[252:253], v[178:179] op_sel_hi:[1,0,1]
	ds_read_b128 v[252:255], v193 offset:51424
	s_waitcnt lgkmcnt(0)
	v_pk_fma_f32 v[178:179], v[126:127], v[252:253], v[178:179] op_sel_hi:[1,0,1]
	s_nop 0
	v_pk_fma_f32 v[178:179], v[108:109], v[252:253], v[178:179] op_sel:[0,1,0]
	v_mov_b32_e32 v252, v255
	v_pk_fma_f32 v[178:179], v[128:129], v[254:255], v[178:179] op_sel_hi:[1,0,1]
	s_nop 0
	v_pk_fma_f32 v[178:179], v[106:107], v[252:253], v[178:179] op_sel_hi:[1,0,1]
	ds_read_b128 v[252:255], v193 offset:52448
	s_waitcnt lgkmcnt(0)
	v_pk_fma_f32 v[178:179], v[130:131], v[252:253], v[178:179] op_sel_hi:[1,0,1]
	s_nop 0
	v_pk_fma_f32 v[178:179], v[112:113], v[252:253], v[178:179] op_sel:[0,1,0]
	v_mov_b32_e32 v252, v255
	v_pk_fma_f32 v[178:179], v[132:133], v[254:255], v[178:179] op_sel_hi:[1,0,1]
	s_nop 0
	v_pk_fma_f32 v[178:179], v[110:111], v[252:253], v[178:179] op_sel_hi:[1,0,1]
	ds_read_b128 v[252:255], v193 offset:53472
	s_waitcnt lgkmcnt(0)
	v_pk_fma_f32 v[178:179], v[134:135], v[252:253], v[178:179] op_sel_hi:[1,0,1]
	s_nop 0
	v_pk_fma_f32 v[178:179], v[116:117], v[252:253], v[178:179] op_sel:[0,1,0]
	v_mov_b32_e32 v252, v255
	v_pk_fma_f32 v[178:179], v[136:137], v[254:255], v[178:179] op_sel_hi:[1,0,1]
	s_nop 0
	v_pk_fma_f32 v[178:179], v[114:115], v[252:253], v[178:179] op_sel_hi:[1,0,1]
	ds_read_b128 v[252:255], v193 offset:54496
	s_waitcnt lgkmcnt(0)
	v_pk_fma_f32 v[178:179], v[138:139], v[252:253], v[178:179] op_sel_hi:[1,0,1]
	s_nop 0
	v_pk_fma_f32 v[178:179], v[120:121], v[252:253], v[178:179] op_sel:[0,1,0]
	v_mov_b32_e32 v252, v255
	v_pk_fma_f32 v[178:179], v[140:141], v[254:255], v[178:179] op_sel_hi:[1,0,1]
	s_nop 0
	v_pk_fma_f32 v[178:179], v[118:119], v[252:253], v[178:179] op_sel_hi:[1,0,1]
	ds_read_b128 v[252:255], v193 offset:55520
	s_waitcnt lgkmcnt(0)
	v_pk_fma_f32 v[178:179], v[142:143], v[252:253], v[178:179] op_sel_hi:[1,0,1]
	s_nop 0
	v_pk_fma_f32 v[178:179], v[124:125], v[252:253], v[178:179] op_sel:[0,1,0]
	v_mov_b32_e32 v252, v255
	v_pk_fma_f32 v[178:179], v[144:145], v[254:255], v[178:179] op_sel_hi:[1,0,1]
	s_nop 0
	v_pk_fma_f32 v[178:179], v[122:123], v[252:253], v[178:179] op_sel_hi:[1,0,1]
	ds_read_b128 v[252:255], v193 offset:56544
	s_waitcnt lgkmcnt(0)
	v_pk_fma_f32 v[178:179], v[148:149], v[252:253], v[178:179] op_sel_hi:[1,0,1]
	s_nop 0
	v_pk_fma_f32 v[178:179], v[2:3], v[252:253], v[178:179] op_sel:[0,1,0]
	v_mov_b32_e32 v252, v255
	v_pk_fma_f32 v[178:179], v[150:151], v[254:255], v[178:179] op_sel_hi:[1,0,1]
	s_nop 0
	v_pk_fma_f32 v[178:179], v[4:5], v[252:253], v[178:179] op_sel_hi:[1,0,1]
	s_nop 0
	v_mov_b32_e32 v177, v179
	ds_read_b128 v[252:255], v193 offset:57584
	s_waitcnt lgkmcnt(0)
	v_pk_fma_f32 v[6:7], v[6:7], v[252:253], 0 op_sel_hi:[1,0,0]
	s_nop 0
	v_pk_fma_f32 v[6:7], v[100:101], v[252:253], v[6:7] op_sel:[0,1,0]
	s_nop 0
	v_pk_fma_f32 v[6:7], v[8:9], v[254:255], v[6:7] op_sel_hi:[1,0,1]
	v_mov_b32_e32 v8, v255
	v_pk_fma_f32 v[98:99], v[98:99], v[8:9], v[6:7] op_sel_hi:[1,0,1]
	ds_read_b128 v[6:9], v193 offset:58608
	s_waitcnt lgkmcnt(0)
	v_pk_fma_f32 v[10:11], v[10:11], v[6:7], v[98:99] op_sel_hi:[1,0,1]
	s_nop 0
	v_pk_fma_f32 v[6:7], v[104:105], v[6:7], v[10:11] op_sel:[0,1,0]
	s_nop 0
	v_pk_fma_f32 v[6:7], v[12:13], v[8:9], v[6:7] op_sel_hi:[1,0,1]
	v_mov_b32_e32 v8, v9
	v_pk_fma_f32 v[10:11], v[102:103], v[8:9], v[6:7] op_sel_hi:[1,0,1]
	ds_read_b128 v[6:9], v193 offset:59632
	s_waitcnt lgkmcnt(0)
	v_pk_fma_f32 v[10:11], v[126:127], v[6:7], v[10:11] op_sel_hi:[1,0,1]
	s_nop 0
	v_pk_fma_f32 v[6:7], v[108:109], v[6:7], v[10:11] op_sel:[0,1,0]
	s_nop 0
	v_pk_fma_f32 v[6:7], v[128:129], v[8:9], v[6:7] op_sel_hi:[1,0,1]
	v_mov_b32_e32 v8, v9
	v_pk_fma_f32 v[10:11], v[106:107], v[8:9], v[6:7] op_sel_hi:[1,0,1]
	ds_read_b128 v[6:9], v193 offset:60656
	s_waitcnt lgkmcnt(0)
	v_pk_fma_f32 v[10:11], v[130:131], v[6:7], v[10:11] op_sel_hi:[1,0,1]
	s_nop 0
	v_pk_fma_f32 v[6:7], v[112:113], v[6:7], v[10:11] op_sel:[0,1,0]
	s_nop 0
	v_pk_fma_f32 v[6:7], v[132:133], v[8:9], v[6:7] op_sel_hi:[1,0,1]
	v_mov_b32_e32 v8, v9
	v_pk_fma_f32 v[10:11], v[110:111], v[8:9], v[6:7] op_sel_hi:[1,0,1]
	ds_read_b128 v[6:9], v193 offset:61680
	s_waitcnt lgkmcnt(0)
	v_pk_fma_f32 v[10:11], v[134:135], v[6:7], v[10:11] op_sel_hi:[1,0,1]
	s_nop 0
	v_pk_fma_f32 v[6:7], v[116:117], v[6:7], v[10:11] op_sel:[0,1,0]
	s_nop 0
	v_pk_fma_f32 v[6:7], v[136:137], v[8:9], v[6:7] op_sel_hi:[1,0,1]
	v_mov_b32_e32 v8, v9
	v_pk_fma_f32 v[10:11], v[114:115], v[8:9], v[6:7] op_sel_hi:[1,0,1]
	ds_read_b128 v[6:9], v193 offset:62704
	s_waitcnt lgkmcnt(0)
	v_pk_fma_f32 v[10:11], v[138:139], v[6:7], v[10:11] op_sel_hi:[1,0,1]
	s_nop 0
	v_pk_fma_f32 v[6:7], v[120:121], v[6:7], v[10:11] op_sel:[0,1,0]
	s_nop 0
	v_pk_fma_f32 v[6:7], v[140:141], v[8:9], v[6:7] op_sel_hi:[1,0,1]
	v_mov_b32_e32 v8, v9
	v_pk_fma_f32 v[10:11], v[118:119], v[8:9], v[6:7] op_sel_hi:[1,0,1]
	ds_read_b128 v[6:9], v193 offset:63728
	s_waitcnt lgkmcnt(0)
	v_pk_fma_f32 v[10:11], v[142:143], v[6:7], v[10:11] op_sel_hi:[1,0,1]
	s_nop 0
	v_pk_fma_f32 v[6:7], v[124:125], v[6:7], v[10:11] op_sel:[0,1,0]
	s_nop 0
	v_pk_fma_f32 v[6:7], v[144:145], v[8:9], v[6:7] op_sel_hi:[1,0,1]
	v_mov_b32_e32 v8, v9
	v_pk_fma_f32 v[10:11], v[122:123], v[8:9], v[6:7] op_sel_hi:[1,0,1]
	ds_read_b128 v[6:9], v193 offset:64752
	s_waitcnt lgkmcnt(0)
	v_pk_fma_f32 v[10:11], v[148:149], v[6:7], v[10:11] op_sel_hi:[1,0,1]
	s_nop 0
	v_pk_fma_f32 v[2:3], v[2:3], v[6:7], v[10:11] op_sel:[0,1,0]
	v_mov_b32_e32 v6, v9
	v_pk_fma_f32 v[2:3], v[150:151], v[8:9], v[2:3] op_sel_hi:[1,0,1]
	v_cndmask_b32_e64 v8, v156, v172, s[6:7]
	v_pk_fma_f32 v[4:5], v[4:5], v[6:7], v[2:3] op_sel_hi:[1,0,1]
	v_cndmask_b32_e64 v6, v152, v168, s[6:7]
	v_mov_b32_e32 v2, v5
	v_cndmask_b32_e64 v5, v146, v166, s[6:7]
	ds_bpermute_b32 v5, v183, v5
	ds_bpermute_b32 v6, v183, v6
	v_cndmask_b32_e64 v7, v154, v170, s[6:7]
	ds_bpermute_b32 v7, v183, v7
	ds_bpermute_b32 v8, v183, v8
	v_cndmask_b32_e64 v9, v158, v174, s[6:7]
	v_cndmask_b32_e64 v3, v166, v146, s[6:7]
	ds_bpermute_b32 v9, v183, v9
	v_cndmask_b32_e64 v10, v160, v176, s[6:7]
	s_waitcnt lgkmcnt(4)
	v_add_f32_e32 v3, v3, v5
	v_cndmask_b32_e64 v5, v168, v152, s[6:7]
	ds_bpermute_b32 v10, v183, v10
	v_cndmask_b32_e64 v11, v162, v178, s[6:7]
	s_waitcnt lgkmcnt(4)
	v_add_f32_e32 v5, v5, v6
	v_cndmask_b32_e64 v6, v170, v154, s[6:7]
	ds_bpermute_b32 v11, v183, v11
	s_waitcnt lgkmcnt(4)
	v_add_f32_e32 v6, v6, v7
	v_cndmask_b32_e64 v7, v172, v156, s[6:7]
	s_waitcnt lgkmcnt(3)
	v_add_f32_e32 v7, v7, v8
	v_cndmask_b32_e64 v8, v174, v158, s[6:7]
	s_waitcnt lgkmcnt(2)
	v_add_f32_e32 v8, v8, v9
	v_cndmask_b32_e64 v9, v176, v160, s[6:7]
	s_waitcnt lgkmcnt(1)
	v_add_f32_e32 v9, v9, v10
	v_cndmask_b32_e64 v10, v178, v162, s[6:7]
	s_waitcnt lgkmcnt(0)
	v_add_f32_e32 v10, v10, v11
	v_cndmask_b32_e64 v11, v4, v164, s[6:7]
	v_cndmask_b32_e64 v4, v164, v4, s[6:7]
	ds_bpermute_b32 v4, v183, v4
	s_load_dwordx2 s[14:15], s[0:1], 0xc0
	s_waitcnt lgkmcnt(0)
	v_add_f32_e32 v4, v11, v4
	v_cndmask_b32_e64 v11, v8, v3, s[8:9]
	v_cndmask_b32_e64 v3, v3, v8, s[8:9]
	v_cndmask_b32_e64 v8, v9, v5, s[8:9]
	v_cndmask_b32_e64 v5, v5, v9, s[8:9]
	ds_bpermute_b32 v5, v182, v5
	ds_bpermute_b32 v3, v182, v3
	s_waitcnt lgkmcnt(1)
	v_add_f32_e32 v5, v8, v5
	v_cndmask_b32_e64 v8, v10, v6, s[8:9]
	v_cndmask_b32_e64 v6, v6, v10, s[8:9]
	ds_bpermute_b32 v6, v182, v6
	s_waitcnt lgkmcnt(1)
	v_add_f32_e32 v3, v11, v3
	s_waitcnt lgkmcnt(0)
	v_add_f32_e32 v6, v8, v6
	v_cndmask_b32_e64 v8, v4, v7, s[8:9]
	v_cndmask_b32_e64 v4, v7, v4, s[8:9]
	ds_bpermute_b32 v4, v182, v4
	v_cndmask_b32_e64 v7, v6, v3, s[10:11]
	v_cndmask_b32_e64 v3, v3, v6, s[10:11]
	ds_bpermute_b32 v3, v181, v3
	s_waitcnt lgkmcnt(1)
	v_add_f32_e32 v4, v8, v4
	v_cndmask_b32_e64 v6, v4, v5, s[10:11]
	v_cndmask_b32_e64 v4, v5, v4, s[10:11]
	ds_bpermute_b32 v4, v181, v4
	s_waitcnt lgkmcnt(1)
	v_add_f32_e32 v3, v7, v3
	s_waitcnt lgkmcnt(0)
	v_add_f32_e32 v4, v6, v4
	v_cndmask_b32_e64 v5, v4, v3, s[12:13]
	v_cndmask_b32_e64 v3, v3, v4, s[12:13]
	ds_bpermute_b32 v3, v180, v3
	s_waitcnt lgkmcnt(0)
	v_add_f32_e32 v3, v5, v3
	ds_bpermute_b32 v4, v15, v3
	s_waitcnt lgkmcnt(0)
	v_add_f32_e32 v3, v3, v4
	ds_bpermute_b32 v4, v1, v3
	s_waitcnt lgkmcnt(0)
	v_add_f32_e32 v3, v3, v4
	v_mul_f32_e32 v3, 0xbfb8aa3b, v3
	v_exp_f32_e32 v3, v3
	s_nop 0
	v_add_f32_e32 v3, 1.0, v3
	v_div_scale_f32 v4, s[16:17], v3, v3, 1.0
	v_rcp_f32_e32 v5, v4
	s_nop 0
	v_fma_f32 v6, -v4, v5, 1.0
	v_fmac_f32_e32 v5, v6, v5
	v_div_scale_f32 v6, vcc, 1.0, v3, 1.0
	v_mul_f32_e32 v7, v6, v5
	v_fma_f32 v8, -v4, v7, v6
	v_fmac_f32_e32 v7, v8, v5
	v_fma_f32 v4, -v4, v7, v6
	v_div_fmas_f32 v4, v4, v5, v7
	v_div_fixup_f32 v4, v4, v3, 1.0
	global_load_dword v3, v249, s[14:15]
	s_waitcnt vmcnt(0)
	v_add_f32_e32 v5, v3, v4
	ds_bpermute_b32 v6, v185, v5
	ds_bpermute_b32 v7, v186, v5
	ds_bpermute_b32 v8, v187, v5
	ds_bpermute_b32 v9, v188, v5
	s_waitcnt lgkmcnt(2)
	v_add_f32_e32 v10, v6, v7
	s_waitcnt lgkmcnt(1)
	v_add_f32_e32 v11, v6, v8
	v_max_f32_e32 v10, v10, v11
	s_waitcnt lgkmcnt(0)
	v_add_f32_e32 v6, v6, v9
	v_add_f32_e32 v11, v7, v8
	v_add_f32_e32 v7, v7, v9
	v_add_f32_e32 v8, v8, v9
	v_max_f32_e32 v6, v6, v11
	v_max_f32_e32 v7, v7, v8
	v_max3_f32 v6, v10, v6, v7
	ds_bpermute_b32 v7, v189, v6
	ds_bpermute_b32 v8, v190, v6
	ds_bpermute_b32 v9, v191, v6
	ds_bpermute_b32 v6, v192, v6
	s_waitcnt lgkmcnt(2)
	v_cmp_gt_f32_e32 vcc, v8, v7
	s_nop 1
	v_cndmask_b32_e32 v7, v7, v8, vcc
	v_cndmask_b32_e64 v8, 0, 1, vcc
	s_waitcnt lgkmcnt(1)
	v_cmp_lt_f32_e32 vcc, v7, v9
	s_nop 1
	v_cndmask_b32_e32 v7, v7, v9, vcc
	v_cndmask_b32_e64 v8, v8, 2, vcc
	s_waitcnt lgkmcnt(0)
	v_cmp_nlt_f32_e32 vcc, v7, v6
	s_nop 1
	v_cndmask_b32_e32 v6, 3, v8, vcc
	v_lshl_or_b32 v7, v6, 6, v189
	ds_bpermute_b32 v98, v7, v5
	ds_bpermute_b32 v13, v7, v5 offset:16
	ds_bpermute_b32 v11, v7, v5 offset:32
	ds_bpermute_b32 v12, v7, v5 offset:48
	ds_bpermute_b32 v10, v7, v4
	ds_bpermute_b32 v5, v7, v4 offset:16
	s_waitcnt lgkmcnt(4)
	v_cmp_gt_f32_e32 vcc, v13, v98
	ds_bpermute_b32 v8, v7, v4 offset:32
	ds_bpermute_b32 v9, v7, v4 offset:48
	v_cndmask_b32_e32 v7, v98, v13, vcc
	v_cndmask_b32_e64 v4, 0, 1, vcc
	s_waitcnt lgkmcnt(5)
	v_cmp_lt_f32_e32 vcc, v7, v11
	s_nop 1
	v_cndmask_b32_e32 v7, v7, v11, vcc
	v_cndmask_b32_e64 v4, v4, 2, vcc
	s_waitcnt lgkmcnt(4)
	v_cmp_nlt_f32_e64 s[14:15], v7, v12
	s_and_b64 vcc, vcc, s[14:15]
	s_nop 0
	v_cndmask_b32_e64 v7, 3, v4, s[14:15]
	v_cmp_lt_i32_e64 s[16:17], 0, v7
	s_waitcnt lgkmcnt(3)
	v_mov_b32_e32 v4, v10
	s_and_saveexec_b64 s[18:19], s[16:17]
	s_cbranch_execz .LBB0_1705
	v_cmp_ne_u32_e64 s[16:17], 1, v7
	s_and_saveexec_b64 s[24:25], s[16:17]
	s_xor_b64 s[16:17], exec, s[24:25]
	s_cbranch_execz .LBB0_1702
	s_waitcnt lgkmcnt(0)
	v_cndmask_b32_e32 v4, v9, v8, vcc

.LBB0_3194:
	s_or_b64 exec, exec, s[4:5]
	s_waitcnt vmcnt(0) lgkmcnt(0)
	s_barrier
	s_load_dword s28, s[0:1], 0xf8
	s_ashr_i32 s18, s14, 6
	s_add_u32 s20, s0, 0xf8
	s_addc_u32 s21, s1, 0
	s_waitcnt lgkmcnt(0)
	s_abs_i32 s4, s28
	v_cvt_f32_u32_e32 v1, s4
	s_add_i32 s5, s28, 0x3fff
	s_sub_i32 s6, 0xffffc001, s28
	s_xor_b32 s7, s5, s28
	v_rcp_iflag_f32_e32 v1, v1
	s_max_i32 s5, s5, s6
	s_sub_i32 s6, 0, s4
	s_ashr_i32 s7, s7, 31
	v_mul_f32_e32 v1, 0x4f7ffffe, v1
	v_cvt_u32_f32_e32 v1, v1
	s_nop 0
	v_readfirstlane_b32 s8, v1
	s_mul_i32 s6, s6, s8
	s_mul_hi_u32 s6, s8, s6
	s_add_i32 s8, s8, s6
	s_mul_hi_u32 s6, s5, s8
	s_mul_i32 s8, s6, s4
	s_sub_i32 s5, s5, s8
	s_add_i32 s9, s6, 1
	s_sub_i32 s8, s5, s4
	s_cmp_ge_u32 s5, s4
	s_cselect_b32 s6, s9, s6
	s_cselect_b32 s5, s8, s5
	s_add_i32 s8, s6, 1
	s_cmp_ge_u32 s5, s4
	s_cselect_b32 s4, s8, s6
	s_xor_b32 s4, s4, s7
	s_sub_i32 s30, s4, s7
	s_ashr_i32 s31, s30, 1
	s_cmp_lt_i32 s18, s31
	s_mul_i32 s29, s30, s2
	s_cbranch_scc0 .LBB0_3235
	s_add_u32 s33, s40, 0x124000
	s_addc_u32 s34, s41, 0
	s_add_i32 s4, s29, s18
	s_add_u32 s14, s40, 0x21c00000
	s_addc_u32 s15, s41, 0
	s_ashr_i32 s5, s4, 31
	s_lshl_b64 s[6:7], s[4:5], 12
	s_add_u32 s8, s14, s6
	s_addc_u32 s9, s15, s7
	s_add_u32 s16, s40, 0x36600000
	s_addc_u32 s17, s41, 0
	s_add_u32 s6, s16, s6
	s_addc_u32 s7, s17, s7
	s_add_i32 s4, s4, s31
	v_and_b32_e32 v5, 63, v6
	s_ashr_i32 s5, s4, 31
	v_lshlrev_b32_e32 v2, 3, v5
	s_lshl_b64 s[4:5], s[4:5], 12
	global_load_dwordx2 v[18:19], v2, s[8:9] nt
	global_load_dwordx2 v[20:21], v2, s[8:9] offset:512 nt
	global_load_dwordx2 v[22:23], v2, s[8:9] offset:1024 nt
	global_load_dwordx2 v[24:25], v2, s[8:9] offset:1536 nt
	global_load_dwordx2 v[26:27], v2, s[6:7] nt
	global_load_dwordx2 v[28:29], v2, s[6:7] offset:512 nt
	global_load_dwordx2 v[30:31], v2, s[6:7] offset:1024 nt
	global_load_dwordx2 v[32:33], v2, s[6:7] offset:1536 nt
	global_load_dwordx2 v[34:35], v2, s[8:9] offset:2048 nt
	global_load_dwordx2 v[36:37], v2, s[8:9] offset:2560 nt
	global_load_dwordx2 v[38:39], v2, s[8:9] offset:3072 nt
	global_load_dwordx2 v[40:41], v2, s[8:9] offset:3584 nt
	global_load_dwordx2 v[42:43], v2, s[6:7] offset:2048 nt
	global_load_dwordx2 v[44:45], v2, s[6:7] offset:2560 nt
	global_load_dwordx2 v[46:47], v2, s[6:7] offset:3072 nt
	global_load_dwordx2 v[48:49], v2, s[6:7] offset:3584 nt
	s_add_u32 s6, s14, s4
	s_addc_u32 s7, s15, s5
	s_add_u32 s4, s16, s4
	s_addc_u32 s5, s17, s5
	global_load_dwordx2 v[50:51], v2, s[6:7] nt
	global_load_dwordx2 v[52:53], v2, s[6:7] offset:512 nt
	global_load_dwordx2 v[54:55], v2, s[6:7] offset:1024 nt
	global_load_dwordx2 v[56:57], v2, s[6:7] offset:1536 nt
	global_load_dwordx2 v[58:59], v2, s[4:5] nt
	global_load_dwordx2 v[60:61], v2, s[4:5] offset:512 nt
	global_load_dwordx2 v[62:63], v2, s[4:5] offset:1024 nt
	global_load_dwordx2 v[64:65], v2, s[4:5] offset:1536 nt
	global_load_dwordx2 v[66:67], v2, s[6:7] offset:2048 nt
	global_load_dwordx2 v[68:69], v2, s[6:7] offset:2560 nt
	global_load_dwordx2 v[70:71], v2, s[6:7] offset:3072 nt
	global_load_dwordx2 v[72:73], v2, s[6:7] offset:3584 nt
	global_load_dwordx2 v[74:75], v2, s[4:5] offset:2048 nt
	global_load_dwordx2 v[76:77], v2, s[4:5] offset:2560 nt
	global_load_dwordx2 v[78:79], v2, s[4:5] offset:3072 nt
	global_load_dwordx2 v[80:81], v2, s[4:5] offset:3584 nt
	v_mbcnt_lo_u32_b32 v1, -1, 0
	v_mbcnt_hi_u32_b32 v7, -1, v1
	v_and_b32_e32 v9, 64, v7
	v_add_u32_e32 v11, 64, v9
	v_xor_b32_e32 v1, 1, v7
	v_cmp_lt_i32_e32 vcc, v1, v11
	v_xor_b32_e32 v13, 2, v7
	s_load_dwordx2 s[22:23], s[0:1], 0x38
	v_cndmask_b32_e32 v1, v7, v1, vcc
	v_cmp_lt_i32_e32 vcc, v13, v11
	v_lshlrev_b32_e32 v16, 2, v5
	v_cmp_eq_u32_e64 s[4:5], 0, v5
	v_cndmask_b32_e32 v13, v7, v13, vcc
	v_lshlrev_b32_e32 v15, 2, v13
	v_xor_b32_e32 v13, 4, v7
	v_cmp_lt_i32_e32 vcc, v13, v11
	v_lshlrev_b32_e32 v82, 4, v5
	v_cmp_gt_u32_e64 s[6:7], 32, v5
	v_cndmask_b32_e32 v13, v7, v13, vcc
	v_lshlrev_b32_e32 v186, 2, v13
	v_xor_b32_e32 v13, 8, v7
	v_cmp_lt_i32_e32 vcc, v13, v11
	v_and_b32_e32 v5, 16, v6
	v_cmp_eq_u32_e64 s[8:9], 0, v5
	v_cndmask_b32_e32 v13, v7, v13, vcc
	v_lshlrev_b32_e32 v187, 2, v13
	v_xor_b32_e32 v13, 16, v7
	v_cmp_lt_i32_e32 vcc, v13, v11
	v_and_b32_e32 v5, 8, v6
	v_mov_b32_e32 v17, 0
	v_cndmask_b32_e32 v13, v7, v13, vcc
	v_lshlrev_b32_e32 v188, 2, v13
	v_xor_b32_e32 v13, 32, v7
	v_cmp_lt_i32_e32 vcc, v13, v11
	v_or_b32_e32 v4, 0x100, v16
	v_cmp_eq_u32_e64 s[10:11], 0, v5
	v_cndmask_b32_e32 v7, v7, v13, vcc
	v_and_b32_e32 v5, 4, v6
	s_waitcnt lgkmcnt(0)
	s_add_u32 s22, s22, 0x2000
	v_or_b32_e32 v8, 0x200, v16
	v_lshlrev_b32_e32 v189, 2, v7
	v_cmp_eq_u32_e64 s[12:13], 0, v5
	v_bfe_u32 v110, v6, 2, 4
	v_and_or_b32 v5, v6, 48, v9
	s_addc_u32 s23, s23, 0
	v_lshlrev_b32_e32 v6, 2, v4
	v_mov_b32_e32 v7, v17
	v_or_b32_e32 v10, 0x300, v16
	v_lshl_add_u64 v[84:85], s[22:23], 0, v[6:7]
	v_lshlrev_b32_e32 v6, 2, v8
	v_or_b32_e32 v12, 0x400, v16
	v_lshl_add_u64 v[86:87], s[22:23], 0, v[6:7]
	v_lshlrev_b32_e32 v6, 2, v10
	v_or_b32_e32 v104, 0x500, v16
	v_lshl_add_u64 v[88:89], s[22:23], 0, v[6:7]
	v_lshlrev_b32_e32 v6, 2, v12
	v_or_b32_e32 v106, 0x600, v16
	v_lshl_add_u64 v[90:91], s[22:23], 0, v[6:7]
	v_lshlrev_b32_e32 v6, 2, v104
	v_or_b32_e32 v108, 0x700, v16
	v_lshl_add_u64 v[92:93], s[22:23], 0, v[6:7]
	v_lshlrev_b32_e32 v6, 2, v106
	v_mov_b32_e32 v3, v17
	v_lshl_add_u64 v[94:95], s[22:23], 0, v[6:7]
	v_lshlrev_b32_e32 v6, 2, v108
	v_lshl_add_u64 v[96:97], s[22:23], 0, v[6:7]
	s_add_u32 s35, s40, 0x4dc00000
	v_lshl_add_u64 v[98:99], s[14:15], 0, v[2:3]
	v_lshl_add_u64 v[6:7], s[40:41], 0, v[16:17]
	s_mov_b64 s[14:15], 0x4dd00000
	s_addc_u32 s38, s41, 0
	v_lshl_add_u64 v[100:101], v[6:7], 0, s[14:15]
	s_lshl_b32 s14, s18, 3
	s_add_i32 s14, s14, 0
	s_add_i32 s39, s14, 0x20300
	s_lshl_b32 s14, s18, 2
	s_add_i32 s14, s14, 0
	s_add_i32 s47, s18, 8
	s_add_i32 s18, s18, s31
	s_add_i32 s46, s14, 0x20100
	s_lshl_b32 s14, s18, 3
	s_add_i32 s14, s14, 0
	s_add_i32 s48, s14, 0x20300
	s_lshl_b32 s14, s18, 2
	v_add_u32_e32 v190, 0, v82
	v_lshlrev_b32_e32 v191, 2, v5
	v_lshlrev_b32_e32 v195, 2, v9
	v_mov_b32_e32 v83, v17
	s_add_i32 s14, s14, 0
	v_lshlrev_b32_e32 v1, 2, v1
	v_or_b32_e32 v192, 16, v191
	v_or_b32_e32 v193, 32, v191
	v_or_b32_e32 v194, 48, v191
	v_or_b32_e32 v196, 64, v195
	v_or_b32_e32 v197, 0x80, v195
	v_or_b32_e32 v198, 0xc0, v195
	v_add_u32_e32 v199, 0x10000, v190
	v_lshl_add_u64 v[82:83], s[22:23], 0, v[82:83]
	v_lshl_add_u64 v[102:103], s[16:17], 0, v[2:3]
	s_add_i32 s49, s14, 0x20100
	s_add_i32 s50, s31, s29
	v_lshlrev_b32_e32 v240, 2, v16
	v_lshlrev_b32_e32 v241, 2, v4
	v_lshlrev_b32_e32 v242, 2, v8
	v_lshlrev_b32_e32 v243, 2, v10
	v_lshlrev_b32_e32 v244, 2, v12
	v_lshlrev_b32_e32 v245, 2, v104
	v_lshlrev_b32_e32 v246, 2, v106
	v_lshlrev_b32_e32 v247, 2, v108
	v_mov_b32_e32 v248, 0x358637bd
	s_mov_b32 s51, 0x800000
	v_lshlrev_b32_e32 v16, 2, v110
	s_mov_b32 s52, 0xff61b1e6
	v_mov_b32_e32 v249, 0xff61b1e6
	s_branch .LBB0_3197

.LBB0_3197:
	s_add_i32 s14, s29, s47
	s_add_i32 s16, s14, -8
	s_min_i32 s15, s16, 0x4000
	s_ashr_i32 s15, s15, 13
	s_mul_i32 s18, s15, 0x3000
	s_ashr_i32 s17, s16, 31
	s_ashr_i32 s19, s18, 31
	s_lshl_b64 s[22:23], s[16:17], 11
	s_lshl_b64 s[18:19], s[18:19], 2
	s_add_u32 s15, s33, s18
	s_addc_u32 s26, s34, s19
	s_add_u32 s18, s15, 0x4000
	s_addc_u32 s19, s26, 0
	s_waitcnt lgkmcnt(0)
	s_add_u32 s100, s15, 0x6000
	s_addc_u32 s101, s26, 0
	s_add_u32 s98, s15, 0x8000
	s_addc_u32 s99, s26, 0
	global_load_dwordx4 v[140:143], v240, s[18:19]
	global_load_dwordx4 v[144:147], v241, s[18:19]
	global_load_dwordx4 v[148:151], v242, s[18:19]
	global_load_dwordx4 v[152:155], v243, s[18:19]
	global_load_dwordx4 v[156:159], v244, s[18:19]
	global_load_dwordx4 v[160:163], v245, s[18:19]
	global_load_dwordx4 v[164:167], v246, s[18:19]
	global_load_dwordx4 v[168:171], v247, s[18:19]
	global_load_dwordx4 v[172:175], v[82:83], off
	global_load_dwordx4 v[176:179], v240, s[100:101]
	global_load_dwordx4 v[180:183], v240, s[98:99]
	global_load_dwordx4 v[200:203], v[84:85], off
	global_load_dwordx4 v[204:207], v241, s[100:101]
	global_load_dwordx4 v[208:211], v241, s[98:99]
	global_load_dwordx4 v[212:215], v[86:87], off
	global_load_dwordx4 v[216:219], v242, s[100:101]
	global_load_dwordx4 v[220:223], v242, s[98:99]
	global_load_dwordx4 v[224:227], v[88:89], off
	global_load_dwordx4 v[228:231], v243, s[100:101]
	global_load_dwordx4 v[232:235], v243, s[98:99]
	global_load_dwordx4 v[236:239], v[90:91], off
	global_load_dwordx4 v[252:255], v244, s[100:101]
	s_waitcnt vmcnt(32)
	v_lshlrev_b32_e32 v2, 16, v18
	v_and_b32_e32 v3, 0xffff0000, v18
	s_waitcnt vmcnt(28)
	v_lshlrev_b32_e32 v8, 16, v26
	v_and_b32_e32 v9, 0xffff0000, v26
	s_lshl_b64 s[24:25], s[16:17], 12
	v_lshl_add_u64 v[108:109], v[98:99], 0, s[24:25]
	s_waitcnt vmcnt(27)
	v_lshlrev_b32_e32 v12, 16, v28
	v_and_b32_e32 v13, 0xffff0000, v28
	s_waitcnt vmcnt(25)
	v_lshlrev_b32_e32 v112, 16, v32
	v_and_b32_e32 v113, 0xffff0000, v32
	s_waitcnt vmcnt(20)
	v_lshlrev_b32_e32 v116, 16, v42
	v_and_b32_e32 v117, 0xffff0000, v42
	v_lshlrev_b32_e32 v134, 16, v40
	v_and_b32_e32 v135, 0xffff0000, v40
	s_waitcnt vmcnt(17)
	v_lshlrev_b32_e32 v136, 16, v48
	v_and_b32_e32 v137, 0xffff0000, v48
	s_add_u32 s24, s15, 0x6000
	s_addc_u32 s25, s26, 0
	s_waitcnt vmcnt(21)
	v_pk_fma_f32 v[4:5], v[140:141], v[8:9], v[2:3]
	v_lshlrev_b32_e32 v2, 16, v19
	v_and_b32_e32 v3, 0xffff0000, v19
	v_lshlrev_b32_e32 v8, 16, v27
	v_and_b32_e32 v9, 0xffff0000, v27
	v_pk_fma_f32 v[10:11], v[142:143], v[8:9], v[2:3]
	v_cvt_pk_bf16_f32 v2, v4, v5
	v_cvt_pk_bf16_f32 v3, v10, v11
	global_store_dwordx2 v[108:109], v[2:3], off nt
	v_lshlrev_b32_e32 v2, 16, v20
	v_and_b32_e32 v3, 0xffff0000, v20
	v_mov_b32_e32 v104, v11
	s_waitcnt vmcnt(21)
	v_pk_fma_f32 v[2:3], v[144:145], v[12:13], v[2:3]
	v_lshlrev_b32_e32 v6, 16, v21
	v_and_b32_e32 v7, 0xffff0000, v21
	v_lshlrev_b32_e32 v12, 16, v29
	v_and_b32_e32 v13, 0xffff0000, v29
	v_pk_fma_f32 v[6:7], v[146:147], v[12:13], v[6:7]
	v_cvt_pk_bf16_f32 v8, v2, v3
	v_cvt_pk_bf16_f32 v9, v6, v7
	v_mov_b32_e32 v12, v5
	v_mov_b32_e32 v13, v3
	global_store_dwordx2 v[108:109], v[8:9], off offset:512 nt
	v_mov_b32_e32 v8, v4
	v_mov_b32_e32 v9, v2
	v_pk_mul_f32 v[12:13], v[12:13], v[12:13]
	v_mov_b32_e32 v105, v7
	v_pk_fma_f32 v[8:9], v[8:9], v[8:9], v[12:13]
	v_mov_b32_e32 v12, v10
	v_mov_b32_e32 v13, v6
	v_pk_mul_f32 v[104:105], v[104:105], v[104:105]
	s_nop 0
	v_pk_fma_f32 v[12:13], v[12:13], v[12:13], v[104:105]
	v_pk_add_f32 v[8:9], v[8:9], v[12:13]
	v_lshlrev_b32_e32 v12, 16, v30
	v_pk_add_f32 v[110:111], v[8:9], v[8:9] op_sel:[0,1] op_sel_hi:[1,0]
	v_lshlrev_b32_e32 v8, 16, v22
	v_and_b32_e32 v9, 0xffff0000, v22
	v_and_b32_e32 v13, 0xffff0000, v30
	s_waitcnt vmcnt(21)
	v_pk_fma_f32 v[12:13], v[148:149], v[12:13], v[8:9]
	v_lshlrev_b32_e32 v8, 16, v23
	v_and_b32_e32 v9, 0xffff0000, v23
	v_lshlrev_b32_e32 v104, 16, v31
	v_and_b32_e32 v105, 0xffff0000, v31
	v_pk_fma_f32 v[118:119], v[150:151], v[104:105], v[8:9]
	v_cvt_pk_bf16_f32 v8, v12, v13
	v_cvt_pk_bf16_f32 v9, v118, v119
	v_mov_b32_e32 v104, v13
	v_mov_b32_e32 v105, v119
	global_store_dwordx2 v[108:109], v[8:9], off offset:1024 nt
	v_mov_b32_e32 v8, v12
	v_mov_b32_e32 v9, v118
	v_pk_mul_f32 v[104:105], v[104:105], v[104:105]
	s_nop 0
	v_pk_fma_f32 v[8:9], v[8:9], v[8:9], v[104:105]
	v_pk_add_f32 v[114:115], v[8:9], v[8:9] op_sel:[0,1] op_sel_hi:[1,0]
	v_lshlrev_b32_e32 v8, 16, v24
	v_and_b32_e32 v9, 0xffff0000, v24
	s_waitcnt vmcnt(21)
	v_pk_fma_f32 v[112:113], v[152:153], v[112:113], v[8:9]
	v_lshlrev_b32_e32 v8, 16, v25
	v_and_b32_e32 v9, 0xffff0000, v25
	v_lshlrev_b32_e32 v104, 16, v33
	v_and_b32_e32 v105, 0xffff0000, v33
	v_pk_fma_f32 v[122:123], v[154:155], v[104:105], v[8:9]
	v_cvt_pk_bf16_f32 v8, v112, v113
	v_cvt_pk_bf16_f32 v9, v122, v123
	global_store_dwordx2 v[108:109], v[8:9], off offset:1536 nt
	v_mul_f32_e32 v8, v113, v113
	v_pk_fma_f32 v[120:121], v[112:113], v[112:113], v[8:9] op_sel_hi:[1,1,0]
	v_mul_f32_e32 v8, v123, v123
	v_pk_fma_f32 v[124:125], v[122:123], v[122:123], v[8:9] op_sel_hi:[1,1,0]
	v_lshlrev_b32_e32 v8, 16, v34
	v_and_b32_e32 v9, 0xffff0000, v34
	s_waitcnt vmcnt(21)
	v_pk_fma_f32 v[8:9], v[156:157], v[116:117], v[8:9]
	v_lshlrev_b32_e32 v104, 16, v35
	v_and_b32_e32 v105, 0xffff0000, v35
	v_lshlrev_b32_e32 v116, 16, v43
	v_and_b32_e32 v117, 0xffff0000, v43
	v_pk_fma_f32 v[116:117], v[158:159], v[116:117], v[104:105]
	v_cvt_pk_bf16_f32 v104, v8, v9
	v_cvt_pk_bf16_f32 v105, v116, v117
	global_store_dwordx2 v[108:109], v[104:105], off offset:2048 nt
	v_pk_mul_f32 v[104:105], v[8:9], v[8:9]
	v_pk_mul_f32 v[106:107], v[116:117], v[116:117]
	v_mov_b32_e32 v111, v104
	v_mov_b32_e32 v115, v105
	v_mov_b32_e32 v121, v106
	v_mov_b32_e32 v125, v107
	v_pk_add_f32 v[104:105], v[110:111], v[114:115]
	v_pk_add_f32 v[106:107], v[120:121], v[124:125]
	v_lshlrev_b32_e32 v110, 16, v36
	v_pk_add_f32 v[104:105], v[104:105], v[106:107]
	v_and_b32_e32 v111, 0xffff0000, v36
	v_pk_add_f32 v[126:127], v[104:105], v[104:105] op_sel:[0,1] op_sel_hi:[1,0]
	v_lshlrev_b32_e32 v114, 16, v44
	v_and_b32_e32 v115, 0xffff0000, v44
	v_lshlrev_b32_e32 v120, 16, v46
	v_and_b32_e32 v121, 0xffff0000, v46
	s_waitcnt vmcnt(21)
	v_pk_fma_f32 v[114:115], v[160:161], v[114:115], v[110:111]
	v_lshlrev_b32_e32 v104, 16, v37
	v_and_b32_e32 v105, 0xffff0000, v37
	v_lshlrev_b32_e32 v110, 16, v45
	v_and_b32_e32 v111, 0xffff0000, v45
	v_pk_fma_f32 v[124:125], v[162:163], v[110:111], v[104:105]
	v_cvt_pk_bf16_f32 v104, v114, v115
	v_cvt_pk_bf16_f32 v105, v124, v125
	v_mov_b32_e32 v106, v115
	v_mov_b32_e32 v107, v125
	global_store_dwordx2 v[108:109], v[104:105], off offset:2560 nt
	v_mov_b32_e32 v104, v114
	v_mov_b32_e32 v105, v124
	v_pk_mul_f32 v[106:107], v[106:107], v[106:107]
	v_lshlrev_b32_e32 v110, 16, v38
	v_pk_fma_f32 v[104:105], v[104:105], v[104:105], v[106:107]
	v_and_b32_e32 v111, 0xffff0000, v38
	v_pk_add_f32 v[128:129], v[104:105], v[104:105] op_sel:[0,1] op_sel_hi:[1,0]
	s_waitcnt vmcnt(21)
	v_pk_fma_f32 v[110:111], v[164:165], v[120:121], v[110:111]
	v_lshlrev_b32_e32 v104, 16, v39
	v_and_b32_e32 v105, 0xffff0000, v39
	v_lshlrev_b32_e32 v120, 16, v47
	v_and_b32_e32 v121, 0xffff0000, v47
	v_pk_fma_f32 v[120:121], v[166:167], v[120:121], v[104:105]
	global_load_dwordx4 v[164:167], v244, s[98:99]
	v_cvt_pk_bf16_f32 v104, v110, v111
	v_cvt_pk_bf16_f32 v105, v120, v121
	global_store_dwordx2 v[108:109], v[104:105], off offset:3072 nt
	v_mul_f32_e32 v104, v111, v111
	v_pk_fma_f32 v[130:131], v[110:111], v[110:111], v[104:105] op_sel_hi:[1,1,0]
	v_mul_f32_e32 v104, v121, v121
	v_pk_fma_f32 v[132:133], v[120:121], v[120:121], v[104:105] op_sel_hi:[1,1,0]
	s_add_u32 s18, s15, 0x8000
	s_addc_u32 s19, s26, 0
	s_waitcnt vmcnt(22)
	v_pk_fma_f32 v[104:105], v[168:169], v[136:137], v[134:135]
	v_lshlrev_b32_e32 v134, 16, v41
	v_and_b32_e32 v135, 0xffff0000, v41
	v_lshlrev_b32_e32 v136, 16, v49
	v_and_b32_e32 v137, 0xffff0000, v49
	v_pk_fma_f32 v[106:107], v[170:171], v[136:137], v[134:135]
	global_load_dwordx4 v[168:171], v[92:93], off
	v_cvt_pk_bf16_f32 v134, v104, v105
	v_cvt_pk_bf16_f32 v135, v106, v107
	global_store_dwordx2 v[108:109], v[134:135], off offset:3584 nt
	v_pk_mul_f32 v[108:109], v[104:105], v[104:105]
	v_pk_mul_f32 v[134:135], v[106:107], v[106:107]
	v_mov_b32_e32 v127, v108
	v_mov_b32_e32 v129, v109
	v_mov_b32_e32 v131, v134
	v_mov_b32_e32 v133, v135
	v_pk_add_f32 v[108:109], v[126:127], v[128:129]
	v_pk_add_f32 v[126:127], v[130:131], v[132:133]
	s_nop 0
	v_pk_add_f32 v[108:109], v[108:109], v[126:127]
	v_add_f32_e32 v108, v108, v109
	ds_bpermute_b32 v109, v1, v108
	s_waitcnt lgkmcnt(0)
	v_add_f32_e32 v108, v108, v109
	ds_bpermute_b32 v109, v15, v108
	s_waitcnt lgkmcnt(0)
	v_add_f32_e32 v108, v108, v109
	ds_bpermute_b32 v109, v186, v108
	s_waitcnt lgkmcnt(0)
	v_add_f32_e32 v108, v108, v109
	ds_bpermute_b32 v109, v187, v108
	s_waitcnt lgkmcnt(0)
	v_add_f32_e32 v108, v108, v109
	ds_bpermute_b32 v109, v188, v108
	s_waitcnt lgkmcnt(0)
	v_add_f32_e32 v108, v108, v109
	ds_bpermute_b32 v109, v189, v108
	s_waitcnt lgkmcnt(0)
	v_add_f32_e32 v108, v108, v109
	v_fmamk_f32 v108, v108, 0x3a000000, v248
	v_cmp_gt_f32_e32 vcc, s51, v108
	v_mul_f32_e32 v109, 0x4b800000, v108
	s_nop 0
	v_cndmask_b32_e32 v108, v108, v109, vcc
	v_rsq_f32_e32 v108, v108
	s_nop 0
	v_mul_f32_e32 v109, 0x45800000, v108
	v_cndmask_b32_e32 v108, v108, v109, vcc
	v_pk_mul_f32 v[10:11], v[10:11], v[108:109] op_sel_hi:[1,0]
	v_pk_mul_f32 v[4:5], v[4:5], v[108:109] op_sel_hi:[1,0]
	s_waitcnt vmcnt(23)
	v_pk_mul_f32 v[10:11], v[174:175], v[10:11]
	v_pk_mul_f32 v[4:5], v[172:173], v[4:5]
	global_load_dwordx4 v[172:175], v245, s[100:101]
	s_waitcnt vmcnt(22)
	v_pk_add_f32 v[126:127], v[182:183], 1.0 op_sel_hi:[1,0]
	v_pk_add_f32 v[128:129], v[180:181], 1.0 op_sel_hi:[1,0]
	global_load_dwordx4 v[180:183], v245, s[98:99]
	v_pk_fma_f32 v[134:135], v[126:127], v[10:11], v[178:179]
	v_pk_fma_f32 v[132:133], v[128:129], v[4:5], v[176:177]
	global_load_dwordx4 v[176:179], v[94:95], off
	v_max_f32_e64 v4, |v134|, |v135|
	v_max3_f32 v109, |v132|, |v133|, v4
	v_pk_mul_f32 v[4:5], v[6:7], v[108:109] op_sel_hi:[1,0]
	v_pk_mul_f32 v[2:3], v[2:3], v[108:109] op_sel_hi:[1,0]
	s_waitcnt vmcnt(23)
	v_pk_mul_f32 v[4:5], v[202:203], v[4:5]
	v_pk_mul_f32 v[2:3], v[200:201], v[2:3]
	global_load_dwordx4 v[200:203], v246, s[100:101]
	s_waitcnt vmcnt(22)
	v_pk_add_f32 v[6:7], v[210:211], 1.0 op_sel_hi:[1,0]
	v_pk_add_f32 v[10:11], v[208:209], 1.0 op_sel_hi:[1,0]
	global_load_dwordx4 v[208:211], v246, s[98:99]
	v_pk_fma_f32 v[138:139], v[6:7], v[4:5], v[206:207]
	v_pk_fma_f32 v[136:137], v[10:11], v[2:3], v[204:205]
	global_load_dwordx4 v[204:207], v[96:97], off
	v_max_f32_e64 v2, |v138|, |v139|
	v_max3_f32 v2, |v136|, |v137|, v2
	v_max3_f32 v109, v109, 0, v2
	v_pk_mul_f32 v[6:7], v[118:119], v[108:109] op_sel_hi:[1,0]
	v_pk_mul_f32 v[10:11], v[12:13], v[108:109] op_sel_hi:[1,0]
	v_pk_mul_f32 v[112:113], v[112:113], v[108:109] op_sel_hi:[1,0]
	s_waitcnt vmcnt(23)
	v_pk_mul_f32 v[4:5], v[214:215], v[6:7]
	v_pk_mul_f32 v[2:3], v[212:213], v[10:11]
	global_load_dwordx4 v[212:215], v247, s[100:101]
	s_waitcnt vmcnt(22)
	v_pk_add_f32 v[6:7], v[222:223], 1.0 op_sel_hi:[1,0]
	v_pk_add_f32 v[10:11], v[220:221], 1.0 op_sel_hi:[1,0]
	global_load_dwordx4 v[220:223], v247, s[98:99]
	v_pk_fma_f32 v[142:143], v[6:7], v[4:5], v[218:219]
	v_pk_fma_f32 v[140:141], v[10:11], v[2:3], v[216:217]
	v_max_f32_e64 v2, |v142|, |v143|
	v_max3_f32 v118, |v140|, |v141|, v2
	v_pk_mul_f32 v[6:7], v[122:123], v[108:109] op_sel_hi:[1,0]
	s_waitcnt vmcnt(22)
	v_pk_mul_f32 v[2:3], v[224:225], v[112:113]
	v_pk_mul_f32 v[4:5], v[226:227], v[6:7]
	s_waitcnt vmcnt(20)
	v_pk_add_f32 v[6:7], v[234:235], 1.0 op_sel_hi:[1,0]
	v_pk_add_f32 v[112:113], v[232:233], 1.0 op_sel_hi:[1,0]
	v_pk_fma_f32 v[146:147], v[6:7], v[4:5], v[230:231]
	v_pk_fma_f32 v[144:145], v[112:113], v[2:3], v[228:229]
	v_max_f32_e64 v2, |v146|, |v147|
	v_max3_f32 v2, |v144|, |v145|, v2
	v_max3_f32 v109, v109, v118, v2
	v_pk_mul_f32 v[6:7], v[116:117], v[108:109] op_sel_hi:[1,0]
	v_pk_mul_f32 v[8:9], v[8:9], v[108:109] op_sel_hi:[1,0]
	v_pk_mul_f32 v[112:113], v[124:125], v[108:109] op_sel_hi:[1,0]
	v_pk_mul_f32 v[114:115], v[114:115], v[108:109] op_sel_hi:[1,0]
	s_waitcnt vmcnt(19)
	v_pk_mul_f32 v[4:5], v[238:239], v[6:7]
	v_pk_mul_f32 v[2:3], v[236:237], v[8:9]
	s_waitcnt vmcnt(11)
	v_pk_add_f32 v[6:7], v[166:167], 1.0 op_sel_hi:[1,0]
	v_pk_add_f32 v[8:9], v[164:165], 1.0 op_sel_hi:[1,0]
	v_pk_fma_f32 v[150:151], v[4:5], v[6:7], v[254:255]
	v_pk_fma_f32 v[148:149], v[2:3], v[8:9], v[252:253]
	v_max_f32_e64 v2, |v150|, |v151|
	v_max3_f32 v116, |v148|, |v149|, v2
	s_waitcnt vmcnt(9)
	v_pk_mul_f32 v[4:5], v[112:113], v[170:171]
	v_pk_mul_f32 v[2:3], v[114:115], v[168:169]
	s_waitcnt vmcnt(6)
	v_pk_add_f32 v[12:13], v[182:183], 1.0 op_sel_hi:[1,0]
	v_pk_add_f32 v[10:11], v[180:181], 1.0 op_sel_hi:[1,0]
	v_pk_fma_f32 v[154:155], v[4:5], v[12:13], v[174:175]
	v_pk_fma_f32 v[152:153], v[2:3], v[10:11], v[172:173]
	v_max_f32_e64 v2, |v154|, |v155|
	v_max3_f32 v2, |v152|, |v153|, v2
	v_max3_f32 v109, v109, v116, v2
	v_pk_mul_f32 v[112:113], v[120:121], v[108:109] op_sel_hi:[1,0]
	v_pk_mul_f32 v[110:111], v[110:111], v[108:109] op_sel_hi:[1,0]
	v_pk_mul_f32 v[106:107], v[106:107], v[108:109] op_sel_hi:[1,0]
	v_pk_mul_f32 v[104:105], v[104:105], v[108:109] op_sel_hi:[1,0]
	s_waitcnt vmcnt(5)
	v_pk_mul_f32 v[4:5], v[112:113], v[178:179]
	v_pk_mul_f32 v[2:3], v[110:111], v[176:177]
	s_waitcnt vmcnt(3)
	v_pk_add_f32 v[12:13], v[210:211], 1.0 op_sel_hi:[1,0]
	v_pk_add_f32 v[10:11], v[208:209], 1.0 op_sel_hi:[1,0]
	v_pk_fma_f32 v[158:159], v[4:5], v[12:13], v[202:203]
	v_pk_fma_f32 v[156:157], v[2:3], v[10:11], v[200:201]
	v_max_f32_e64 v2, |v158|, |v159|
	v_max3_f32 v110, |v156|, |v157|, v2
	s_waitcnt vmcnt(2)
	v_pk_mul_f32 v[8:9], v[106:107], v[206:207]
	v_pk_mul_f32 v[6:7], v[104:105], v[204:205]
	s_waitcnt vmcnt(0)
	v_pk_add_f32 v[12:13], v[222:223], 1.0 op_sel_hi:[1,0]
	v_pk_add_f32 v[10:11], v[220:221], 1.0 op_sel_hi:[1,0]
	v_pk_fma_f32 v[162:163], v[8:9], v[12:13], v[214:215]
	v_pk_fma_f32 v[160:161], v[6:7], v[10:11], v[212:213]
	v_max_f32_e64 v2, |v162|, |v163|
	v_max3_f32 v2, |v160|, |v161|, v2
	v_max3_f32 v2, v109, v110, v2
	ds_bpermute_b32 v3, v1, v2
	s_waitcnt lgkmcnt(0)
	v_max_f32_e32 v3, v3, v3
	v_max_f32_e32 v2, v2, v3
	ds_bpermute_b32 v3, v15, v2
	s_waitcnt lgkmcnt(0)
	v_max_f32_e32 v3, v3, v3
	v_max_f32_e32 v2, v2, v3
	ds_bpermute_b32 v3, v186, v2
	s_waitcnt lgkmcnt(0)
	v_max_f32_e32 v3, v3, v3
	v_max_f32_e32 v2, v2, v3
	ds_bpermute_b32 v3, v187, v2
	s_waitcnt lgkmcnt(0)
	v_max_f32_e32 v3, v3, v3
	v_max_f32_e32 v2, v2, v3
	ds_bpermute_b32 v3, v188, v2
	s_waitcnt lgkmcnt(0)
	v_max_f32_e32 v3, v3, v3
	v_max_f32_e32 v2, v2, v3
	ds_bpermute_b32 v3, v189, v2
	s_and_saveexec_b64 s[18:19], s[4:5]
	s_cbranch_execz .LBB0_3199
	s_waitcnt lgkmcnt(0)
	v_max_f32_e32 v3, v3, v3
	v_max_f32_e32 v2, v2, v2
	s_lshl_b64 s[16:17], s[16:17], 2
	v_max_f32_e32 v2, v2, v3
	s_add_u32 s16, s35, s16
	v_mul_f32_e32 v2, 0x3c010204, v2
	s_addc_u32 s17, s38, s17
	global_store_dword v17, v2, s[16:17]
.LBB0_3199:
	s_or_b64 exec, exec, s[18:19]
	v_mov_b32_e32 v4, 0
	v_cvt_pk_fp8_f32 v4, v132, v133
	s_waitcnt lgkmcnt(0)
	v_lshl_add_u64 v[2:3], v[100:101], 0, s[22:23]
	s_add_i32 s16, s50, s47
	s_add_i32 s18, s16, -8
	v_cvt_pk_fp8_f32 v4, v134, v135 op_sel:[0,0,1]
	s_min_i32 s15, s18, 0x4000
	s_ashr_i32 s15, s15, 13
	s_mul_i32 s22, s15, 0x3000
	global_store_dword v[2:3], v4, off
	v_mov_b32_e32 v4, 0
	v_cvt_pk_fp8_f32 v4, v136, v137
	s_ashr_i32 s23, s22, 31
	s_ashr_i32 s19, s18, 31
	s_lshl_b64 s[22:23], s[22:23], 2
	v_cvt_pk_fp8_f32 v4, v138, v139 op_sel:[0,0,1]
	s_add_u32 s15, s33, s22
	s_addc_u32 s17, s34, s23
	s_add_u32 s22, s15, 0x4000
	global_store_dword v[2:3], v4, off offset:256
	v_mov_b32_e32 v4, 0
	v_cvt_pk_fp8_f32 v4, v140, v141
	s_addc_u32 s23, s17, 0
	v_lshlrev_b32_e32 v8, 16, v58
	v_and_b32_e32 v9, 0xffff0000, v58
	v_cvt_pk_fp8_f32 v4, v142, v143 op_sel:[0,0,1]
	s_lshl_b64 s[24:25], s[18:19], 12
	v_lshl_add_u64 v[104:105], v[98:99], 0, s[24:25]
	v_lshlrev_b32_e32 v12, 16, v60
	global_store_dword v[2:3], v4, off offset:512
	v_mov_b32_e32 v4, 0
	v_cvt_pk_fp8_f32 v4, v144, v145
	v_and_b32_e32 v13, 0xffff0000, v60
	v_lshlrev_b32_e32 v116, 16, v64
	v_and_b32_e32 v117, 0xffff0000, v64
	v_cvt_pk_fp8_f32 v4, v146, v147 op_sel:[0,0,1]
	v_lshlrev_b32_e32 v120, 16, v74
	v_and_b32_e32 v121, 0xffff0000, v74
	v_lshlrev_b32_e32 v128, 16, v78
	global_store_dword v[2:3], v4, off offset:768
	v_mov_b32_e32 v4, 0
	v_cvt_pk_fp8_f32 v4, v148, v149
	v_and_b32_e32 v129, 0xffff0000, v78
	v_lshlrev_b32_e32 v164, 16, v72
	v_and_b32_e32 v165, 0xffff0000, v72
	v_cvt_pk_fp8_f32 v4, v150, v151 op_sel:[0,0,1]
	v_lshlrev_b32_e32 v166, 16, v80
	v_and_b32_e32 v167, 0xffff0000, v80
	s_add_u32 s24, s15, 0x6000
	global_store_dword v[2:3], v4, off offset:1024
	v_mov_b32_e32 v4, 0
	v_cvt_pk_fp8_f32 v4, v152, v153
	s_addc_u32 s25, s17, 0
	v_cvt_pk_fp8_f32 v4, v154, v155 op_sel:[0,0,1]
	global_store_dword v[2:3], v4, off offset:1280
	v_mov_b32_e32 v4, 0
	v_cvt_pk_fp8_f32 v4, v156, v157
	v_cvt_pk_fp8_f32 v4, v158, v159 op_sel:[0,0,1]
	global_store_dword v[2:3], v4, off offset:1536
	v_mov_b32_e32 v4, 0
	v_cvt_pk_fp8_f32 v4, v160, v161
	v_cvt_pk_fp8_f32 v4, v162, v163 op_sel:[0,0,1]
	global_store_dword v[2:3], v4, off offset:1792
	s_add_u32 s100, s15, 0x6000
	s_addc_u32 s101, s17, 0
	s_add_u32 s98, s15, 0x8000
	s_addc_u32 s99, s17, 0
	global_load_dwordx4 v[172:175], v240, s[22:23]
	global_load_dwordx4 v[176:179], v241, s[22:23]
	global_load_dwordx4 v[180:183], v242, s[22:23]
	global_load_dwordx4 v[200:203], v243, s[22:23]
	global_load_dwordx4 v[204:207], v244, s[22:23]
	global_load_dwordx4 v[208:211], v245, s[22:23]
	global_load_dwordx4 v[212:215], v246, s[22:23]
	global_load_dwordx4 v[216:219], v247, s[22:23]
	global_load_dwordx4 v[220:223], v[82:83], off
	global_load_dwordx4 v[224:227], v240, s[100:101]
	global_load_dwordx4 v[228:231], v240, s[98:99]
	global_load_dwordx4 v[232:235], v[84:85], off
	global_load_dwordx4 v[236:239], v241, s[100:101]
	global_load_dwordx4 v[252:255], v241, s[98:99]
	v_lshlrev_b32_e32 v2, 16, v50
	v_and_b32_e32 v3, 0xffff0000, v50
	s_waitcnt vmcnt(13)
	v_pk_fma_f32 v[4:5], v[172:173], v[8:9], v[2:3]
	v_lshlrev_b32_e32 v2, 16, v51
	v_and_b32_e32 v3, 0xffff0000, v51
	v_lshlrev_b32_e32 v8, 16, v59
	v_and_b32_e32 v9, 0xffff0000, v59
	v_pk_fma_f32 v[10:11], v[174:175], v[8:9], v[2:3]
	v_cvt_pk_bf16_f32 v2, v4, v5
	v_cvt_pk_bf16_f32 v3, v10, v11
	global_store_dwordx2 v[104:105], v[2:3], off nt
	v_lshlrev_b32_e32 v2, 16, v52
	v_and_b32_e32 v3, 0xffff0000, v52
	v_mov_b32_e32 v106, v11
	s_waitcnt vmcnt(13)
	v_pk_fma_f32 v[2:3], v[176:177], v[12:13], v[2:3]
	v_lshlrev_b32_e32 v6, 16, v53
	v_and_b32_e32 v7, 0xffff0000, v53
	v_lshlrev_b32_e32 v12, 16, v61
	v_and_b32_e32 v13, 0xffff0000, v61
	v_pk_fma_f32 v[6:7], v[178:179], v[12:13], v[6:7]
	v_cvt_pk_bf16_f32 v8, v2, v3
	v_cvt_pk_bf16_f32 v9, v6, v7
	v_mov_b32_e32 v12, v5
	v_mov_b32_e32 v13, v3
	global_store_dwordx2 v[104:105], v[8:9], off offset:512 nt
	v_mov_b32_e32 v8, v4
	v_mov_b32_e32 v9, v2
	v_pk_mul_f32 v[12:13], v[12:13], v[12:13]
	v_mov_b32_e32 v107, v7
	v_pk_fma_f32 v[8:9], v[8:9], v[8:9], v[12:13]
	v_mov_b32_e32 v12, v10
	v_mov_b32_e32 v13, v6
	v_pk_mul_f32 v[106:107], v[106:107], v[106:107]
	s_nop 0
	v_pk_fma_f32 v[12:13], v[12:13], v[12:13], v[106:107]
	v_pk_add_f32 v[8:9], v[8:9], v[12:13]
	v_lshlrev_b32_e32 v12, 16, v62
	v_pk_add_f32 v[110:111], v[8:9], v[8:9] op_sel:[0,1] op_sel_hi:[1,0]
	v_lshlrev_b32_e32 v8, 16, v54
	v_and_b32_e32 v9, 0xffff0000, v54
	v_and_b32_e32 v13, 0xffff0000, v62
	s_waitcnt vmcnt(13)
	v_pk_fma_f32 v[12:13], v[180:181], v[12:13], v[8:9]
	v_lshlrev_b32_e32 v8, 16, v55
	v_and_b32_e32 v9, 0xffff0000, v55
	v_lshlrev_b32_e32 v106, 16, v63
	v_and_b32_e32 v107, 0xffff0000, v63
	v_pk_fma_f32 v[112:113], v[182:183], v[106:107], v[8:9]
	global_load_dwordx4 v[180:183], v[86:87], off
	v_cvt_pk_bf16_f32 v8, v12, v13
	v_cvt_pk_bf16_f32 v9, v112, v113
	v_mov_b32_e32 v106, v13
	v_mov_b32_e32 v107, v113
	global_store_dwordx2 v[104:105], v[8:9], off offset:1024 nt
	v_mov_b32_e32 v8, v12
	v_mov_b32_e32 v9, v112
	v_pk_mul_f32 v[106:107], v[106:107], v[106:107]
	s_nop 0
	v_pk_fma_f32 v[8:9], v[8:9], v[8:9], v[106:107]
	v_pk_add_f32 v[114:115], v[8:9], v[8:9] op_sel:[0,1] op_sel_hi:[1,0]
	v_lshlrev_b32_e32 v8, 16, v56
	v_and_b32_e32 v9, 0xffff0000, v56
	s_waitcnt vmcnt(14)
	v_pk_fma_f32 v[116:117], v[200:201], v[116:117], v[8:9]
	v_lshlrev_b32_e32 v8, 16, v57
	v_and_b32_e32 v9, 0xffff0000, v57
	v_lshlrev_b32_e32 v106, 16, v65
	v_and_b32_e32 v107, 0xffff0000, v65
	v_pk_fma_f32 v[118:119], v[202:203], v[106:107], v[8:9]
	global_load_dwordx4 v[200:203], v242, s[100:101]
	v_cvt_pk_bf16_f32 v8, v116, v117
	v_cvt_pk_bf16_f32 v9, v118, v119
	global_store_dwordx2 v[104:105], v[8:9], off offset:1536 nt
	v_mul_f32_e32 v8, v117, v117
	v_pk_fma_f32 v[122:123], v[116:117], v[116:117], v[8:9] op_sel_hi:[1,1,0]
	v_mul_f32_e32 v8, v119, v119
	v_pk_fma_f32 v[124:125], v[118:119], v[118:119], v[8:9] op_sel_hi:[1,1,0]
	v_lshlrev_b32_e32 v8, 16, v66
	v_and_b32_e32 v9, 0xffff0000, v66
	s_waitcnt vmcnt(15)
	v_pk_fma_f32 v[8:9], v[204:205], v[120:121], v[8:9]
	v_lshlrev_b32_e32 v106, 16, v67
	v_and_b32_e32 v107, 0xffff0000, v67
	v_lshlrev_b32_e32 v120, 16, v75
	v_and_b32_e32 v121, 0xffff0000, v75
	v_pk_fma_f32 v[120:121], v[206:207], v[120:121], v[106:107]
	global_load_dwordx4 v[204:207], v242, s[98:99]
	v_cvt_pk_bf16_f32 v106, v8, v9
	v_cvt_pk_bf16_f32 v107, v120, v121
	global_store_dwordx2 v[104:105], v[106:107], off offset:2048 nt
	v_pk_mul_f32 v[106:107], v[8:9], v[8:9]
	v_pk_mul_f32 v[108:109], v[120:121], v[120:121]
	v_mov_b32_e32 v111, v106
	v_mov_b32_e32 v115, v107
	v_mov_b32_e32 v123, v108
	v_mov_b32_e32 v125, v109
	v_pk_add_f32 v[106:107], v[110:111], v[114:115]
	v_pk_add_f32 v[108:109], v[122:123], v[124:125]
	v_lshlrev_b32_e32 v114, 16, v68
	v_pk_add_f32 v[106:107], v[106:107], v[108:109]
	v_and_b32_e32 v115, 0xffff0000, v68
	v_pk_add_f32 v[110:111], v[106:107], v[106:107] op_sel:[0,1] op_sel_hi:[1,0]
	v_lshlrev_b32_e32 v122, 16, v76
	v_and_b32_e32 v123, 0xffff0000, v76
	s_waitcnt vmcnt(16)
	v_pk_fma_f32 v[124:125], v[208:209], v[122:123], v[114:115]
	v_lshlrev_b32_e32 v106, 16, v69
	v_and_b32_e32 v107, 0xffff0000, v69
	v_lshlrev_b32_e32 v114, 16, v77
	v_and_b32_e32 v115, 0xffff0000, v77
	v_pk_fma_f32 v[126:127], v[210:211], v[114:115], v[106:107]
	global_load_dwordx4 v[208:211], v[88:89], off
	v_cvt_pk_bf16_f32 v106, v124, v125
	v_cvt_pk_bf16_f32 v107, v126, v127
	v_mov_b32_e32 v108, v125
	v_mov_b32_e32 v109, v127
	global_store_dwordx2 v[104:105], v[106:107], off offset:2560 nt
	v_mov_b32_e32 v106, v124
	v_mov_b32_e32 v107, v126
	v_pk_mul_f32 v[108:109], v[108:109], v[108:109]
	v_lshlrev_b32_e32 v122, 16, v70
	v_pk_fma_f32 v[106:107], v[106:107], v[106:107], v[108:109]
	v_and_b32_e32 v123, 0xffff0000, v70
	v_pk_add_f32 v[114:115], v[106:107], v[106:107] op_sel:[0,1] op_sel_hi:[1,0]
	s_waitcnt vmcnt(17)
	v_pk_fma_f32 v[128:129], v[212:213], v[128:129], v[122:123]
	v_lshlrev_b32_e32 v106, 16, v71
	v_and_b32_e32 v107, 0xffff0000, v71
	v_lshlrev_b32_e32 v122, 16, v79
	v_and_b32_e32 v123, 0xffff0000, v79
	v_pk_fma_f32 v[130:131], v[214:215], v[122:123], v[106:107]
	global_load_dwordx4 v[212:215], v243, s[100:101]
	v_cvt_pk_bf16_f32 v106, v128, v129
	v_cvt_pk_bf16_f32 v107, v130, v131
	global_store_dwordx2 v[104:105], v[106:107], off offset:3072 nt
	v_mul_f32_e32 v106, v129, v129
	v_pk_fma_f32 v[122:123], v[128:129], v[128:129], v[106:107] op_sel_hi:[1,1,0]
	v_mul_f32_e32 v106, v131, v131
	v_pk_fma_f32 v[168:169], v[130:131], v[130:131], v[106:107] op_sel_hi:[1,1,0]
	s_add_u32 s22, s15, 0x8000
	s_addc_u32 s23, s17, 0
	s_waitcnt vmcnt(18)
	v_pk_fma_f32 v[164:165], v[216:217], v[166:167], v[164:165]
	v_lshlrev_b32_e32 v106, 16, v73
	v_and_b32_e32 v107, 0xffff0000, v73
	v_lshlrev_b32_e32 v166, 16, v81
	v_and_b32_e32 v167, 0xffff0000, v81
	v_pk_fma_f32 v[166:167], v[218:219], v[166:167], v[106:107]
	global_load_dwordx4 v[216:219], v243, s[98:99]
	v_cvt_pk_bf16_f32 v106, v164, v165
	v_cvt_pk_bf16_f32 v107, v166, v167
	global_store_dwordx2 v[104:105], v[106:107], off offset:3584 nt
	v_pk_mul_f32 v[104:105], v[164:165], v[164:165]
	v_pk_mul_f32 v[106:107], v[166:167], v[166:167]
	v_mov_b32_e32 v111, v104
	v_mov_b32_e32 v115, v105
	v_mov_b32_e32 v123, v106
	v_mov_b32_e32 v169, v107
	v_pk_add_f32 v[104:105], v[110:111], v[114:115]
	v_pk_add_f32 v[106:107], v[122:123], v[168:169]
	s_nop 0
	v_pk_add_f32 v[104:105], v[104:105], v[106:107]
	s_nop 0
	v_add_f32_e32 v104, v104, v105
	ds_bpermute_b32 v105, v1, v104
	s_waitcnt lgkmcnt(0)
	v_add_f32_e32 v104, v104, v105
	ds_bpermute_b32 v105, v15, v104
	s_waitcnt lgkmcnt(0)
	v_add_f32_e32 v104, v104, v105
	ds_bpermute_b32 v105, v186, v104
	s_waitcnt lgkmcnt(0)
	v_add_f32_e32 v104, v104, v105
	ds_bpermute_b32 v105, v187, v104
	s_waitcnt lgkmcnt(0)
	v_add_f32_e32 v104, v104, v105
	ds_bpermute_b32 v105, v188, v104
	s_waitcnt lgkmcnt(0)
	v_add_f32_e32 v104, v104, v105
	ds_bpermute_b32 v105, v189, v104
	s_waitcnt lgkmcnt(0)
	v_add_f32_e32 v104, v104, v105
	v_fmamk_f32 v104, v104, 0x3a000000, v248
	v_cmp_gt_f32_e32 vcc, s51, v104
	v_mul_f32_e32 v105, 0x4b800000, v104
	s_nop 0
	v_cndmask_b32_e32 v104, v104, v105, vcc
	v_rsq_f32_e32 v104, v104
	s_nop 0
	v_mul_f32_e32 v105, 0x45800000, v104
	v_cndmask_b32_e32 v168, v104, v105, vcc
	v_pk_mul_f32 v[10:11], v[10:11], v[168:169] op_sel_hi:[1,0]
	v_pk_mul_f32 v[4:5], v[4:5], v[168:169] op_sel_hi:[1,0]
	v_pk_mul_f32 v[2:3], v[2:3], v[168:169] op_sel_hi:[1,0]
	v_pk_mul_f32 v[116:117], v[116:117], v[168:169] op_sel_hi:[1,0]
	s_waitcnt vmcnt(19)
	v_pk_mul_f32 v[4:5], v[220:221], v[4:5]
	v_pk_mul_f32 v[10:11], v[222:223], v[10:11]
	global_load_dwordx4 v[220:223], v[90:91], off
	s_waitcnt vmcnt(18)
	v_pk_add_f32 v[104:105], v[230:231], 1.0 op_sel_hi:[1,0]
	v_pk_add_f32 v[106:107], v[228:229], 1.0 op_sel_hi:[1,0]
	global_load_dwordx4 v[228:231], v244, s[100:101]
	v_pk_fma_f32 v[104:105], v[104:105], v[10:11], v[226:227]
	v_pk_fma_f32 v[106:107], v[106:107], v[4:5], v[224:225]
	global_load_dwordx4 v[224:227], v244, s[98:99]
	v_max_f32_e64 v4, |v104|, |v105|
	v_max3_f32 v114, |v106|, |v107|, v4
	v_pk_mul_f32 v[4:5], v[6:7], v[168:169] op_sel_hi:[1,0]
	s_waitcnt vmcnt(19)
	v_pk_mul_f32 v[2:3], v[232:233], v[2:3]
	v_pk_mul_f32 v[4:5], v[234:235], v[4:5]
	global_load_dwordx4 v[232:235], v[92:93], off
	s_waitcnt vmcnt(18)
	v_pk_add_f32 v[6:7], v[254:255], 1.0 op_sel_hi:[1,0]
	v_pk_add_f32 v[10:11], v[252:253], 1.0 op_sel_hi:[1,0]
	global_load_dwordx4 v[252:255], v245, s[100:101]
	v_pk_fma_f32 v[108:109], v[6:7], v[4:5], v[238:239]
	v_pk_fma_f32 v[110:111], v[10:11], v[2:3], v[236:237]
	global_load_dwordx4 v[236:239], v245, s[98:99]
	v_max_f32_e64 v2, |v108|, |v109|
	v_max3_f32 v2, |v110|, |v111|, v2
	v_max3_f32 v122, v114, 0, v2
	v_pk_mul_f32 v[6:7], v[112:113], v[168:169] op_sel_hi:[1,0]
	v_pk_mul_f32 v[10:11], v[12:13], v[168:169] op_sel_hi:[1,0]
	s_waitcnt vmcnt(17)
	v_pk_mul_f32 v[4:5], v[182:183], v[6:7]
	v_pk_mul_f32 v[2:3], v[180:181], v[10:11]
	global_load_dwordx4 v[180:183], v[94:95], off
	s_waitcnt vmcnt(14)
	v_pk_add_f32 v[6:7], v[206:207], 1.0 op_sel_hi:[1,0]
	v_pk_add_f32 v[10:11], v[204:205], 1.0 op_sel_hi:[1,0]
	global_load_dwordx4 v[204:207], v246, s[100:101]
	v_pk_fma_f32 v[112:113], v[6:7], v[4:5], v[202:203]
	v_pk_fma_f32 v[114:115], v[10:11], v[2:3], v[200:201]
	global_load_dwordx4 v[200:203], v246, s[98:99]
	v_max_f32_e64 v2, |v112|, |v113|
	v_max3_f32 v123, |v114|, |v115|, v2
	v_pk_mul_f32 v[6:7], v[118:119], v[168:169] op_sel_hi:[1,0]
	s_waitcnt vmcnt(14)
	v_pk_mul_f32 v[2:3], v[208:209], v[116:117]
	v_pk_mul_f32 v[4:5], v[210:211], v[6:7]
	global_load_dwordx4 v[208:211], v[96:97], off
	s_waitcnt vmcnt(11)
	v_pk_add_f32 v[6:7], v[218:219], 1.0 op_sel_hi:[1,0]
	v_pk_add_f32 v[118:119], v[216:217], 1.0 op_sel_hi:[1,0]
	global_load_dwordx4 v[216:219], v247, s[100:101]
	v_pk_fma_f32 v[116:117], v[6:7], v[4:5], v[214:215]
	v_pk_fma_f32 v[118:119], v[118:119], v[2:3], v[212:213]
	global_load_dwordx4 v[212:215], v247, s[98:99]
	v_max_f32_e64 v2, |v116|, |v117|
	v_max3_f32 v2, |v118|, |v119|, v2
	v_max3_f32 v169, v122, v123, v2
	v_pk_mul_f32 v[6:7], v[120:121], v[168:169] op_sel_hi:[1,0]
	v_pk_mul_f32 v[8:9], v[8:9], v[168:169] op_sel_hi:[1,0]
	v_pk_mul_f32 v[126:127], v[126:127], v[168:169] op_sel_hi:[1,0]
	v_pk_mul_f32 v[124:125], v[124:125], v[168:169] op_sel_hi:[1,0]
	s_waitcnt vmcnt(11)
	v_pk_mul_f32 v[4:5], v[222:223], v[6:7]
	v_pk_mul_f32 v[2:3], v[220:221], v[8:9]
	s_waitcnt vmcnt(9)
	v_pk_add_f32 v[6:7], v[226:227], 1.0 op_sel_hi:[1,0]
	v_pk_add_f32 v[8:9], v[224:225], 1.0 op_sel_hi:[1,0]
	v_pk_fma_f32 v[120:121], v[6:7], v[4:5], v[230:231]
	v_pk_fma_f32 v[122:123], v[8:9], v[2:3], v[228:229]
	v_max_f32_e64 v2, |v120|, |v121|
	v_max3_f32 v170, |v122|, |v123|, v2
	s_waitcnt vmcnt(8)
	v_pk_mul_f32 v[4:5], v[126:127], v[234:235]
	v_pk_mul_f32 v[2:3], v[124:125], v[232:233]
	s_waitcnt vmcnt(6)
	v_pk_add_f32 v[12:13], v[238:239], 1.0 op_sel_hi:[1,0]
	v_pk_add_f32 v[10:11], v[236:237], 1.0 op_sel_hi:[1,0]
	v_pk_fma_f32 v[124:125], v[4:5], v[12:13], v[254:255]
	v_pk_fma_f32 v[126:127], v[2:3], v[10:11], v[252:253]
	v_max_f32_e64 v2, |v124|, |v125|
	v_max3_f32 v2, |v126|, |v127|, v2
	v_max3_f32 v169, v169, v170, v2
	v_pk_mul_f32 v[130:131], v[130:131], v[168:169] op_sel_hi:[1,0]
	v_pk_mul_f32 v[128:129], v[128:129], v[168:169] op_sel_hi:[1,0]
	v_pk_mul_f32 v[166:167], v[166:167], v[168:169] op_sel_hi:[1,0]
	v_pk_mul_f32 v[164:165], v[164:165], v[168:169] op_sel_hi:[1,0]
	s_waitcnt vmcnt(5)
	v_pk_mul_f32 v[4:5], v[130:131], v[182:183]
	v_pk_mul_f32 v[2:3], v[128:129], v[180:181]
	s_waitcnt vmcnt(3)
	v_pk_add_f32 v[12:13], v[202:203], 1.0 op_sel_hi:[1,0]
	v_pk_add_f32 v[10:11], v[200:201], 1.0 op_sel_hi:[1,0]
	v_pk_fma_f32 v[128:129], v[4:5], v[12:13], v[206:207]
	v_pk_fma_f32 v[130:131], v[2:3], v[10:11], v[204:205]
	v_max_f32_e64 v2, |v128|, |v129|
	v_max3_f32 v170, |v130|, |v131|, v2
	s_waitcnt vmcnt(2)
	v_pk_mul_f32 v[8:9], v[166:167], v[210:211]
	v_pk_mul_f32 v[6:7], v[164:165], v[208:209]
	s_waitcnt vmcnt(0)
	v_pk_add_f32 v[12:13], v[214:215], 1.0 op_sel_hi:[1,0]
	v_pk_add_f32 v[10:11], v[212:213], 1.0 op_sel_hi:[1,0]
	v_pk_fma_f32 v[4:5], v[8:9], v[12:13], v[218:219]
	v_pk_fma_f32 v[6:7], v[6:7], v[10:11], v[216:217]
	v_max_f32_e64 v2, |v4|, |v5|
	v_max3_f32 v2, |v6|, |v7|, v2
	v_max3_f32 v2, v169, v170, v2
	ds_bpermute_b32 v3, v1, v2
	s_waitcnt lgkmcnt(0)
	v_max_f32_e32 v3, v3, v3
	v_max_f32_e32 v2, v2, v3
	ds_bpermute_b32 v3, v15, v2
	s_waitcnt lgkmcnt(0)
	v_max_f32_e32 v3, v3, v3
	v_max_f32_e32 v2, v2, v3
	ds_bpermute_b32 v3, v186, v2
	s_waitcnt lgkmcnt(0)
	v_max_f32_e32 v3, v3, v3
	v_max_f32_e32 v2, v2, v3
	ds_bpermute_b32 v3, v187, v2
	s_waitcnt lgkmcnt(0)
	v_max_f32_e32 v3, v3, v3
	v_max_f32_e32 v2, v2, v3
	ds_bpermute_b32 v3, v188, v2
	s_waitcnt lgkmcnt(0)
	v_max_f32_e32 v3, v3, v3
	v_max_f32_e32 v2, v2, v3
	ds_bpermute_b32 v3, v189, v2
	s_and_saveexec_b64 s[22:23], s[4:5]
	s_cbranch_execz .LBB0_3201
	s_waitcnt lgkmcnt(0)
	v_max_f32_e32 v3, v3, v3
	v_max_f32_e32 v2, v2, v2
	s_lshl_b64 s[24:25], s[18:19], 2
	v_max_f32_e32 v2, v2, v3
	s_add_u32 s24, s35, s24
	v_mul_f32_e32 v2, 0x3c010204, v2
	s_addc_u32 s25, s38, s25
	global_store_dword v17, v2, s[24:25]

.LBB0_3203:
	ds_read_b128 v[8:11], v190
	v_mov_b32_e32 v12, v132
	v_mov_b32_e32 v13, v106
	v_mov_b32_e32 v106, v133
	v_mov_b32_e32 v132, v134
	s_waitcnt lgkmcnt(0)
	v_pk_fma_f32 v[2:3], v[12:13], v[8:9], 0 op_sel_hi:[1,0,0]
	v_mov_b32_e32 v133, v104
	v_pk_fma_f32 v[2:3], v[106:107], v[8:9], v[2:3] op_sel:[0,1,0]
	v_mov_b32_e32 v104, v135
	v_pk_fma_f32 v[2:3], v[132:133], v[10:11], v[2:3] op_sel_hi:[1,0,1]
	v_mov_b32_e32 v8, v11
	v_pk_fma_f32 v[2:3], v[104:105], v[8:9], v[2:3] op_sel_hi:[1,0,1]
	ds_read_b128 v[8:11], v190 offset:1024
	v_mov_b32_e32 v134, v136
	v_mov_b32_e32 v135, v110
	v_mov_b32_e32 v110, v137
	v_mov_b32_e32 v136, v138
	s_waitcnt lgkmcnt(0)
	v_pk_fma_f32 v[2:3], v[134:135], v[8:9], v[2:3] op_sel_hi:[1,0,1]
	v_mov_b32_e32 v137, v108
	v_pk_fma_f32 v[2:3], v[110:111], v[8:9], v[2:3] op_sel:[0,1,0]
	v_mov_b32_e32 v108, v139
	v_pk_fma_f32 v[2:3], v[136:137], v[10:11], v[2:3] op_sel_hi:[1,0,1]
	v_mov_b32_e32 v8, v11
	v_pk_fma_f32 v[2:3], v[108:109], v[8:9], v[2:3] op_sel_hi:[1,0,1]
	ds_read_b128 v[8:11], v190 offset:2048
	v_mov_b32_e32 v138, v140
	v_mov_b32_e32 v139, v114
	v_mov_b32_e32 v114, v141
	v_mov_b32_e32 v140, v142
	s_waitcnt lgkmcnt(0)
	v_pk_fma_f32 v[2:3], v[138:139], v[8:9], v[2:3] op_sel_hi:[1,0,1]
	v_mov_b32_e32 v141, v112
	v_pk_fma_f32 v[2:3], v[114:115], v[8:9], v[2:3] op_sel:[0,1,0]
	v_mov_b32_e32 v112, v143
	v_pk_fma_f32 v[2:3], v[140:141], v[10:11], v[2:3] op_sel_hi:[1,0,1]
	v_mov_b32_e32 v8, v11
	v_pk_fma_f32 v[2:3], v[112:113], v[8:9], v[2:3] op_sel_hi:[1,0,1]
	ds_read_b128 v[8:11], v190 offset:3072
	v_mov_b32_e32 v142, v144
	v_mov_b32_e32 v143, v118
	v_mov_b32_e32 v118, v145
	v_mov_b32_e32 v144, v146
	s_waitcnt lgkmcnt(0)
	v_pk_fma_f32 v[2:3], v[142:143], v[8:9], v[2:3] op_sel_hi:[1,0,1]
	v_mov_b32_e32 v145, v116
	v_pk_fma_f32 v[2:3], v[118:119], v[8:9], v[2:3] op_sel:[0,1,0]
	v_mov_b32_e32 v116, v147
	v_pk_fma_f32 v[2:3], v[144:145], v[10:11], v[2:3] op_sel_hi:[1,0,1]
	v_mov_b32_e32 v8, v11
	v_pk_fma_f32 v[2:3], v[116:117], v[8:9], v[2:3] op_sel_hi:[1,0,1]
	ds_read_b128 v[8:11], v190 offset:4096
	v_mov_b32_e32 v146, v148
	v_mov_b32_e32 v147, v122
	v_mov_b32_e32 v122, v149
	v_mov_b32_e32 v148, v150
	s_waitcnt lgkmcnt(0)
	v_pk_fma_f32 v[2:3], v[146:147], v[8:9], v[2:3] op_sel_hi:[1,0,1]
	v_mov_b32_e32 v149, v120
	v_pk_fma_f32 v[2:3], v[122:123], v[8:9], v[2:3] op_sel:[0,1,0]
	v_mov_b32_e32 v120, v151
	v_pk_fma_f32 v[2:3], v[148:149], v[10:11], v[2:3] op_sel_hi:[1,0,1]
	v_mov_b32_e32 v8, v11
	v_pk_fma_f32 v[2:3], v[120:121], v[8:9], v[2:3] op_sel_hi:[1,0,1]
	ds_read_b128 v[8:11], v190 offset:5120
	v_mov_b32_e32 v150, v152
	v_mov_b32_e32 v151, v126
	v_mov_b32_e32 v126, v153
	v_mov_b32_e32 v152, v154
	s_waitcnt lgkmcnt(0)
	v_pk_fma_f32 v[2:3], v[150:151], v[8:9], v[2:3] op_sel_hi:[1,0,1]
	v_mov_b32_e32 v153, v124
	v_pk_fma_f32 v[2:3], v[126:127], v[8:9], v[2:3] op_sel:[0,1,0]
	v_mov_b32_e32 v124, v155
	v_pk_fma_f32 v[2:3], v[152:153], v[10:11], v[2:3] op_sel_hi:[1,0,1]
	v_mov_b32_e32 v8, v11
	v_pk_fma_f32 v[2:3], v[124:125], v[8:9], v[2:3] op_sel_hi:[1,0,1]
	ds_read_b128 v[8:11], v190 offset:6144
	v_mov_b32_e32 v154, v156
	v_mov_b32_e32 v155, v130
	v_mov_b32_e32 v130, v157
	v_mov_b32_e32 v156, v158
	s_waitcnt lgkmcnt(0)
	v_pk_fma_f32 v[2:3], v[154:155], v[8:9], v[2:3] op_sel_hi:[1,0,1]
	v_mov_b32_e32 v157, v128
	v_pk_fma_f32 v[2:3], v[130:131], v[8:9], v[2:3] op_sel:[0,1,0]
	v_mov_b32_e32 v128, v159
	v_pk_fma_f32 v[2:3], v[156:157], v[10:11], v[2:3] op_sel_hi:[1,0,1]
	v_mov_b32_e32 v8, v11
	v_pk_fma_f32 v[2:3], v[128:129], v[8:9], v[2:3] op_sel_hi:[1,0,1]
	ds_read_b128 v[8:11], v190 offset:7168
	v_mov_b32_e32 v158, v160
	v_mov_b32_e32 v159, v6
	v_mov_b32_e32 v6, v161
	v_mov_b32_e32 v160, v162
	s_waitcnt lgkmcnt(0)
	v_pk_fma_f32 v[2:3], v[158:159], v[8:9], v[2:3] op_sel_hi:[1,0,1]
	v_mov_b32_e32 v161, v4
	v_pk_fma_f32 v[2:3], v[6:7], v[8:9], v[2:3] op_sel:[0,1,0]
	v_mov_b32_e32 v4, v163
	v_pk_fma_f32 v[2:3], v[160:161], v[10:11], v[2:3] op_sel_hi:[1,0,1]
	v_mov_b32_e32 v8, v11
	v_pk_fma_f32 v[2:3], v[4:5], v[8:9], v[2:3] op_sel_hi:[1,0,1]
	s_nop 0
	ds_read_b128 v[8:11], v190 offset:8208
	s_waitcnt lgkmcnt(0)
	v_pk_fma_f32 v[162:163], v[12:13], v[8:9], 0 op_sel_hi:[1,0,0]
	s_nop 0
	v_pk_fma_f32 v[8:9], v[106:107], v[8:9], v[162:163] op_sel:[0,1,0]
	s_nop 0
	v_pk_fma_f32 v[8:9], v[132:133], v[10:11], v[8:9] op_sel_hi:[1,0,1]
	v_mov_b32_e32 v10, v11
	v_pk_fma_f32 v[162:163], v[104:105], v[10:11], v[8:9] op_sel_hi:[1,0,1]
	ds_read_b128 v[8:11], v190 offset:9232
	s_waitcnt lgkmcnt(0)
	v_pk_fma_f32 v[162:163], v[134:135], v[8:9], v[162:163] op_sel_hi:[1,0,1]
	s_nop 0
	v_pk_fma_f32 v[8:9], v[110:111], v[8:9], v[162:163] op_sel:[0,1,0]
	s_nop 0
	v_pk_fma_f32 v[8:9], v[136:137], v[10:11], v[8:9] op_sel_hi:[1,0,1]
	v_mov_b32_e32 v10, v11
	v_pk_fma_f32 v[162:163], v[108:109], v[10:11], v[8:9] op_sel_hi:[1,0,1]
	ds_read_b128 v[8:11], v190 offset:10256
	s_waitcnt lgkmcnt(0)
	v_pk_fma_f32 v[162:163], v[138:139], v[8:9], v[162:163] op_sel_hi:[1,0,1]
	s_nop 0
	v_pk_fma_f32 v[8:9], v[114:115], v[8:9], v[162:163] op_sel:[0,1,0]
	s_nop 0
	v_pk_fma_f32 v[8:9], v[140:141], v[10:11], v[8:9] op_sel_hi:[1,0,1]
	v_mov_b32_e32 v10, v11
	v_pk_fma_f32 v[162:163], v[112:113], v[10:11], v[8:9] op_sel_hi:[1,0,1]
	ds_read_b128 v[8:11], v190 offset:11280
	s_waitcnt lgkmcnt(0)
	v_pk_fma_f32 v[162:163], v[142:143], v[8:9], v[162:163] op_sel_hi:[1,0,1]
	s_nop 0
	v_pk_fma_f32 v[8:9], v[118:119], v[8:9], v[162:163] op_sel:[0,1,0]
	s_nop 0
	v_pk_fma_f32 v[8:9], v[144:145], v[10:11], v[8:9] op_sel_hi:[1,0,1]
	v_mov_b32_e32 v10, v11
	v_pk_fma_f32 v[162:163], v[116:117], v[10:11], v[8:9] op_sel_hi:[1,0,1]
	ds_read_b128 v[8:11], v190 offset:12304
	s_waitcnt lgkmcnt(0)
	v_pk_fma_f32 v[162:163], v[146:147], v[8:9], v[162:163] op_sel_hi:[1,0,1]
	s_nop 0
	v_pk_fma_f32 v[8:9], v[122:123], v[8:9], v[162:163] op_sel:[0,1,0]
	s_nop 0
	v_pk_fma_f32 v[8:9], v[148:149], v[10:11], v[8:9] op_sel_hi:[1,0,1]
	v_mov_b32_e32 v10, v11
	v_pk_fma_f32 v[162:163], v[120:121], v[10:11], v[8:9] op_sel_hi:[1,0,1]
	ds_read_b128 v[8:11], v190 offset:13328
	s_waitcnt lgkmcnt(0)
	v_pk_fma_f32 v[162:163], v[150:151], v[8:9], v[162:163] op_sel_hi:[1,0,1]
	s_nop 0
	v_pk_fma_f32 v[8:9], v[126:127], v[8:9], v[162:163] op_sel:[0,1,0]
	s_nop 0
	v_pk_fma_f32 v[8:9], v[152:153], v[10:11], v[8:9] op_sel_hi:[1,0,1]
	v_mov_b32_e32 v10, v11
	v_pk_fma_f32 v[162:163], v[124:125], v[10:11], v[8:9] op_sel_hi:[1,0,1]
	ds_read_b128 v[8:11], v190 offset:14352
	s_waitcnt lgkmcnt(0)
	v_pk_fma_f32 v[162:163], v[154:155], v[8:9], v[162:163] op_sel_hi:[1,0,1]
	s_nop 0
	v_pk_fma_f32 v[8:9], v[130:131], v[8:9], v[162:163] op_sel:[0,1,0]
	s_nop 0
	v_pk_fma_f32 v[8:9], v[156:157], v[10:11], v[8:9] op_sel_hi:[1,0,1]
	v_mov_b32_e32 v10, v11
	v_pk_fma_f32 v[162:163], v[128:129], v[10:11], v[8:9] op_sel_hi:[1,0,1]
	ds_read_b128 v[8:11], v190 offset:15376
	s_waitcnt lgkmcnt(0)
	v_pk_fma_f32 v[162:163], v[158:159], v[8:9], v[162:163] op_sel_hi:[1,0,1]
	s_nop 0
	v_pk_fma_f32 v[8:9], v[6:7], v[8:9], v[162:163] op_sel:[0,1,0]
	s_nop 0
	v_pk_fma_f32 v[8:9], v[160:161], v[10:11], v[8:9] op_sel_hi:[1,0,1]
	v_mov_b32_e32 v10, v11
	v_pk_fma_f32 v[8:9], v[4:5], v[10:11], v[8:9] op_sel_hi:[1,0,1]
	s_nop 0
	ds_read_b128 v[162:165], v190 offset:16416
	s_waitcnt lgkmcnt(0)
	v_pk_fma_f32 v[10:11], v[12:13], v[162:163], 0 op_sel_hi:[1,0,0]
	s_nop 0
	v_pk_fma_f32 v[10:11], v[106:107], v[162:163], v[10:11] op_sel:[0,1,0]
	v_mov_b32_e32 v162, v165
	v_pk_fma_f32 v[10:11], v[132:133], v[164:165], v[10:11] op_sel_hi:[1,0,1]
	s_nop 0
	v_pk_fma_f32 v[10:11], v[104:105], v[162:163], v[10:11] op_sel_hi:[1,0,1]
	ds_read_b128 v[162:165], v190 offset:17440
	s_waitcnt lgkmcnt(0)
	v_pk_fma_f32 v[10:11], v[134:135], v[162:163], v[10:11] op_sel_hi:[1,0,1]
	s_nop 0
	v_pk_fma_f32 v[10:11], v[110:111], v[162:163], v[10:11] op_sel:[0,1,0]
	v_mov_b32_e32 v162, v165
	v_pk_fma_f32 v[10:11], v[136:137], v[164:165], v[10:11] op_sel_hi:[1,0,1]
	s_nop 0
	v_pk_fma_f32 v[10:11], v[108:109], v[162:163], v[10:11] op_sel_hi:[1,0,1]
	ds_read_b128 v[162:165], v190 offset:18464
	s_waitcnt lgkmcnt(0)
	v_pk_fma_f32 v[10:11], v[138:139], v[162:163], v[10:11] op_sel_hi:[1,0,1]
	s_nop 0
	v_pk_fma_f32 v[10:11], v[114:115], v[162:163], v[10:11] op_sel:[0,1,0]
	v_mov_b32_e32 v162, v165
	v_pk_fma_f32 v[10:11], v[140:141], v[164:165], v[10:11] op_sel_hi:[1,0,1]
	s_nop 0
	v_pk_fma_f32 v[10:11], v[112:113], v[162:163], v[10:11] op_sel_hi:[1,0,1]
	ds_read_b128 v[162:165], v190 offset:19488
	s_waitcnt lgkmcnt(0)
	v_pk_fma_f32 v[10:11], v[142:143], v[162:163], v[10:11] op_sel_hi:[1,0,1]
	s_nop 0
	v_pk_fma_f32 v[10:11], v[118:119], v[162:163], v[10:11] op_sel:[0,1,0]
	v_mov_b32_e32 v162, v165
	v_pk_fma_f32 v[10:11], v[144:145], v[164:165], v[10:11] op_sel_hi:[1,0,1]
	s_nop 0
	v_pk_fma_f32 v[10:11], v[116:117], v[162:163], v[10:11] op_sel_hi:[1,0,1]
	ds_read_b128 v[162:165], v190 offset:20512
	s_waitcnt lgkmcnt(0)
	v_pk_fma_f32 v[10:11], v[146:147], v[162:163], v[10:11] op_sel_hi:[1,0,1]
	s_nop 0
	v_pk_fma_f32 v[10:11], v[122:123], v[162:163], v[10:11] op_sel:[0,1,0]
	v_mov_b32_e32 v162, v165
	v_pk_fma_f32 v[10:11], v[148:149], v[164:165], v[10:11] op_sel_hi:[1,0,1]
	s_nop 0
	v_pk_fma_f32 v[10:11], v[120:121], v[162:163], v[10:11] op_sel_hi:[1,0,1]
	ds_read_b128 v[162:165], v190 offset:21536
	s_waitcnt lgkmcnt(0)
	v_pk_fma_f32 v[10:11], v[150:151], v[162:163], v[10:11] op_sel_hi:[1,0,1]
	s_nop 0
	v_pk_fma_f32 v[10:11], v[126:127], v[162:163], v[10:11] op_sel:[0,1,0]
	v_mov_b32_e32 v162, v165
	v_pk_fma_f32 v[10:11], v[152:153], v[164:165], v[10:11] op_sel_hi:[1,0,1]
	s_nop 0
	v_pk_fma_f32 v[10:11], v[124:125], v[162:163], v[10:11] op_sel_hi:[1,0,1]
	ds_read_b128 v[162:165], v190 offset:22560
	s_waitcnt lgkmcnt(0)
	v_pk_fma_f32 v[10:11], v[154:155], v[162:163], v[10:11] op_sel_hi:[1,0,1]
	s_nop 0
	v_pk_fma_f32 v[10:11], v[130:131], v[162:163], v[10:11] op_sel:[0,1,0]
	v_mov_b32_e32 v162, v165
	v_pk_fma_f32 v[10:11], v[156:157], v[164:165], v[10:11] op_sel_hi:[1,0,1]
	s_nop 0
	v_pk_fma_f32 v[10:11], v[128:129], v[162:163], v[10:11] op_sel_hi:[1,0,1]
	ds_read_b128 v[162:165], v190 offset:23584
	s_waitcnt lgkmcnt(0)
	v_pk_fma_f32 v[10:11], v[158:159], v[162:163], v[10:11] op_sel_hi:[1,0,1]
	s_nop 0
	v_pk_fma_f32 v[10:11], v[6:7], v[162:163], v[10:11] op_sel:[0,1,0]
	v_mov_b32_e32 v162, v165
	v_pk_fma_f32 v[10:11], v[160:161], v[164:165], v[10:11] op_sel_hi:[1,0,1]
	s_nop 0
	v_pk_fma_f32 v[10:11], v[4:5], v[162:163], v[10:11] op_sel_hi:[1,0,1]
	s_nop 0
	ds_read_b128 v[162:165], v190 offset:24624
	s_waitcnt lgkmcnt(0)
	v_pk_fma_f32 v[166:167], v[12:13], v[162:163], 0 op_sel_hi:[1,0,0]
	s_nop 0
	v_pk_fma_f32 v[162:163], v[106:107], v[162:163], v[166:167] op_sel:[0,1,0]
	s_nop 0
	v_pk_fma_f32 v[162:163], v[132:133], v[164:165], v[162:163] op_sel_hi:[1,0,1]
	v_mov_b32_e32 v164, v165
	v_pk_fma_f32 v[166:167], v[104:105], v[164:165], v[162:163] op_sel_hi:[1,0,1]
	ds_read_b128 v[162:165], v190 offset:25648
	s_waitcnt lgkmcnt(0)
	v_pk_fma_f32 v[166:167], v[134:135], v[162:163], v[166:167] op_sel_hi:[1,0,1]
	s_nop 0
	v_pk_fma_f32 v[162:163], v[110:111], v[162:163], v[166:167] op_sel:[0,1,0]
	s_nop 0
	v_pk_fma_f32 v[162:163], v[136:137], v[164:165], v[162:163] op_sel_hi:[1,0,1]
	v_mov_b32_e32 v164, v165
	v_pk_fma_f32 v[166:167], v[108:109], v[164:165], v[162:163] op_sel_hi:[1,0,1]
	ds_read_b128 v[162:165], v190 offset:26672
	s_waitcnt lgkmcnt(0)
	v_pk_fma_f32 v[166:167], v[138:139], v[162:163], v[166:167] op_sel_hi:[1,0,1]
	s_nop 0
	v_pk_fma_f32 v[162:163], v[114:115], v[162:163], v[166:167] op_sel:[0,1,0]
	s_nop 0
	v_pk_fma_f32 v[162:163], v[140:141], v[164:165], v[162:163] op_sel_hi:[1,0,1]
	v_mov_b32_e32 v164, v165
	v_pk_fma_f32 v[166:167], v[112:113], v[164:165], v[162:163] op_sel_hi:[1,0,1]
	ds_read_b128 v[162:165], v190 offset:27696
	s_waitcnt lgkmcnt(0)
	v_pk_fma_f32 v[166:167], v[142:143], v[162:163], v[166:167] op_sel_hi:[1,0,1]
	s_nop 0
	v_pk_fma_f32 v[162:163], v[118:119], v[162:163], v[166:167] op_sel:[0,1,0]
	s_nop 0
	v_pk_fma_f32 v[162:163], v[144:145], v[164:165], v[162:163] op_sel_hi:[1,0,1]
	v_mov_b32_e32 v164, v165
	v_pk_fma_f32 v[166:167], v[116:117], v[164:165], v[162:163] op_sel_hi:[1,0,1]
	ds_read_b128 v[162:165], v190 offset:28720
	s_waitcnt lgkmcnt(0)
	v_pk_fma_f32 v[166:167], v[146:147], v[162:163], v[166:167] op_sel_hi:[1,0,1]
	s_nop 0
	v_pk_fma_f32 v[162:163], v[122:123], v[162:163], v[166:167] op_sel:[0,1,0]
	s_nop 0
	v_pk_fma_f32 v[162:163], v[148:149], v[164:165], v[162:163] op_sel_hi:[1,0,1]
	v_mov_b32_e32 v164, v165
	v_pk_fma_f32 v[166:167], v[120:121], v[164:165], v[162:163] op_sel_hi:[1,0,1]
	ds_read_b128 v[162:165], v190 offset:29744
	s_waitcnt lgkmcnt(0)
	v_pk_fma_f32 v[166:167], v[150:151], v[162:163], v[166:167] op_sel_hi:[1,0,1]
	s_nop 0
	v_pk_fma_f32 v[162:163], v[126:127], v[162:163], v[166:167] op_sel:[0,1,0]
	s_nop 0
	v_pk_fma_f32 v[162:163], v[152:153], v[164:165], v[162:163] op_sel_hi:[1,0,1]
	v_mov_b32_e32 v164, v165
	v_pk_fma_f32 v[166:167], v[124:125], v[164:165], v[162:163] op_sel_hi:[1,0,1]
	ds_read_b128 v[162:165], v190 offset:30768
	s_waitcnt lgkmcnt(0)
	v_pk_fma_f32 v[166:167], v[154:155], v[162:163], v[166:167] op_sel_hi:[1,0,1]
	s_nop 0
	v_pk_fma_f32 v[162:163], v[130:131], v[162:163], v[166:167] op_sel:[0,1,0]
	s_nop 0
	v_pk_fma_f32 v[162:163], v[156:157], v[164:165], v[162:163] op_sel_hi:[1,0,1]
	v_mov_b32_e32 v164, v165
	v_pk_fma_f32 v[166:167], v[128:129], v[164:165], v[162:163] op_sel_hi:[1,0,1]
	ds_read_b128 v[162:165], v190 offset:31792
	s_waitcnt lgkmcnt(0)
	v_pk_fma_f32 v[166:167], v[158:159], v[162:163], v[166:167] op_sel_hi:[1,0,1]
	s_nop 0
	v_pk_fma_f32 v[162:163], v[6:7], v[162:163], v[166:167] op_sel:[0,1,0]
	s_nop 0
	v_pk_fma_f32 v[162:163], v[160:161], v[164:165], v[162:163] op_sel_hi:[1,0,1]
	v_mov_b32_e32 v164, v165
	v_pk_fma_f32 v[162:163], v[4:5], v[164:165], v[162:163] op_sel_hi:[1,0,1]
	s_nop 0
	ds_read_b128 v[164:167], v190 offset:32832
	s_waitcnt lgkmcnt(0)
	v_pk_fma_f32 v[168:169], v[12:13], v[164:165], 0 op_sel_hi:[1,0,0]
	s_nop 0
	v_pk_fma_f32 v[164:165], v[106:107], v[164:165], v[168:169] op_sel:[0,1,0]
	s_nop 0
	v_pk_fma_f32 v[164:165], v[132:133], v[166:167], v[164:165] op_sel_hi:[1,0,1]
	v_mov_b32_e32 v166, v167
	v_pk_fma_f32 v[168:169], v[104:105], v[166:167], v[164:165] op_sel_hi:[1,0,1]
	ds_read_b128 v[164:167], v190 offset:33856
	s_waitcnt lgkmcnt(0)
	v_pk_fma_f32 v[168:169], v[134:135], v[164:165], v[168:169] op_sel_hi:[1,0,1]
	s_nop 0
	v_pk_fma_f32 v[164:165], v[110:111], v[164:165], v[168:169] op_sel:[0,1,0]
	s_nop 0
	v_pk_fma_f32 v[164:165], v[136:137], v[166:167], v[164:165] op_sel_hi:[1,0,1]
	v_mov_b32_e32 v166, v167
	v_pk_fma_f32 v[168:169], v[108:109], v[166:167], v[164:165] op_sel_hi:[1,0,1]
	ds_read_b128 v[164:167], v190 offset:34880
	s_waitcnt lgkmcnt(0)
	v_pk_fma_f32 v[168:169], v[138:139], v[164:165], v[168:169] op_sel_hi:[1,0,1]
	s_nop 0
	v_pk_fma_f32 v[164:165], v[114:115], v[164:165], v[168:169] op_sel:[0,1,0]
	s_nop 0
	v_pk_fma_f32 v[164:165], v[140:141], v[166:167], v[164:165] op_sel_hi:[1,0,1]
	v_mov_b32_e32 v166, v167
	v_pk_fma_f32 v[168:169], v[112:113], v[166:167], v[164:165] op_sel_hi:[1,0,1]
	ds_read_b128 v[164:167], v190 offset:35904
	s_waitcnt lgkmcnt(0)
	v_pk_fma_f32 v[168:169], v[142:143], v[164:165], v[168:169] op_sel_hi:[1,0,1]
	s_nop 0
	v_pk_fma_f32 v[164:165], v[118:119], v[164:165], v[168:169] op_sel:[0,1,0]
	s_nop 0
	v_pk_fma_f32 v[164:165], v[144:145], v[166:167], v[164:165] op_sel_hi:[1,0,1]
	v_mov_b32_e32 v166, v167
	v_pk_fma_f32 v[168:169], v[116:117], v[166:167], v[164:165] op_sel_hi:[1,0,1]
	ds_read_b128 v[164:167], v190 offset:36928
	s_waitcnt lgkmcnt(0)
	v_pk_fma_f32 v[168:169], v[146:147], v[164:165], v[168:169] op_sel_hi:[1,0,1]
	s_nop 0
	v_pk_fma_f32 v[164:165], v[122:123], v[164:165], v[168:169] op_sel:[0,1,0]
	s_nop 0
	v_pk_fma_f32 v[164:165], v[148:149], v[166:167], v[164:165] op_sel_hi:[1,0,1]
	v_mov_b32_e32 v166, v167
	v_pk_fma_f32 v[168:169], v[120:121], v[166:167], v[164:165] op_sel_hi:[1,0,1]
	ds_read_b128 v[164:167], v190 offset:37952
	s_waitcnt lgkmcnt(0)
	v_pk_fma_f32 v[168:169], v[150:151], v[164:165], v[168:169] op_sel_hi:[1,0,1]
	s_nop 0
	v_pk_fma_f32 v[164:165], v[126:127], v[164:165], v[168:169] op_sel:[0,1,0]
	s_nop 0
	v_pk_fma_f32 v[164:165], v[152:153], v[166:167], v[164:165] op_sel_hi:[1,0,1]
	v_mov_b32_e32 v166, v167
	v_pk_fma_f32 v[168:169], v[124:125], v[166:167], v[164:165] op_sel_hi:[1,0,1]
	ds_read_b128 v[164:167], v190 offset:38976
	s_waitcnt lgkmcnt(0)
	v_pk_fma_f32 v[168:169], v[154:155], v[164:165], v[168:169] op_sel_hi:[1,0,1]
	s_nop 0
	v_pk_fma_f32 v[164:165], v[130:131], v[164:165], v[168:169] op_sel:[0,1,0]
	s_nop 0
	v_pk_fma_f32 v[164:165], v[156:157], v[166:167], v[164:165] op_sel_hi:[1,0,1]
	v_mov_b32_e32 v166, v167
	v_pk_fma_f32 v[168:169], v[128:129], v[166:167], v[164:165] op_sel_hi:[1,0,1]
	ds_read_b128 v[164:167], v190 offset:40000
	s_waitcnt lgkmcnt(0)
	v_pk_fma_f32 v[168:169], v[158:159], v[164:165], v[168:169] op_sel_hi:[1,0,1]
	s_nop 0
	v_pk_fma_f32 v[164:165], v[6:7], v[164:165], v[168:169] op_sel:[0,1,0]
	s_nop 0
	v_pk_fma_f32 v[164:165], v[160:161], v[166:167], v[164:165] op_sel_hi:[1,0,1]
	v_mov_b32_e32 v166, v167
	v_pk_fma_f32 v[164:165], v[4:5], v[166:167], v[164:165] op_sel_hi:[1,0,1]
	s_nop 0
	ds_read_b128 v[166:169], v190 offset:41040
	s_waitcnt lgkmcnt(0)
	v_pk_fma_f32 v[170:171], v[12:13], v[166:167], 0 op_sel_hi:[1,0,0]
	s_nop 0
	v_pk_fma_f32 v[166:167], v[106:107], v[166:167], v[170:171] op_sel:[0,1,0]
	s_nop 0
	v_pk_fma_f32 v[166:167], v[132:133], v[168:169], v[166:167] op_sel_hi:[1,0,1]
	v_mov_b32_e32 v168, v169
	v_pk_fma_f32 v[170:171], v[104:105], v[168:169], v[166:167] op_sel_hi:[1,0,1]
	ds_read_b128 v[166:169], v190 offset:42064
	s_waitcnt lgkmcnt(0)
	v_pk_fma_f32 v[170:171], v[134:135], v[166:167], v[170:171] op_sel_hi:[1,0,1]
	s_nop 0
	v_pk_fma_f32 v[166:167], v[110:111], v[166:167], v[170:171] op_sel:[0,1,0]
	s_nop 0
	v_pk_fma_f32 v[166:167], v[136:137], v[168:169], v[166:167] op_sel_hi:[1,0,1]
	v_mov_b32_e32 v168, v169
	v_pk_fma_f32 v[170:171], v[108:109], v[168:169], v[166:167] op_sel_hi:[1,0,1]
	ds_read_b128 v[166:169], v190 offset:43088
	s_waitcnt lgkmcnt(0)
	v_pk_fma_f32 v[170:171], v[138:139], v[166:167], v[170:171] op_sel_hi:[1,0,1]
	s_nop 0
	v_pk_fma_f32 v[166:167], v[114:115], v[166:167], v[170:171] op_sel:[0,1,0]
	s_nop 0
	v_pk_fma_f32 v[166:167], v[140:141], v[168:169], v[166:167] op_sel_hi:[1,0,1]
	v_mov_b32_e32 v168, v169
	v_pk_fma_f32 v[170:171], v[112:113], v[168:169], v[166:167] op_sel_hi:[1,0,1]
	ds_read_b128 v[166:169], v190 offset:44112
	s_waitcnt lgkmcnt(0)
	v_pk_fma_f32 v[170:171], v[142:143], v[166:167], v[170:171] op_sel_hi:[1,0,1]
	s_nop 0
	v_pk_fma_f32 v[166:167], v[118:119], v[166:167], v[170:171] op_sel:[0,1,0]
	s_nop 0
	v_pk_fma_f32 v[166:167], v[144:145], v[168:169], v[166:167] op_sel_hi:[1,0,1]
	v_mov_b32_e32 v168, v169
	v_pk_fma_f32 v[170:171], v[116:117], v[168:169], v[166:167] op_sel_hi:[1,0,1]
	ds_read_b128 v[166:169], v190 offset:45136
	s_waitcnt lgkmcnt(0)
	v_pk_fma_f32 v[170:171], v[146:147], v[166:167], v[170:171] op_sel_hi:[1,0,1]
	s_nop 0
	v_pk_fma_f32 v[166:167], v[122:123], v[166:167], v[170:171] op_sel:[0,1,0]
	s_nop 0
	v_pk_fma_f32 v[166:167], v[148:149], v[168:169], v[166:167] op_sel_hi:[1,0,1]
	v_mov_b32_e32 v168, v169
	v_pk_fma_f32 v[170:171], v[120:121], v[168:169], v[166:167] op_sel_hi:[1,0,1]
	ds_read_b128 v[166:169], v190 offset:46160
	s_waitcnt lgkmcnt(0)
	v_pk_fma_f32 v[170:171], v[150:151], v[166:167], v[170:171] op_sel_hi:[1,0,1]
	s_nop 0
	v_pk_fma_f32 v[166:167], v[126:127], v[166:167], v[170:171] op_sel:[0,1,0]
	s_nop 0
	v_pk_fma_f32 v[166:167], v[152:153], v[168:169], v[166:167] op_sel_hi:[1,0,1]
	v_mov_b32_e32 v168, v169
	v_pk_fma_f32 v[170:171], v[124:125], v[168:169], v[166:167] op_sel_hi:[1,0,1]
	ds_read_b128 v[166:169], v190 offset:47184
	s_waitcnt lgkmcnt(0)
	v_pk_fma_f32 v[170:171], v[154:155], v[166:167], v[170:171] op_sel_hi:[1,0,1]
	s_nop 0
	v_pk_fma_f32 v[166:167], v[130:131], v[166:167], v[170:171] op_sel:[0,1,0]
	s_nop 0
	v_pk_fma_f32 v[166:167], v[156:157], v[168:169], v[166:167] op_sel_hi:[1,0,1]
	v_mov_b32_e32 v168, v169
	v_pk_fma_f32 v[170:171], v[128:129], v[168:169], v[166:167] op_sel_hi:[1,0,1]
	ds_read_b128 v[166:169], v190 offset:48208
	s_waitcnt lgkmcnt(0)
	v_pk_fma_f32 v[170:171], v[158:159], v[166:167], v[170:171] op_sel_hi:[1,0,1]
	s_nop 0
	v_pk_fma_f32 v[166:167], v[6:7], v[166:167], v[170:171] op_sel:[0,1,0]
	s_nop 0
	v_pk_fma_f32 v[166:167], v[160:161], v[168:169], v[166:167] op_sel_hi:[1,0,1]
	v_mov_b32_e32 v168, v169
	v_pk_fma_f32 v[166:167], v[4:5], v[168:169], v[166:167] op_sel_hi:[1,0,1]
	s_nop 0
	ds_read_b128 v[168:171], v190 offset:49248
	s_waitcnt lgkmcnt(0)
	v_pk_fma_f32 v[172:173], v[12:13], v[168:169], 0 op_sel_hi:[1,0,0]
	s_nop 0
	v_pk_fma_f32 v[168:169], v[106:107], v[168:169], v[172:173] op_sel:[0,1,0]
	s_nop 0
	v_pk_fma_f32 v[168:169], v[132:133], v[170:171], v[168:169] op_sel_hi:[1,0,1]
	v_mov_b32_e32 v170, v171
	v_pk_fma_f32 v[172:173], v[104:105], v[170:171], v[168:169] op_sel_hi:[1,0,1]
	ds_read_b128 v[168:171], v190 offset:50272
	s_waitcnt lgkmcnt(0)
	v_pk_fma_f32 v[172:173], v[134:135], v[168:169], v[172:173] op_sel_hi:[1,0,1]
	s_nop 0
	v_pk_fma_f32 v[168:169], v[110:111], v[168:169], v[172:173] op_sel:[0,1,0]
	s_nop 0
	v_pk_fma_f32 v[168:169], v[136:137], v[170:171], v[168:169] op_sel_hi:[1,0,1]
	v_mov_b32_e32 v170, v171
	v_pk_fma_f32 v[172:173], v[108:109], v[170:171], v[168:169] op_sel_hi:[1,0,1]
	ds_read_b128 v[168:171], v190 offset:51296
	s_waitcnt lgkmcnt(0)
	v_pk_fma_f32 v[172:173], v[138:139], v[168:169], v[172:173] op_sel_hi:[1,0,1]
	s_nop 0
	v_pk_fma_f32 v[168:169], v[114:115], v[168:169], v[172:173] op_sel:[0,1,0]
	s_nop 0
	v_pk_fma_f32 v[168:169], v[140:141], v[170:171], v[168:169] op_sel_hi:[1,0,1]
	v_mov_b32_e32 v170, v171
	v_pk_fma_f32 v[172:173], v[112:113], v[170:171], v[168:169] op_sel_hi:[1,0,1]
	ds_read_b128 v[168:171], v190 offset:52320
	s_waitcnt lgkmcnt(0)
	v_pk_fma_f32 v[172:173], v[142:143], v[168:169], v[172:173] op_sel_hi:[1,0,1]
	s_nop 0
	v_pk_fma_f32 v[168:169], v[118:119], v[168:169], v[172:173] op_sel:[0,1,0]
	s_nop 0
	v_pk_fma_f32 v[168:169], v[144:145], v[170:171], v[168:169] op_sel_hi:[1,0,1]
	v_mov_b32_e32 v170, v171
	v_pk_fma_f32 v[172:173], v[116:117], v[170:171], v[168:169] op_sel_hi:[1,0,1]
	ds_read_b128 v[168:171], v190 offset:53344
	s_waitcnt lgkmcnt(0)
	v_pk_fma_f32 v[172:173], v[146:147], v[168:169], v[172:173] op_sel_hi:[1,0,1]
	s_nop 0
	v_pk_fma_f32 v[168:169], v[122:123], v[168:169], v[172:173] op_sel:[0,1,0]
	s_nop 0
	v_pk_fma_f32 v[168:169], v[148:149], v[170:171], v[168:169] op_sel_hi:[1,0,1]
	v_mov_b32_e32 v170, v171
	v_pk_fma_f32 v[172:173], v[120:121], v[170:171], v[168:169] op_sel_hi:[1,0,1]
	ds_read_b128 v[168:171], v190 offset:54368
	s_waitcnt lgkmcnt(0)
	v_pk_fma_f32 v[172:173], v[150:151], v[168:169], v[172:173] op_sel_hi:[1,0,1]
	s_nop 0
	v_pk_fma_f32 v[168:169], v[126:127], v[168:169], v[172:173] op_sel:[0,1,0]
	s_nop 0
	v_pk_fma_f32 v[168:169], v[152:153], v[170:171], v[168:169] op_sel_hi:[1,0,1]
	v_mov_b32_e32 v170, v171
	v_pk_fma_f32 v[172:173], v[124:125], v[170:171], v[168:169] op_sel_hi:[1,0,1]
	ds_read_b128 v[168:171], v190 offset:55392
	s_waitcnt lgkmcnt(0)
	v_pk_fma_f32 v[172:173], v[154:155], v[168:169], v[172:173] op_sel_hi:[1,0,1]
	s_nop 0
	v_pk_fma_f32 v[168:169], v[130:131], v[168:169], v[172:173] op_sel:[0,1,0]
	s_nop 0
	v_pk_fma_f32 v[168:169], v[156:157], v[170:171], v[168:169] op_sel_hi:[1,0,1]
	v_mov_b32_e32 v170, v171
	v_pk_fma_f32 v[172:173], v[128:129], v[170:171], v[168:169] op_sel_hi:[1,0,1]
	ds_read_b128 v[168:171], v190 offset:56416
	s_waitcnt lgkmcnt(0)
	v_pk_fma_f32 v[172:173], v[158:159], v[168:169], v[172:173] op_sel_hi:[1,0,1]
	s_nop 0
	v_pk_fma_f32 v[168:169], v[6:7], v[168:169], v[172:173] op_sel:[0,1,0]
	s_nop 0
	v_pk_fma_f32 v[168:169], v[160:161], v[170:171], v[168:169] op_sel_hi:[1,0,1]
	v_mov_b32_e32 v170, v171
	v_pk_fma_f32 v[168:169], v[4:5], v[170:171], v[168:169] op_sel_hi:[1,0,1]
	s_nop 0
	ds_read_b128 v[170:173], v190 offset:57456
	s_waitcnt lgkmcnt(0)
	v_pk_fma_f32 v[174:175], v[12:13], v[170:171], 0 op_sel_hi:[1,0,0]
	s_nop 0
	v_pk_fma_f32 v[170:171], v[106:107], v[170:171], v[174:175] op_sel:[0,1,0]
	s_nop 0
	v_pk_fma_f32 v[170:171], v[132:133], v[172:173], v[170:171] op_sel_hi:[1,0,1]
	v_mov_b32_e32 v172, v173
	v_pk_fma_f32 v[174:175], v[104:105], v[172:173], v[170:171] op_sel_hi:[1,0,1]
	ds_read_b128 v[170:173], v190 offset:58480
	s_waitcnt lgkmcnt(0)
	v_pk_fma_f32 v[174:175], v[134:135], v[170:171], v[174:175] op_sel_hi:[1,0,1]
	s_nop 0
	v_pk_fma_f32 v[170:171], v[110:111], v[170:171], v[174:175] op_sel:[0,1,0]
	s_nop 0
	v_pk_fma_f32 v[170:171], v[136:137], v[172:173], v[170:171] op_sel_hi:[1,0,1]
	v_mov_b32_e32 v172, v173
	v_pk_fma_f32 v[174:175], v[108:109], v[172:173], v[170:171] op_sel_hi:[1,0,1]
	ds_read_b128 v[170:173], v190 offset:59504
	s_waitcnt lgkmcnt(0)
	v_pk_fma_f32 v[174:175], v[138:139], v[170:171], v[174:175] op_sel_hi:[1,0,1]
	s_nop 0
	v_pk_fma_f32 v[170:171], v[114:115], v[170:171], v[174:175] op_sel:[0,1,0]
	s_nop 0
	v_pk_fma_f32 v[170:171], v[140:141], v[172:173], v[170:171] op_sel_hi:[1,0,1]
	v_mov_b32_e32 v172, v173
	v_pk_fma_f32 v[174:175], v[112:113], v[172:173], v[170:171] op_sel_hi:[1,0,1]
	ds_read_b128 v[170:173], v190 offset:60528
	s_waitcnt lgkmcnt(0)
	v_pk_fma_f32 v[174:175], v[142:143], v[170:171], v[174:175] op_sel_hi:[1,0,1]
	s_nop 0
	v_pk_fma_f32 v[170:171], v[118:119], v[170:171], v[174:175] op_sel:[0,1,0]
	s_nop 0
	v_pk_fma_f32 v[170:171], v[144:145], v[172:173], v[170:171] op_sel_hi:[1,0,1]
	v_mov_b32_e32 v172, v173
	v_pk_fma_f32 v[174:175], v[116:117], v[172:173], v[170:171] op_sel_hi:[1,0,1]
	ds_read_b128 v[170:173], v190 offset:61552
	s_waitcnt lgkmcnt(0)
	v_pk_fma_f32 v[174:175], v[146:147], v[170:171], v[174:175] op_sel_hi:[1,0,1]
	s_nop 0
	v_pk_fma_f32 v[170:171], v[122:123], v[170:171], v[174:175] op_sel:[0,1,0]
	s_nop 0
	v_pk_fma_f32 v[170:171], v[148:149], v[172:173], v[170:171] op_sel_hi:[1,0,1]
	v_mov_b32_e32 v172, v173
	v_pk_fma_f32 v[174:175], v[120:121], v[172:173], v[170:171] op_sel_hi:[1,0,1]
	ds_read_b128 v[170:173], v190 offset:62576
	s_waitcnt lgkmcnt(0)
	v_pk_fma_f32 v[174:175], v[150:151], v[170:171], v[174:175] op_sel_hi:[1,0,1]
	s_nop 0
	v_pk_fma_f32 v[170:171], v[126:127], v[170:171], v[174:175] op_sel:[0,1,0]
	s_nop 0
	v_pk_fma_f32 v[170:171], v[152:153], v[172:173], v[170:171] op_sel_hi:[1,0,1]
	v_mov_b32_e32 v172, v173
	v_pk_fma_f32 v[174:175], v[124:125], v[172:173], v[170:171] op_sel_hi:[1,0,1]
	ds_read_b128 v[170:173], v190 offset:63600
	s_waitcnt lgkmcnt(0)
	v_pk_fma_f32 v[174:175], v[154:155], v[170:171], v[174:175] op_sel_hi:[1,0,1]
	s_nop 0
	v_pk_fma_f32 v[170:171], v[130:131], v[170:171], v[174:175] op_sel:[0,1,0]
	s_nop 0
	v_pk_fma_f32 v[170:171], v[156:157], v[172:173], v[170:171] op_sel_hi:[1,0,1]
	v_mov_b32_e32 v172, v173
	v_pk_fma_f32 v[174:175], v[128:129], v[172:173], v[170:171] op_sel_hi:[1,0,1]
	ds_read_b128 v[170:173], v190 offset:64624
	s_waitcnt lgkmcnt(0)
	v_pk_fma_f32 v[174:175], v[158:159], v[170:171], v[174:175] op_sel_hi:[1,0,1]
	s_nop 0
	v_pk_fma_f32 v[170:171], v[6:7], v[170:171], v[174:175] op_sel:[0,1,0]
	s_nop 0
	v_pk_fma_f32 v[170:171], v[160:161], v[172:173], v[170:171] op_sel_hi:[1,0,1]
	v_mov_b32_e32 v172, v173
	v_pk_fma_f32 v[170:171], v[4:5], v[172:173], v[170:171] op_sel_hi:[1,0,1]
	v_add_u32_e32 v172, 0x10080, v190
	ds_read_b128 v[172:175], v172
	s_waitcnt lgkmcnt(0)
	v_pk_fma_f32 v[176:177], v[12:13], v[172:173], 0 op_sel_hi:[1,0,0]
	s_nop 0
	v_pk_fma_f32 v[172:173], v[106:107], v[172:173], v[176:177] op_sel:[0,1,0]
	s_nop 0
	v_pk_fma_f32 v[172:173], v[132:133], v[174:175], v[172:173] op_sel_hi:[1,0,1]
	v_mov_b32_e32 v174, v175
	v_pk_fma_f32 v[176:177], v[104:105], v[174:175], v[172:173] op_sel_hi:[1,0,1]
	v_add_u32_e32 v172, 0x10480, v190
	ds_read_b128 v[172:175], v172
	s_waitcnt lgkmcnt(0)
	v_pk_fma_f32 v[176:177], v[134:135], v[172:173], v[176:177] op_sel_hi:[1,0,1]
	s_nop 0
	v_pk_fma_f32 v[172:173], v[110:111], v[172:173], v[176:177] op_sel:[0,1,0]
	s_nop 0
	v_pk_fma_f32 v[172:173], v[136:137], v[174:175], v[172:173] op_sel_hi:[1,0,1]
	v_mov_b32_e32 v174, v175
	v_pk_fma_f32 v[176:177], v[108:109], v[174:175], v[172:173] op_sel_hi:[1,0,1]
	v_add_u32_e32 v172, 0x10880, v190
	ds_read_b128 v[172:175], v172
	s_waitcnt lgkmcnt(0)
	v_pk_fma_f32 v[176:177], v[138:139], v[172:173], v[176:177] op_sel_hi:[1,0,1]
	s_nop 0
	v_pk_fma_f32 v[172:173], v[114:115], v[172:173], v[176:177] op_sel:[0,1,0]
	s_nop 0
	v_pk_fma_f32 v[172:173], v[140:141], v[174:175], v[172:173] op_sel_hi:[1,0,1]
	v_mov_b32_e32 v174, v175
	v_pk_fma_f32 v[176:177], v[112:113], v[174:175], v[172:173] op_sel_hi:[1,0,1]
	v_add_u32_e32 v172, 0x10c80, v190
	ds_read_b128 v[172:175], v172
	s_waitcnt lgkmcnt(0)
	v_pk_fma_f32 v[176:177], v[142:143], v[172:173], v[176:177] op_sel_hi:[1,0,1]
	s_nop 0
	v_pk_fma_f32 v[172:173], v[118:119], v[172:173], v[176:177] op_sel:[0,1,0]
	s_nop 0
	v_pk_fma_f32 v[172:173], v[144:145], v[174:175], v[172:173] op_sel_hi:[1,0,1]
	v_mov_b32_e32 v174, v175
	v_pk_fma_f32 v[176:177], v[116:117], v[174:175], v[172:173] op_sel_hi:[1,0,1]
	v_add_u32_e32 v172, 0x11080, v190
	ds_read_b128 v[172:175], v172
	s_waitcnt lgkmcnt(0)
	v_pk_fma_f32 v[176:177], v[146:147], v[172:173], v[176:177] op_sel_hi:[1,0,1]
	s_nop 0
	v_pk_fma_f32 v[172:173], v[122:123], v[172:173], v[176:177] op_sel:[0,1,0]
	s_nop 0
	v_pk_fma_f32 v[172:173], v[148:149], v[174:175], v[172:173] op_sel_hi:[1,0,1]
	v_mov_b32_e32 v174, v175
	v_pk_fma_f32 v[176:177], v[120:121], v[174:175], v[172:173] op_sel_hi:[1,0,1]
	v_add_u32_e32 v172, 0x11480, v190
	ds_read_b128 v[172:175], v172
	s_waitcnt lgkmcnt(0)
	v_pk_fma_f32 v[176:177], v[150:151], v[172:173], v[176:177] op_sel_hi:[1,0,1]
	s_nop 0
	v_pk_fma_f32 v[172:173], v[126:127], v[172:173], v[176:177] op_sel:[0,1,0]
	s_nop 0
	v_pk_fma_f32 v[172:173], v[152:153], v[174:175], v[172:173] op_sel_hi:[1,0,1]
	v_mov_b32_e32 v174, v175
	v_pk_fma_f32 v[176:177], v[124:125], v[174:175], v[172:173] op_sel_hi:[1,0,1]
	v_add_u32_e32 v172, 0x11880, v190
	ds_read_b128 v[172:175], v172
	s_waitcnt lgkmcnt(0)
	v_pk_fma_f32 v[176:177], v[154:155], v[172:173], v[176:177] op_sel_hi:[1,0,1]
	s_nop 0
	v_pk_fma_f32 v[172:173], v[130:131], v[172:173], v[176:177] op_sel:[0,1,0]
	s_nop 0
	v_pk_fma_f32 v[172:173], v[156:157], v[174:175], v[172:173] op_sel_hi:[1,0,1]
	v_mov_b32_e32 v174, v175
	v_pk_fma_f32 v[176:177], v[128:129], v[174:175], v[172:173] op_sel_hi:[1,0,1]
	v_add_u32_e32 v172, 0x11c80, v190
	ds_read_b128 v[172:175], v172
	s_waitcnt lgkmcnt(0)
	v_pk_fma_f32 v[176:177], v[158:159], v[172:173], v[176:177] op_sel_hi:[1,0,1]
	s_nop 0
	v_pk_fma_f32 v[172:173], v[6:7], v[172:173], v[176:177] op_sel:[0,1,0]
	s_nop 0
	v_pk_fma_f32 v[172:173], v[160:161], v[174:175], v[172:173] op_sel_hi:[1,0,1]
	v_mov_b32_e32 v174, v175
	v_pk_fma_f32 v[172:173], v[4:5], v[174:175], v[172:173] op_sel_hi:[1,0,1]
	v_add_u32_e32 v174, 0x12090, v190
	ds_read_b128 v[174:177], v174
	s_waitcnt lgkmcnt(0)
	v_pk_fma_f32 v[178:179], v[12:13], v[174:175], 0 op_sel_hi:[1,0,0]
	s_nop 0
	v_pk_fma_f32 v[174:175], v[106:107], v[174:175], v[178:179] op_sel:[0,1,0]
	s_nop 0
	v_pk_fma_f32 v[174:175], v[132:133], v[176:177], v[174:175] op_sel_hi:[1,0,1]
	v_mov_b32_e32 v176, v177
	v_pk_fma_f32 v[178:179], v[104:105], v[176:177], v[174:175] op_sel_hi:[1,0,1]
	v_add_u32_e32 v174, 0x12490, v190
	ds_read_b128 v[174:177], v174
	s_waitcnt lgkmcnt(0)
	v_pk_fma_f32 v[178:179], v[134:135], v[174:175], v[178:179] op_sel_hi:[1,0,1]
	s_nop 0
	v_pk_fma_f32 v[174:175], v[110:111], v[174:175], v[178:179] op_sel:[0,1,0]
	s_nop 0
	v_pk_fma_f32 v[174:175], v[136:137], v[176:177], v[174:175] op_sel_hi:[1,0,1]
	v_mov_b32_e32 v176, v177
	v_pk_fma_f32 v[178:179], v[108:109], v[176:177], v[174:175] op_sel_hi:[1,0,1]
	v_add_u32_e32 v174, 0x12890, v190
	ds_read_b128 v[174:177], v174
	s_waitcnt lgkmcnt(0)
	v_pk_fma_f32 v[178:179], v[138:139], v[174:175], v[178:179] op_sel_hi:[1,0,1]
	s_nop 0
	v_pk_fma_f32 v[174:175], v[114:115], v[174:175], v[178:179] op_sel:[0,1,0]
	s_nop 0
	v_pk_fma_f32 v[174:175], v[140:141], v[176:177], v[174:175] op_sel_hi:[1,0,1]
	v_mov_b32_e32 v176, v177
	v_pk_fma_f32 v[178:179], v[112:113], v[176:177], v[174:175] op_sel_hi:[1,0,1]
	v_add_u32_e32 v174, 0x12c90, v190
	ds_read_b128 v[174:177], v174
	s_waitcnt lgkmcnt(0)
	v_pk_fma_f32 v[178:179], v[142:143], v[174:175], v[178:179] op_sel_hi:[1,0,1]
	s_nop 0
	v_pk_fma_f32 v[174:175], v[118:119], v[174:175], v[178:179] op_sel:[0,1,0]
	s_nop 0
	v_pk_fma_f32 v[174:175], v[144:145], v[176:177], v[174:175] op_sel_hi:[1,0,1]
	v_mov_b32_e32 v176, v177
	v_pk_fma_f32 v[178:179], v[116:117], v[176:177], v[174:175] op_sel_hi:[1,0,1]
	v_add_u32_e32 v174, 0x13090, v190
	ds_read_b128 v[174:177], v174
	s_waitcnt lgkmcnt(0)
	v_pk_fma_f32 v[178:179], v[146:147], v[174:175], v[178:179] op_sel_hi:[1,0,1]
	s_nop 0
	v_pk_fma_f32 v[174:175], v[122:123], v[174:175], v[178:179] op_sel:[0,1,0]
	s_nop 0
	v_pk_fma_f32 v[174:175], v[148:149], v[176:177], v[174:175] op_sel_hi:[1,0,1]
	v_mov_b32_e32 v176, v177
	v_pk_fma_f32 v[178:179], v[120:121], v[176:177], v[174:175] op_sel_hi:[1,0,1]
	v_add_u32_e32 v174, 0x13490, v190
	ds_read_b128 v[174:177], v174
	s_waitcnt lgkmcnt(0)
	v_pk_fma_f32 v[178:179], v[150:151], v[174:175], v[178:179] op_sel_hi:[1,0,1]
	s_nop 0
	v_pk_fma_f32 v[174:175], v[126:127], v[174:175], v[178:179] op_sel:[0,1,0]
	s_nop 0
	v_pk_fma_f32 v[174:175], v[152:153], v[176:177], v[174:175] op_sel_hi:[1,0,1]
	v_mov_b32_e32 v176, v177
	v_pk_fma_f32 v[178:179], v[124:125], v[176:177], v[174:175] op_sel_hi:[1,0,1]
	v_add_u32_e32 v174, 0x13890, v190
	ds_read_b128 v[174:177], v174
	s_waitcnt lgkmcnt(0)
	v_pk_fma_f32 v[178:179], v[154:155], v[174:175], v[178:179] op_sel_hi:[1,0,1]
	s_nop 0
	v_pk_fma_f32 v[174:175], v[130:131], v[174:175], v[178:179] op_sel:[0,1,0]
	s_nop 0
	v_pk_fma_f32 v[174:175], v[156:157], v[176:177], v[174:175] op_sel_hi:[1,0,1]
	v_mov_b32_e32 v176, v177
	v_pk_fma_f32 v[178:179], v[128:129], v[176:177], v[174:175] op_sel_hi:[1,0,1]
	v_add_u32_e32 v174, 0x13c90, v190
	ds_read_b128 v[174:177], v174
	s_waitcnt lgkmcnt(0)
	v_pk_fma_f32 v[178:179], v[158:159], v[174:175], v[178:179] op_sel_hi:[1,0,1]
	s_nop 0
	v_pk_fma_f32 v[174:175], v[6:7], v[174:175], v[178:179] op_sel:[0,1,0]
	s_nop 0
	v_pk_fma_f32 v[174:175], v[160:161], v[176:177], v[174:175] op_sel_hi:[1,0,1]
	v_mov_b32_e32 v176, v177
	v_pk_fma_f32 v[174:175], v[4:5], v[176:177], v[174:175] op_sel_hi:[1,0,1]
	v_add_u32_e32 v176, 0x140a0, v190
	ds_read_b128 v[176:179], v176
	s_waitcnt lgkmcnt(0)
	v_pk_fma_f32 v[180:181], v[12:13], v[176:177], 0 op_sel_hi:[1,0,0]
	s_nop 0
	v_pk_fma_f32 v[176:177], v[106:107], v[176:177], v[180:181] op_sel:[0,1,0]
	s_nop 0
	v_pk_fma_f32 v[176:177], v[132:133], v[178:179], v[176:177] op_sel_hi:[1,0,1]
	v_mov_b32_e32 v178, v179
	v_pk_fma_f32 v[180:181], v[104:105], v[178:179], v[176:177] op_sel_hi:[1,0,1]
	v_add_u32_e32 v176, 0x144a0, v190
	ds_read_b128 v[176:179], v176
	s_waitcnt lgkmcnt(0)
	v_pk_fma_f32 v[180:181], v[134:135], v[176:177], v[180:181] op_sel_hi:[1,0,1]
	s_nop 0
	v_pk_fma_f32 v[176:177], v[110:111], v[176:177], v[180:181] op_sel:[0,1,0]
	s_nop 0
	v_pk_fma_f32 v[176:177], v[136:137], v[178:179], v[176:177] op_sel_hi:[1,0,1]
	v_mov_b32_e32 v178, v179
	v_pk_fma_f32 v[180:181], v[108:109], v[178:179], v[176:177] op_sel_hi:[1,0,1]
	v_add_u32_e32 v176, 0x148a0, v190
	ds_read_b128 v[176:179], v176
	s_waitcnt lgkmcnt(0)
	v_pk_fma_f32 v[180:181], v[138:139], v[176:177], v[180:181] op_sel_hi:[1,0,1]
	s_nop 0
	v_pk_fma_f32 v[176:177], v[114:115], v[176:177], v[180:181] op_sel:[0,1,0]
	s_nop 0
	v_pk_fma_f32 v[176:177], v[140:141], v[178:179], v[176:177] op_sel_hi:[1,0,1]
	v_mov_b32_e32 v178, v179
	v_pk_fma_f32 v[180:181], v[112:113], v[178:179], v[176:177] op_sel_hi:[1,0,1]
	v_add_u32_e32 v176, 0x14ca0, v190
	ds_read_b128 v[176:179], v176
	s_waitcnt lgkmcnt(0)
	v_pk_fma_f32 v[180:181], v[142:143], v[176:177], v[180:181] op_sel_hi:[1,0,1]
	s_nop 0
	v_pk_fma_f32 v[176:177], v[118:119], v[176:177], v[180:181] op_sel:[0,1,0]
	s_nop 0
	v_pk_fma_f32 v[176:177], v[144:145], v[178:179], v[176:177] op_sel_hi:[1,0,1]
	v_mov_b32_e32 v178, v179
	v_pk_fma_f32 v[180:181], v[116:117], v[178:179], v[176:177] op_sel_hi:[1,0,1]
	v_add_u32_e32 v176, 0x150a0, v190
	ds_read_b128 v[176:179], v176
	s_waitcnt lgkmcnt(0)
	v_pk_fma_f32 v[180:181], v[146:147], v[176:177], v[180:181] op_sel_hi:[1,0,1]
	s_nop 0
	v_pk_fma_f32 v[176:177], v[122:123], v[176:177], v[180:181] op_sel:[0,1,0]
	s_nop 0
	v_pk_fma_f32 v[176:177], v[148:149], v[178:179], v[176:177] op_sel_hi:[1,0,1]
	v_mov_b32_e32 v178, v179
	v_pk_fma_f32 v[180:181], v[120:121], v[178:179], v[176:177] op_sel_hi:[1,0,1]
	v_add_u32_e32 v176, 0x154a0, v190
	ds_read_b128 v[176:179], v176
	s_waitcnt lgkmcnt(0)
	v_pk_fma_f32 v[180:181], v[150:151], v[176:177], v[180:181] op_sel_hi:[1,0,1]
	s_nop 0
	v_pk_fma_f32 v[176:177], v[126:127], v[176:177], v[180:181] op_sel:[0,1,0]
	s_nop 0
	v_pk_fma_f32 v[176:177], v[152:153], v[178:179], v[176:177] op_sel_hi:[1,0,1]
	v_mov_b32_e32 v178, v179
	v_pk_fma_f32 v[180:181], v[124:125], v[178:179], v[176:177] op_sel_hi:[1,0,1]
	v_add_u32_e32 v176, 0x158a0, v190
	ds_read_b128 v[176:179], v176
	s_waitcnt lgkmcnt(0)
	v_pk_fma_f32 v[180:181], v[154:155], v[176:177], v[180:181] op_sel_hi:[1,0,1]
	s_nop 0
	v_pk_fma_f32 v[176:177], v[130:131], v[176:177], v[180:181] op_sel:[0,1,0]
	s_nop 0
	v_pk_fma_f32 v[176:177], v[156:157], v[178:179], v[176:177] op_sel_hi:[1,0,1]
	v_mov_b32_e32 v178, v179
	v_pk_fma_f32 v[180:181], v[128:129], v[178:179], v[176:177] op_sel_hi:[1,0,1]
	ds_read_b128 v[176:179], v199 offset:23712
	s_waitcnt lgkmcnt(0)
	v_pk_fma_f32 v[180:181], v[158:159], v[176:177], v[180:181] op_sel_hi:[1,0,1]
	s_nop 0
	v_pk_fma_f32 v[176:177], v[6:7], v[176:177], v[180:181] op_sel:[0,1,0]
	s_nop 0
	v_pk_fma_f32 v[176:177], v[160:161], v[178:179], v[176:177] op_sel_hi:[1,0,1]
	v_mov_b32_e32 v178, v179
	v_pk_fma_f32 v[176:177], v[4:5], v[178:179], v[176:177] op_sel_hi:[1,0,1]
	s_nop 0
	ds_read_b128 v[178:181], v199 offset:24752
	s_waitcnt lgkmcnt(0)
	v_pk_fma_f32 v[182:183], v[12:13], v[178:179], 0 op_sel_hi:[1,0,0]
	s_nop 0
	v_pk_fma_f32 v[178:179], v[106:107], v[178:179], v[182:183] op_sel:[0,1,0]
	s_nop 0
	v_pk_fma_f32 v[178:179], v[132:133], v[180:181], v[178:179] op_sel_hi:[1,0,1]
	v_mov_b32_e32 v180, v181
	v_pk_fma_f32 v[182:183], v[104:105], v[180:181], v[178:179] op_sel_hi:[1,0,1]
	ds_read_b128 v[178:181], v199 offset:25776
	s_waitcnt lgkmcnt(0)
	v_pk_fma_f32 v[182:183], v[134:135], v[178:179], v[182:183] op_sel_hi:[1,0,1]
	s_nop 0
	v_pk_fma_f32 v[178:179], v[110:111], v[178:179], v[182:183] op_sel:[0,1,0]
	s_nop 0
	v_pk_fma_f32 v[178:179], v[136:137], v[180:181], v[178:179] op_sel_hi:[1,0,1]
	v_mov_b32_e32 v180, v181
	v_pk_fma_f32 v[182:183], v[108:109], v[180:181], v[178:179] op_sel_hi:[1,0,1]
	ds_read_b128 v[178:181], v199 offset:26800
	s_waitcnt lgkmcnt(0)
	v_pk_fma_f32 v[182:183], v[138:139], v[178:179], v[182:183] op_sel_hi:[1,0,1]
	s_nop 0
	v_pk_fma_f32 v[178:179], v[114:115], v[178:179], v[182:183] op_sel:[0,1,0]
	s_nop 0
	v_pk_fma_f32 v[178:179], v[140:141], v[180:181], v[178:179] op_sel_hi:[1,0,1]
	v_mov_b32_e32 v180, v181
	v_pk_fma_f32 v[182:183], v[112:113], v[180:181], v[178:179] op_sel_hi:[1,0,1]
	ds_read_b128 v[178:181], v199 offset:27824
	s_waitcnt lgkmcnt(0)
	v_pk_fma_f32 v[182:183], v[142:143], v[178:179], v[182:183] op_sel_hi:[1,0,1]
	s_nop 0
	v_pk_fma_f32 v[178:179], v[118:119], v[178:179], v[182:183] op_sel:[0,1,0]
	s_nop 0
	v_pk_fma_f32 v[178:179], v[144:145], v[180:181], v[178:179] op_sel_hi:[1,0,1]
	v_mov_b32_e32 v180, v181
	v_pk_fma_f32 v[182:183], v[116:117], v[180:181], v[178:179] op_sel_hi:[1,0,1]
	ds_read_b128 v[178:181], v199 offset:28848
	s_waitcnt lgkmcnt(0)
	v_pk_fma_f32 v[182:183], v[146:147], v[178:179], v[182:183] op_sel_hi:[1,0,1]
	s_nop 0
	v_pk_fma_f32 v[178:179], v[122:123], v[178:179], v[182:183] op_sel:[0,1,0]
	s_nop 0
	v_pk_fma_f32 v[178:179], v[148:149], v[180:181], v[178:179] op_sel_hi:[1,0,1]
	v_mov_b32_e32 v180, v181
	v_pk_fma_f32 v[182:183], v[120:121], v[180:181], v[178:179] op_sel_hi:[1,0,1]
	ds_read_b128 v[178:181], v199 offset:29872
	s_waitcnt lgkmcnt(0)
	v_pk_fma_f32 v[182:183], v[150:151], v[178:179], v[182:183] op_sel_hi:[1,0,1]
	s_nop 0
	v_pk_fma_f32 v[178:179], v[126:127], v[178:179], v[182:183] op_sel:[0,1,0]
	s_nop 0
	v_pk_fma_f32 v[178:179], v[152:153], v[180:181], v[178:179] op_sel_hi:[1,0,1]
	v_mov_b32_e32 v180, v181
	v_pk_fma_f32 v[182:183], v[124:125], v[180:181], v[178:179] op_sel_hi:[1,0,1]
	ds_read_b128 v[178:181], v199 offset:30896
	s_waitcnt lgkmcnt(0)
	v_pk_fma_f32 v[182:183], v[154:155], v[178:179], v[182:183] op_sel_hi:[1,0,1]
	s_nop 0
	v_pk_fma_f32 v[178:179], v[130:131], v[178:179], v[182:183] op_sel:[0,1,0]
	s_nop 0
	v_pk_fma_f32 v[178:179], v[156:157], v[180:181], v[178:179] op_sel_hi:[1,0,1]
	v_mov_b32_e32 v180, v181
	v_pk_fma_f32 v[182:183], v[128:129], v[180:181], v[178:179] op_sel_hi:[1,0,1]
	ds_read_b128 v[178:181], v199 offset:31920
	s_waitcnt lgkmcnt(0)
	v_pk_fma_f32 v[182:183], v[158:159], v[178:179], v[182:183] op_sel_hi:[1,0,1]
	s_nop 0
	v_pk_fma_f32 v[178:179], v[6:7], v[178:179], v[182:183] op_sel:[0,1,0]
	s_nop 0
	v_pk_fma_f32 v[178:179], v[160:161], v[180:181], v[178:179] op_sel_hi:[1,0,1]
	v_mov_b32_e32 v180, v181
	v_pk_fma_f32 v[178:179], v[4:5], v[180:181], v[178:179] op_sel_hi:[1,0,1]
	s_nop 0
	ds_read_b128 v[180:183], v199 offset:32960
	s_waitcnt lgkmcnt(0)
	v_pk_fma_f32 v[184:185], v[12:13], v[180:181], 0 op_sel_hi:[1,0,0]
	s_nop 0
	v_pk_fma_f32 v[180:181], v[106:107], v[180:181], v[184:185] op_sel:[0,1,0]
	s_nop 0
	v_pk_fma_f32 v[180:181], v[132:133], v[182:183], v[180:181] op_sel_hi:[1,0,1]
	v_mov_b32_e32 v182, v183
	v_pk_fma_f32 v[184:185], v[104:105], v[182:183], v[180:181] op_sel_hi:[1,0,1]
	ds_read_b128 v[180:183], v199 offset:33984
	s_waitcnt lgkmcnt(0)
	v_pk_fma_f32 v[184:185], v[134:135], v[180:181], v[184:185] op_sel_hi:[1,0,1]
	s_nop 0
	v_pk_fma_f32 v[180:181], v[110:111], v[180:181], v[184:185] op_sel:[0,1,0]
	s_nop 0
	v_pk_fma_f32 v[180:181], v[136:137], v[182:183], v[180:181] op_sel_hi:[1,0,1]
	v_mov_b32_e32 v182, v183
	v_pk_fma_f32 v[184:185], v[108:109], v[182:183], v[180:181] op_sel_hi:[1,0,1]
	ds_read_b128 v[180:183], v199 offset:35008
	s_waitcnt lgkmcnt(0)
	v_pk_fma_f32 v[184:185], v[138:139], v[180:181], v[184:185] op_sel_hi:[1,0,1]
	s_nop 0
	v_pk_fma_f32 v[180:181], v[114:115], v[180:181], v[184:185] op_sel:[0,1,0]
	s_nop 0
	v_pk_fma_f32 v[180:181], v[140:141], v[182:183], v[180:181] op_sel_hi:[1,0,1]
	v_mov_b32_e32 v182, v183
	v_pk_fma_f32 v[184:185], v[112:113], v[182:183], v[180:181] op_sel_hi:[1,0,1]
	ds_read_b128 v[180:183], v199 offset:36032
	s_waitcnt lgkmcnt(0)
	v_pk_fma_f32 v[184:185], v[142:143], v[180:181], v[184:185] op_sel_hi:[1,0,1]
	s_nop 0
	v_pk_fma_f32 v[180:181], v[118:119], v[180:181], v[184:185] op_sel:[0,1,0]
	s_nop 0
	v_pk_fma_f32 v[180:181], v[144:145], v[182:183], v[180:181] op_sel_hi:[1,0,1]
	v_mov_b32_e32 v182, v183
	v_pk_fma_f32 v[184:185], v[116:117], v[182:183], v[180:181] op_sel_hi:[1,0,1]
	ds_read_b128 v[180:183], v199 offset:37056
	s_waitcnt lgkmcnt(0)
	v_pk_fma_f32 v[184:185], v[146:147], v[180:181], v[184:185] op_sel_hi:[1,0,1]
	s_nop 0
	v_pk_fma_f32 v[180:181], v[122:123], v[180:181], v[184:185] op_sel:[0,1,0]
	s_nop 0
	v_pk_fma_f32 v[180:181], v[148:149], v[182:183], v[180:181] op_sel_hi:[1,0,1]
	v_mov_b32_e32 v182, v183
	v_pk_fma_f32 v[184:185], v[120:121], v[182:183], v[180:181] op_sel_hi:[1,0,1]
	ds_read_b128 v[180:183], v199 offset:38080
	s_waitcnt lgkmcnt(0)
	v_pk_fma_f32 v[184:185], v[150:151], v[180:181], v[184:185] op_sel_hi:[1,0,1]
	s_nop 0
	v_pk_fma_f32 v[180:181], v[126:127], v[180:181], v[184:185] op_sel:[0,1,0]
	s_nop 0
	v_pk_fma_f32 v[180:181], v[152:153], v[182:183], v[180:181] op_sel_hi:[1,0,1]
	v_mov_b32_e32 v182, v183
	v_pk_fma_f32 v[184:185], v[124:125], v[182:183], v[180:181] op_sel_hi:[1,0,1]
	ds_read_b128 v[180:183], v199 offset:39104
	s_waitcnt lgkmcnt(0)
	v_pk_fma_f32 v[184:185], v[154:155], v[180:181], v[184:185] op_sel_hi:[1,0,1]
	s_nop 0
	v_pk_fma_f32 v[180:181], v[130:131], v[180:181], v[184:185] op_sel:[0,1,0]
	s_nop 0
	v_pk_fma_f32 v[180:181], v[156:157], v[182:183], v[180:181] op_sel_hi:[1,0,1]
	v_mov_b32_e32 v182, v183
	v_pk_fma_f32 v[184:185], v[128:129], v[182:183], v[180:181] op_sel_hi:[1,0,1]
	ds_read_b128 v[180:183], v199 offset:40128
	s_waitcnt lgkmcnt(0)
	v_pk_fma_f32 v[184:185], v[158:159], v[180:181], v[184:185] op_sel_hi:[1,0,1]
	s_nop 0
	v_pk_fma_f32 v[180:181], v[6:7], v[180:181], v[184:185] op_sel:[0,1,0]
	s_nop 0
	v_pk_fma_f32 v[180:181], v[160:161], v[182:183], v[180:181] op_sel_hi:[1,0,1]
	v_mov_b32_e32 v182, v183
	v_pk_fma_f32 v[180:181], v[4:5], v[182:183], v[180:181] op_sel_hi:[1,0,1]
	s_nop 0
	ds_read_b128 v[182:185], v199 offset:41168
	s_waitcnt lgkmcnt(0)
	v_pk_fma_f32 v[250:251], v[12:13], v[182:183], 0 op_sel_hi:[1,0,0]
	s_nop 0
	v_pk_fma_f32 v[182:183], v[106:107], v[182:183], v[250:251] op_sel:[0,1,0]
	s_nop 0
	v_pk_fma_f32 v[182:183], v[132:133], v[184:185], v[182:183] op_sel_hi:[1,0,1]
	v_mov_b32_e32 v184, v185
	v_pk_fma_f32 v[250:251], v[104:105], v[184:185], v[182:183] op_sel_hi:[1,0,1]
	ds_read_b128 v[182:185], v199 offset:42192
	s_waitcnt lgkmcnt(0)
	v_pk_fma_f32 v[250:251], v[134:135], v[182:183], v[250:251] op_sel_hi:[1,0,1]
	s_nop 0
	v_pk_fma_f32 v[182:183], v[110:111], v[182:183], v[250:251] op_sel:[0,1,0]
	s_nop 0
	v_pk_fma_f32 v[182:183], v[136:137], v[184:185], v[182:183] op_sel_hi:[1,0,1]
	v_mov_b32_e32 v184, v185
	v_pk_fma_f32 v[250:251], v[108:109], v[184:185], v[182:183] op_sel_hi:[1,0,1]
	ds_read_b128 v[182:185], v199 offset:43216
	s_waitcnt lgkmcnt(0)
	v_pk_fma_f32 v[250:251], v[138:139], v[182:183], v[250:251] op_sel_hi:[1,0,1]
	s_nop 0
	v_pk_fma_f32 v[182:183], v[114:115], v[182:183], v[250:251] op_sel:[0,1,0]
	s_nop 0
	v_pk_fma_f32 v[182:183], v[140:141], v[184:185], v[182:183] op_sel_hi:[1,0,1]
	v_mov_b32_e32 v184, v185
	v_pk_fma_f32 v[250:251], v[112:113], v[184:185], v[182:183] op_sel_hi:[1,0,1]
	ds_read_b128 v[182:185], v199 offset:44240
	s_waitcnt lgkmcnt(0)
	v_pk_fma_f32 v[250:251], v[142:143], v[182:183], v[250:251] op_sel_hi:[1,0,1]
	s_nop 0
	v_pk_fma_f32 v[182:183], v[118:119], v[182:183], v[250:251] op_sel:[0,1,0]
	s_nop 0
	v_pk_fma_f32 v[182:183], v[144:145], v[184:185], v[182:183] op_sel_hi:[1,0,1]
	v_mov_b32_e32 v184, v185
	v_pk_fma_f32 v[250:251], v[116:117], v[184:185], v[182:183] op_sel_hi:[1,0,1]
	ds_read_b128 v[182:185], v199 offset:45264
	s_waitcnt lgkmcnt(0)
	v_pk_fma_f32 v[250:251], v[146:147], v[182:183], v[250:251] op_sel_hi:[1,0,1]
	s_nop 0
	v_pk_fma_f32 v[182:183], v[122:123], v[182:183], v[250:251] op_sel:[0,1,0]
	s_nop 0
	v_pk_fma_f32 v[182:183], v[148:149], v[184:185], v[182:183] op_sel_hi:[1,0,1]
	v_mov_b32_e32 v184, v185
	v_pk_fma_f32 v[250:251], v[120:121], v[184:185], v[182:183] op_sel_hi:[1,0,1]
	ds_read_b128 v[182:185], v199 offset:46288
	s_waitcnt lgkmcnt(0)
	v_pk_fma_f32 v[250:251], v[150:151], v[182:183], v[250:251] op_sel_hi:[1,0,1]
	s_nop 0
	v_pk_fma_f32 v[182:183], v[126:127], v[182:183], v[250:251] op_sel:[0,1,0]
	s_nop 0
	v_pk_fma_f32 v[182:183], v[152:153], v[184:185], v[182:183] op_sel_hi:[1,0,1]
	v_mov_b32_e32 v184, v185
	v_pk_fma_f32 v[250:251], v[124:125], v[184:185], v[182:183] op_sel_hi:[1,0,1]
	ds_read_b128 v[182:185], v199 offset:47312
	s_waitcnt lgkmcnt(0)
	v_pk_fma_f32 v[250:251], v[154:155], v[182:183], v[250:251] op_sel_hi:[1,0,1]
	s_nop 0
	v_pk_fma_f32 v[182:183], v[130:131], v[182:183], v[250:251] op_sel:[0,1,0]
	s_nop 0
	v_pk_fma_f32 v[182:183], v[156:157], v[184:185], v[182:183] op_sel_hi:[1,0,1]
	v_mov_b32_e32 v184, v185
	v_pk_fma_f32 v[250:251], v[128:129], v[184:185], v[182:183] op_sel_hi:[1,0,1]
	ds_read_b128 v[182:185], v199 offset:48336
	s_waitcnt lgkmcnt(0)
	v_pk_fma_f32 v[250:251], v[158:159], v[182:183], v[250:251] op_sel_hi:[1,0,1]
	s_nop 0
	v_pk_fma_f32 v[182:183], v[6:7], v[182:183], v[250:251] op_sel:[0,1,0]
	s_nop 0
	v_pk_fma_f32 v[182:183], v[160:161], v[184:185], v[182:183] op_sel_hi:[1,0,1]
	v_mov_b32_e32 v184, v185
	v_pk_fma_f32 v[182:183], v[4:5], v[184:185], v[182:183] op_sel_hi:[1,0,1]
	s_nop 0
	ds_read_b128 v[250:253], v199 offset:49376
	s_waitcnt lgkmcnt(0)
	v_pk_fma_f32 v[184:185], v[12:13], v[250:251], 0 op_sel_hi:[1,0,0]
	s_nop 0
	v_pk_fma_f32 v[184:185], v[106:107], v[250:251], v[184:185] op_sel:[0,1,0]
	v_mov_b32_e32 v250, v253
	v_pk_fma_f32 v[184:185], v[132:133], v[252:253], v[184:185] op_sel_hi:[1,0,1]
	s_nop 0
	v_pk_fma_f32 v[184:185], v[104:105], v[250:251], v[184:185] op_sel_hi:[1,0,1]
	ds_read_b128 v[250:253], v199 offset:50400
	s_waitcnt lgkmcnt(0)
	v_pk_fma_f32 v[184:185], v[134:135], v[250:251], v[184:185] op_sel_hi:[1,0,1]
	s_nop 0
	v_pk_fma_f32 v[184:185], v[110:111], v[250:251], v[184:185] op_sel:[0,1,0]
	v_mov_b32_e32 v250, v253
	v_pk_fma_f32 v[184:185], v[136:137], v[252:253], v[184:185] op_sel_hi:[1,0,1]
	s_nop 0
	v_pk_fma_f32 v[184:185], v[108:109], v[250:251], v[184:185] op_sel_hi:[1,0,1]
	ds_read_b128 v[250:253], v199 offset:51424
	s_waitcnt lgkmcnt(0)
	v_pk_fma_f32 v[184:185], v[138:139], v[250:251], v[184:185] op_sel_hi:[1,0,1]
	s_nop 0
	v_pk_fma_f32 v[184:185], v[114:115], v[250:251], v[184:185] op_sel:[0,1,0]
	v_mov_b32_e32 v250, v253
	v_pk_fma_f32 v[184:185], v[140:141], v[252:253], v[184:185] op_sel_hi:[1,0,1]
	s_nop 0
	v_pk_fma_f32 v[184:185], v[112:113], v[250:251], v[184:185] op_sel_hi:[1,0,1]
	ds_read_b128 v[250:253], v199 offset:52448
	s_waitcnt lgkmcnt(0)
	v_pk_fma_f32 v[184:185], v[142:143], v[250:251], v[184:185] op_sel_hi:[1,0,1]
	s_nop 0
	v_pk_fma_f32 v[184:185], v[118:119], v[250:251], v[184:185] op_sel:[0,1,0]
	v_mov_b32_e32 v250, v253
	v_pk_fma_f32 v[184:185], v[144:145], v[252:253], v[184:185] op_sel_hi:[1,0,1]
	s_nop 0
	v_pk_fma_f32 v[184:185], v[116:117], v[250:251], v[184:185] op_sel_hi:[1,0,1]
	ds_read_b128 v[250:253], v199 offset:53472
	s_waitcnt lgkmcnt(0)
	v_pk_fma_f32 v[184:185], v[146:147], v[250:251], v[184:185] op_sel_hi:[1,0,1]
	s_nop 0
	v_pk_fma_f32 v[184:185], v[122:123], v[250:251], v[184:185] op_sel:[0,1,0]
	v_mov_b32_e32 v250, v253
	v_pk_fma_f32 v[184:185], v[148:149], v[252:253], v[184:185] op_sel_hi:[1,0,1]
	s_nop 0
	v_pk_fma_f32 v[184:185], v[120:121], v[250:251], v[184:185] op_sel_hi:[1,0,1]
	ds_read_b128 v[250:253], v199 offset:54496
	s_waitcnt lgkmcnt(0)
	v_pk_fma_f32 v[184:185], v[150:151], v[250:251], v[184:185] op_sel_hi:[1,0,1]
	s_nop 0
	v_pk_fma_f32 v[184:185], v[126:127], v[250:251], v[184:185] op_sel:[0,1,0]
	v_mov_b32_e32 v250, v253
	v_pk_fma_f32 v[184:185], v[152:153], v[252:253], v[184:185] op_sel_hi:[1,0,1]
	s_nop 0
	v_pk_fma_f32 v[184:185], v[124:125], v[250:251], v[184:185] op_sel_hi:[1,0,1]
	ds_read_b128 v[250:253], v199 offset:55520
	s_waitcnt lgkmcnt(0)
	v_pk_fma_f32 v[184:185], v[154:155], v[250:251], v[184:185] op_sel_hi:[1,0,1]
	s_nop 0
	v_pk_fma_f32 v[184:185], v[130:131], v[250:251], v[184:185] op_sel:[0,1,0]
	v_mov_b32_e32 v250, v253
	v_pk_fma_f32 v[184:185], v[156:157], v[252:253], v[184:185] op_sel_hi:[1,0,1]
	s_nop 0
	v_pk_fma_f32 v[184:185], v[128:129], v[250:251], v[184:185] op_sel_hi:[1,0,1]
	ds_read_b128 v[250:253], v199 offset:56544
	s_waitcnt lgkmcnt(0)
	v_pk_fma_f32 v[184:185], v[158:159], v[250:251], v[184:185] op_sel_hi:[1,0,1]
	s_nop 0
	v_pk_fma_f32 v[184:185], v[6:7], v[250:251], v[184:185] op_sel:[0,1,0]
	v_mov_b32_e32 v250, v253
	v_pk_fma_f32 v[184:185], v[160:161], v[252:253], v[184:185] op_sel_hi:[1,0,1]
	s_nop 0
	v_pk_fma_f32 v[184:185], v[4:5], v[250:251], v[184:185] op_sel_hi:[1,0,1]
	s_nop 0
	ds_read_b128 v[250:253], v199 offset:57584
	s_waitcnt lgkmcnt(0)
	v_pk_fma_f32 v[12:13], v[12:13], v[250:251], 0 op_sel_hi:[1,0,0]
	s_nop 0
	v_pk_fma_f32 v[12:13], v[106:107], v[250:251], v[12:13] op_sel:[0,1,0]
	v_mov_b32_e32 v106, v253
	v_pk_fma_f32 v[12:13], v[132:133], v[252:253], v[12:13] op_sel_hi:[1,0,1]
	s_nop 0
	v_pk_fma_f32 v[12:13], v[104:105], v[106:107], v[12:13] op_sel_hi:[1,0,1]
	ds_read_b128 v[104:107], v199 offset:58608
	s_waitcnt lgkmcnt(0)
	v_pk_fma_f32 v[12:13], v[134:135], v[104:105], v[12:13] op_sel_hi:[1,0,1]
	s_nop 0
	v_pk_fma_f32 v[12:13], v[110:111], v[104:105], v[12:13] op_sel:[0,1,0]
	v_mov_b32_e32 v104, v107
	v_pk_fma_f32 v[12:13], v[136:137], v[106:107], v[12:13] op_sel_hi:[1,0,1]
	s_nop 0
	v_pk_fma_f32 v[12:13], v[108:109], v[104:105], v[12:13] op_sel_hi:[1,0,1]
	ds_read_b128 v[104:107], v199 offset:59632
	s_waitcnt lgkmcnt(0)
	v_pk_fma_f32 v[12:13], v[138:139], v[104:105], v[12:13] op_sel_hi:[1,0,1]
	s_nop 0
	v_pk_fma_f32 v[12:13], v[114:115], v[104:105], v[12:13] op_sel:[0,1,0]
	v_mov_b32_e32 v104, v107
	v_pk_fma_f32 v[12:13], v[140:141], v[106:107], v[12:13] op_sel_hi:[1,0,1]
	s_nop 0
	v_pk_fma_f32 v[12:13], v[112:113], v[104:105], v[12:13] op_sel_hi:[1,0,1]
	ds_read_b128 v[104:107], v199 offset:60656
	s_waitcnt lgkmcnt(0)
	v_pk_fma_f32 v[12:13], v[142:143], v[104:105], v[12:13] op_sel_hi:[1,0,1]
	s_nop 0
	v_pk_fma_f32 v[12:13], v[118:119], v[104:105], v[12:13] op_sel:[0,1,0]
	v_mov_b32_e32 v104, v107
	v_pk_fma_f32 v[12:13], v[144:145], v[106:107], v[12:13] op_sel_hi:[1,0,1]
	s_nop 0
	v_pk_fma_f32 v[12:13], v[116:117], v[104:105], v[12:13] op_sel_hi:[1,0,1]
	ds_read_b128 v[104:107], v199 offset:61680
	s_waitcnt lgkmcnt(0)
	v_pk_fma_f32 v[12:13], v[146:147], v[104:105], v[12:13] op_sel_hi:[1,0,1]
	s_nop 0
	v_pk_fma_f32 v[12:13], v[122:123], v[104:105], v[12:13] op_sel:[0,1,0]
	v_mov_b32_e32 v104, v107
	v_pk_fma_f32 v[12:13], v[148:149], v[106:107], v[12:13] op_sel_hi:[1,0,1]
	s_nop 0
	v_pk_fma_f32 v[12:13], v[120:121], v[104:105], v[12:13] op_sel_hi:[1,0,1]
	ds_read_b128 v[104:107], v199 offset:62704
	s_waitcnt lgkmcnt(0)
	v_pk_fma_f32 v[12:13], v[150:151], v[104:105], v[12:13] op_sel_hi:[1,0,1]
	s_nop 0
	v_pk_fma_f32 v[12:13], v[126:127], v[104:105], v[12:13] op_sel:[0,1,0]
	v_mov_b32_e32 v104, v107
	v_pk_fma_f32 v[12:13], v[152:153], v[106:107], v[12:13] op_sel_hi:[1,0,1]
	s_nop 0
	v_pk_fma_f32 v[12:13], v[124:125], v[104:105], v[12:13] op_sel_hi:[1,0,1]
	ds_read_b128 v[104:107], v199 offset:63728
	s_waitcnt lgkmcnt(0)
	v_pk_fma_f32 v[12:13], v[154:155], v[104:105], v[12:13] op_sel_hi:[1,0,1]
	s_nop 0
	v_pk_fma_f32 v[12:13], v[130:131], v[104:105], v[12:13] op_sel:[0,1,0]
	v_mov_b32_e32 v104, v107
	v_pk_fma_f32 v[12:13], v[156:157], v[106:107], v[12:13] op_sel_hi:[1,0,1]
	s_nop 0
	v_pk_fma_f32 v[12:13], v[128:129], v[104:105], v[12:13] op_sel_hi:[1,0,1]
	ds_read_b128 v[104:107], v199 offset:64752
	s_waitcnt lgkmcnt(0)
	v_pk_fma_f32 v[12:13], v[158:159], v[104:105], v[12:13] op_sel_hi:[1,0,1]
	s_nop 0
	v_pk_fma_f32 v[6:7], v[6:7], v[104:105], v[12:13] op_sel:[0,1,0]
	v_mov_b32_e32 v12, v107
	v_pk_fma_f32 v[6:7], v[160:161], v[106:107], v[6:7] op_sel_hi:[1,0,1]
	v_cndmask_b32_e64 v104, v168, v184, s[6:7]
	v_pk_fma_f32 v[4:5], v[4:5], v[12:13], v[6:7] op_sel_hi:[1,0,1]
	v_cndmask_b32_e64 v6, v172, v2, s[6:7]
	v_cndmask_b32_e64 v2, v2, v172, s[6:7]
	ds_bpermute_b32 v2, v189, v2
	v_cndmask_b32_e64 v7, v8, v174, s[6:7]
	ds_bpermute_b32 v7, v189, v7
	v_cndmask_b32_e64 v12, v164, v180, s[6:7]
	ds_bpermute_b32 v12, v189, v12
	s_waitcnt lgkmcnt(2)
	v_add_f32_e32 v2, v6, v2
	v_cndmask_b32_e64 v6, v174, v8, s[6:7]
	v_cndmask_b32_e64 v8, v10, v176, s[6:7]
	s_waitcnt lgkmcnt(1)
	v_add_f32_e32 v6, v6, v7
	v_cndmask_b32_e64 v7, v176, v10, s[6:7]
	ds_bpermute_b32 v8, v189, v8
	v_cndmask_b32_e64 v10, v162, v178, s[6:7]
	ds_bpermute_b32 v10, v189, v10
	v_cndmask_b32_e64 v13, v166, v182, s[6:7]
	ds_bpermute_b32 v13, v189, v13
	ds_bpermute_b32 v104, v189, v104
	s_waitcnt lgkmcnt(3)
	v_add_f32_e32 v7, v7, v8
	v_cndmask_b32_e64 v8, v178, v162, s[6:7]
	s_waitcnt lgkmcnt(2)
	v_add_f32_e32 v8, v8, v10
	v_cndmask_b32_e64 v10, v180, v164, s[6:7]
	v_add_f32_e32 v10, v10, v12
	v_cndmask_b32_e64 v12, v182, v166, s[6:7]
	s_waitcnt lgkmcnt(1)
	v_add_f32_e32 v12, v12, v13
	v_cndmask_b32_e64 v13, v184, v168, s[6:7]
	s_waitcnt lgkmcnt(0)
	v_add_f32_e32 v13, v13, v104
	v_cndmask_b32_e64 v104, v4, v170, s[6:7]
	v_cndmask_b32_e64 v4, v170, v4, s[6:7]
	ds_bpermute_b32 v4, v189, v4
	s_load_dwordx2 s[14:15], s[0:1], 0xc0
	s_waitcnt lgkmcnt(0)
	v_add_f32_e32 v4, v104, v4
	v_cndmask_b32_e64 v104, v10, v2, s[8:9]
	v_cndmask_b32_e64 v2, v2, v10, s[8:9]
	v_cndmask_b32_e64 v10, v12, v6, s[8:9]
	v_cndmask_b32_e64 v6, v6, v12, s[8:9]
	ds_bpermute_b32 v6, v188, v6
	ds_bpermute_b32 v2, v188, v2
	s_waitcnt lgkmcnt(1)
	v_add_f32_e32 v6, v10, v6
	v_cndmask_b32_e64 v10, v13, v7, s[8:9]
	v_cndmask_b32_e64 v7, v7, v13, s[8:9]
	ds_bpermute_b32 v7, v188, v7
	s_waitcnt lgkmcnt(1)
	v_add_f32_e32 v2, v104, v2
	s_waitcnt lgkmcnt(0)
	v_add_f32_e32 v7, v10, v7
	v_cndmask_b32_e64 v10, v4, v8, s[8:9]
	v_cndmask_b32_e64 v4, v8, v4, s[8:9]
	ds_bpermute_b32 v4, v188, v4
	v_cndmask_b32_e64 v8, v7, v2, s[10:11]
	v_cndmask_b32_e64 v2, v2, v7, s[10:11]
	ds_bpermute_b32 v2, v187, v2
	s_waitcnt lgkmcnt(1)
	v_add_f32_e32 v4, v10, v4
	v_cndmask_b32_e64 v7, v4, v6, s[10:11]
	v_cndmask_b32_e64 v4, v6, v4, s[10:11]
	ds_bpermute_b32 v4, v187, v4
	s_waitcnt lgkmcnt(1)
	v_add_f32_e32 v2, v8, v2
	s_waitcnt lgkmcnt(0)
	v_add_f32_e32 v4, v7, v4
	v_cndmask_b32_e64 v6, v4, v2, s[12:13]
	v_cndmask_b32_e64 v2, v2, v4, s[12:13]
	ds_bpermute_b32 v2, v186, v2
	s_waitcnt lgkmcnt(0)
	v_add_f32_e32 v2, v6, v2
	ds_bpermute_b32 v4, v15, v2
	s_waitcnt lgkmcnt(0)
	v_add_f32_e32 v2, v2, v4
	ds_bpermute_b32 v4, v1, v2
	s_waitcnt lgkmcnt(0)
	v_add_f32_e32 v2, v2, v4
	v_mul_f32_e32 v2, 0xbfb8aa3b, v2
	v_exp_f32_e32 v2, v2
	s_nop 0
	v_add_f32_e32 v2, 1.0, v2
	v_div_scale_f32 v4, s[16:17], v2, v2, 1.0
	v_rcp_f32_e32 v6, v4
	s_nop 0
	v_fma_f32 v7, -v4, v6, 1.0
	v_fmac_f32_e32 v6, v7, v6
	v_div_scale_f32 v7, vcc, 1.0, v2, 1.0
	v_mul_f32_e32 v8, v7, v6
	v_fma_f32 v10, -v4, v8, v7
	v_fmac_f32_e32 v8, v10, v6
	v_fma_f32 v4, -v4, v8, v7
	v_div_fmas_f32 v4, v4, v6, v8
	v_div_fixup_f32 v4, v4, v2, 1.0
	global_load_dword v2, v16, s[14:15]
	v_lshl_add_u64 v[6:7], s[14:15], 0, v[16:17]
	s_waitcnt vmcnt(0)
	v_add_f32_e32 v2, v2, v4
	ds_bpermute_b32 v8, v191, v2
	ds_bpermute_b32 v10, v192, v2
	ds_bpermute_b32 v12, v193, v2
	ds_bpermute_b32 v13, v194, v2
	s_waitcnt lgkmcnt(2)
	v_add_f32_e32 v104, v8, v10
	s_waitcnt lgkmcnt(1)
	v_add_f32_e32 v105, v8, v12
	v_max_f32_e32 v104, v104, v105
	s_waitcnt lgkmcnt(0)
	v_add_f32_e32 v8, v8, v13
	v_add_f32_e32 v105, v10, v12
	v_add_f32_e32 v10, v10, v13
	v_add_f32_e32 v12, v12, v13
	v_max_f32_e32 v8, v8, v105
	v_max_f32_e32 v10, v10, v12
	v_max3_f32 v8, v104, v8, v10
	ds_bpermute_b32 v10, v195, v8
	ds_bpermute_b32 v12, v196, v8
	ds_bpermute_b32 v13, v197, v8
	ds_bpermute_b32 v8, v198, v8
	s_waitcnt lgkmcnt(2)
	v_cmp_gt_f32_e32 vcc, v12, v10
	s_nop 1
	v_cndmask_b32_e32 v10, v10, v12, vcc
	v_cndmask_b32_e64 v12, 0, 1, vcc
	s_waitcnt lgkmcnt(1)
	v_cmp_lt_f32_e32 vcc, v10, v13
	s_nop 1
	v_cndmask_b32_e32 v10, v10, v13, vcc
	v_cndmask_b32_e64 v12, v12, 2, vcc
	s_waitcnt lgkmcnt(0)
	v_cmp_nlt_f32_e32 vcc, v10, v8
	s_nop 1
	v_cndmask_b32_e32 v8, 3, v12, vcc
	v_lshl_or_b32 v10, v8, 6, v195
	ds_bpermute_b32 v108, v10, v2
	ds_bpermute_b32 v107, v10, v2 offset:16
	ds_bpermute_b32 v105, v10, v2 offset:32
	ds_bpermute_b32 v106, v10, v2 offset:48
	ds_bpermute_b32 v104, v10, v4
	ds_bpermute_b32 v2, v10, v4 offset:16
	s_waitcnt lgkmcnt(4)
	v_cmp_gt_f32_e32 vcc, v107, v108
	ds_bpermute_b32 v12, v10, v4 offset:32
	ds_bpermute_b32 v13, v10, v4 offset:48
	v_cndmask_b32_e32 v10, v108, v107, vcc
	v_cndmask_b32_e64 v4, 0, 1, vcc
	s_waitcnt lgkmcnt(5)
	v_cmp_lt_f32_e32 vcc, v10, v105
	s_nop 1
	v_cndmask_b32_e32 v10, v10, v105, vcc
	v_cndmask_b32_e64 v4, v4, 2, vcc
	s_waitcnt lgkmcnt(4)
	v_cmp_nlt_f32_e64 s[14:15], v10, v106
	s_and_b64 vcc, vcc, s[14:15]
	s_nop 0
	v_cndmask_b32_e64 v10, 3, v4, s[14:15]
	v_cmp_lt_i32_e64 s[16:17], 0, v10
	s_waitcnt lgkmcnt(3)
	v_mov_b32_e32 v4, v104
	s_and_saveexec_b64 s[18:19], s[16:17]
	s_cbranch_execz .LBB0_3209
	v_cmp_ne_u32_e64 s[16:17], 1, v10
	s_and_saveexec_b64 s[24:25], s[16:17]
	s_xor_b64 s[16:17], exec, s[24:25]
	s_cbranch_execz .LBB0_3206
	s_waitcnt lgkmcnt(0)
	v_cndmask_b32_e32 v4, v13, v12, vcc

	.amdhsa_kernel _Z6mk_fwd4Args
		.amdhsa_group_segment_fixed_size 0
		.amdhsa_private_segment_fixed_size 0
		.amdhsa_kernarg_size 504
		.amdhsa_user_sgpr_count 2
		.amdhsa_user_sgpr_dispatch_ptr 0
		.amdhsa_user_sgpr_queue_ptr 0
		.amdhsa_user_sgpr_kernarg_segment_ptr 1
		.amdhsa_user_sgpr_dispatch_id 0
		.amdhsa_user_sgpr_kernarg_preload_length 0
		.amdhsa_user_sgpr_kernarg_preload_offset 0
		.amdhsa_user_sgpr_private_segment_size 0
		.amdhsa_uses_dynamic_stack 0
		.amdhsa_enable_private_segment 0
		.amdhsa_system_sgpr_workgroup_id_x 1
		.amdhsa_system_sgpr_workgroup_id_y 0
		.amdhsa_system_sgpr_workgroup_id_z 0
		.amdhsa_system_sgpr_workgroup_info 0
		.amdhsa_system_vgpr_workitem_id 0
		.amdhsa_next_free_vgpr 256
		.amdhsa_next_free_sgpr 102
		.amdhsa_accum_offset 256
		.amdhsa_reserve_vcc 1
		.amdhsa_float_round_mode_32 0
		.amdhsa_float_round_mode_16_64 0
		.amdhsa_float_denorm_mode_32 3
		.amdhsa_float_denorm_mode_16_64 3
		.amdhsa_dx10_clamp 1
		.amdhsa_ieee_mode 1
		.amdhsa_fp16_overflow 0
		.amdhsa_tg_split 0
		.amdhsa_exception_fp_ieee_invalid_op 0
		.amdhsa_exception_fp_denorm_src 0
		.amdhsa_exception_fp_ieee_div_zero 0
		.amdhsa_exception_fp_ieee_overflow 0
		.amdhsa_exception_fp_ieee_underflow 0
		.amdhsa_exception_fp_ieee_inexact 0
		.amdhsa_exception_int_div_zero 0
	.end_amdhsa_kernel

amdhsa.kernels:
  - .agpr_count:     0
    .args:
      - .offset:         0
        .size:           248
        .value_kind:     by_value
      - .offset:         248
        .size:           4
        .value_kind:     hidden_block_count_x
      - .offset:         252
        .size:           4
        .value_kind:     hidden_block_count_y
      - .offset:         256
        .size:           4
        .value_kind:     hidden_block_count_z
      - .offset:         260
        .size:           2
        .value_kind:     hidden_group_size_x
      - .offset:         262
        .size:           2
        .value_kind:     hidden_group_size_y
      - .offset:         264
        .size:           2
        .value_kind:     hidden_group_size_z
      - .offset:         266
        .size:           2
        .value_kind:     hidden_remainder_x
      - .offset:         268
        .size:           2
        .value_kind:     hidden_remainder_y
      - .offset:         270
        .size:           2
        .value_kind:     hidden_remainder_z
      - .offset:         288
        .size:           8
        .value_kind:     hidden_global_offset_x
      - .offset:         296
        .size:           8
        .value_kind:     hidden_global_offset_y
      - .offset:         304
        .size:           8
        .value_kind:     hidden_global_offset_z
      - .offset:         312
        .size:           2
        .value_kind:     hidden_grid_dims
      - .offset:         368
        .size:           4
        .value_kind:     hidden_dynamic_lds_size
    .group_segment_fixed_size: 0
    .kernarg_segment_align: 8
    .kernarg_segment_size: 504
    .language:       OpenCL C
    .language_version:
      - 2
      - 0
    .max_flat_workgroup_size: 512
    .name:           _Z6mk_fwd4Args
    .private_segment_fixed_size: 0
    .sgpr_count:     108
    .sgpr_spill_count: 0
    .symbol:         _Z6mk_fwd4Args.kd
    .uniform_work_group_size: 1
    .uses_dynamic_stack: false
    .vgpr_count:     256
    .vgpr_spill_count: 0
    .wavefront_size: 64
